# barrier closing each 32-MFMA block issued before the block's last MFMA (hand-off latency overlaps the last MFMA; LDS ops keep their position relative to the barrier)
# speedup vs baseline: 1.0070x; 1.0012x over previous
.LBB0_575:
	s_add_i32 s28, s6, s77
	s_add_i32 s26, s28, 1
	s_cmp_ge_i32 s26, s52
	s_cselect_b32 s27, s52, 0
	s_sub_i32 s26, s26, s27
	s_ashr_i32 s27, s26, 31
	s_lshl_b64 s[78:79], s[26:27], s41
	s_add_i32 s28, s28, 2
	s_cmp_ge_i32 s28, s52
	s_cselect_b32 s26, s52, 0
	s_sub_i32 s26, s28, s26
	s_ashr_i32 s27, s26, 31
	s_lshl_b64 s[26:27], s[26:27], s41
	v_add_u32_e32 v148, s7, v155
	v_add_u32_e32 v152, s44, v155
	s_add_u32 s28, s22, s26
	ds_read_b128 v[136:139], v148
	ds_read_b128 v[140:143], v148 offset:1024
	ds_read_b128 v[144:147], v148 offset:2048
	ds_read_b128 v[148:151], v148 offset:3072
	ds_read_b128 v[158:161], v152
	ds_read_b128 v[172:175], v152 offset:1024
	ds_read_b128 v[176:179], v152 offset:2048
	ds_read_b128 v[180:183], v152 offset:3072
	s_addc_u32 s29, s23, s27
	s_add_u32 s26, s24, s26
	s_addc_u32 s27, s25, s27
	s_cmp_eq_u32 s53, s77
	s_cselect_b32 s30, s73, s28
	s_cselect_b32 s31, s74, s29
	s_cselect_b32 s29, s76, s27
	s_cselect_b32 s28, s75, s26
	s_add_u32 s26, s30, s54
	s_addc_u32 s27, s31, 0
	s_add_u32 s78, s71, s78
	s_addc_u32 s79, s72, s79
	s_add_i32 m0, s47, 0xc000
	ds_read_b128 v[184:187], v157
	ds_read_b128 v[188:191], v157 offset:1024
	ds_read_b128 v[192:195], v157 offset:2048
	ds_read_b128 v[196:199], v157 offset:3072
	ds_read_b128 v[212:215], v157 offset:4096
	ds_read_b128 v[216:219], v157 offset:5120
	ds_read_b128 v[220:223], v157 offset:6144
	ds_read_b128 v[224:227], v157 offset:7168
	global_load_lds_dwordx4 v130, s[78:79]
	s_add_i32 m0, s47, 0xe000
	s_nop 0
	global_load_lds_dwordx4 v132, s[78:79]
	s_waitcnt vmcnt(8)
	s_waitcnt lgkmcnt(0)
	s_barrier
	s_setprio 1
	s_waitcnt lgkmcnt(0)
	v_mfma_f32_16x16x32_bf16 v[126:129], v[136:139], v[184:187], v[126:129]
	v_mfma_f32_16x16x32_bf16 v[122:125], v[144:147], v[184:187], v[122:125]
	v_mfma_f32_16x16x32_bf16 v[110:113], v[136:139], v[192:195], v[110:113]
	v_mfma_f32_16x16x32_bf16 v[106:109], v[144:147], v[192:195], v[106:109]
	v_mfma_f32_16x16x32_bf16 v[94:97], v[136:139], v[212:215], v[94:97]
	v_mfma_f32_16x16x32_bf16 v[90:93], v[144:147], v[212:215], v[90:93]
	v_mfma_f32_16x16x32_bf16 v[78:81], v[136:139], v[220:223], v[78:81]
	v_mfma_f32_16x16x32_bf16 v[74:77], v[144:147], v[220:223], v[74:77]
	v_mfma_f32_16x16x32_bf16 v[126:129], v[140:143], v[188:191], v[126:129]
	v_mfma_f32_16x16x32_bf16 v[122:125], v[148:151], v[188:191], v[122:125]
	v_mfma_f32_16x16x32_bf16 v[110:113], v[140:143], v[196:199], v[110:113]
	v_mfma_f32_16x16x32_bf16 v[106:109], v[148:151], v[196:199], v[106:109]
	v_mfma_f32_16x16x32_bf16 v[94:97], v[140:143], v[216:219], v[94:97]
	v_mfma_f32_16x16x32_bf16 v[90:93], v[148:151], v[216:219], v[90:93]
	v_mfma_f32_16x16x32_bf16 v[78:81], v[140:143], v[224:227], v[78:81]
	v_mfma_f32_16x16x32_bf16 v[74:77], v[148:151], v[224:227], v[74:77]
	s_setprio 0
	s_setprio 1
	v_mfma_f32_16x16x32_bf16 v[118:121], v[158:161], v[184:187], v[118:121]
	v_mfma_f32_16x16x32_bf16 v[114:117], v[176:179], v[184:187], v[114:117]
	v_mfma_f32_16x16x32_bf16 v[102:105], v[158:161], v[192:195], v[102:105]
	v_mfma_f32_16x16x32_bf16 v[98:101], v[176:179], v[192:195], v[98:101]
	v_mfma_f32_16x16x32_bf16 v[86:89], v[158:161], v[212:215], v[86:89]
	v_mfma_f32_16x16x32_bf16 v[82:85], v[176:179], v[212:215], v[82:85]
	v_mfma_f32_16x16x32_bf16 v[70:73], v[158:161], v[220:223], v[70:73]
	v_mfma_f32_16x16x32_bf16 v[66:69], v[176:179], v[220:223], v[66:69]
	v_mfma_f32_16x16x32_bf16 v[118:121], v[172:175], v[188:191], v[118:121]
	v_mfma_f32_16x16x32_bf16 v[114:117], v[180:183], v[188:191], v[114:117]
	v_mfma_f32_16x16x32_bf16 v[102:105], v[172:175], v[196:199], v[102:105]
	v_mfma_f32_16x16x32_bf16 v[98:101], v[180:183], v[196:199], v[98:101]
	v_mfma_f32_16x16x32_bf16 v[86:89], v[172:175], v[216:219], v[86:89]
	v_mfma_f32_16x16x32_bf16 v[82:85], v[180:183], v[216:219], v[82:85]
	v_mfma_f32_16x16x32_bf16 v[70:73], v[172:175], v[224:227], v[70:73]
	s_barrier
	v_mfma_f32_16x16x32_bf16 v[66:69], v[180:183], v[224:227], v[66:69]
	s_setprio 0
	s_mov_b32 m0, s42
	s_add_u32 s78, s28, s40
	ds_read_b128 v[184:187], v157 offset:16384
	ds_read_b128 v[188:191], v157 offset:17408
	ds_read_b128 v[192:195], v157 offset:18432
	ds_read_b128 v[196:199], v157 offset:19456
	ds_read_b128 v[212:215], v157 offset:20480
	ds_read_b128 v[216:219], v157 offset:21504
	ds_read_b128 v[220:223], v157 offset:22528
	ds_read_b128 v[224:227], v157 offset:23552
	global_load_lds_dwordx4 v0, s[28:29]
	s_mov_b32 m0, s43
	s_addc_u32 s79, s29, 0
	global_load_lds_dwordx4 v134, s[28:29]
	s_mov_b32 m0, s45
	s_nop 0
	global_load_lds_dwordx4 v0, s[78:79]
	s_mov_b32 m0, s46
	s_nop 0
	global_load_lds_dwordx4 v134, s[78:79]
	s_mov_b32 m0, s47
	s_nop 0
	global_load_lds_dwordx4 v130, s[30:31]
	s_mov_b32 m0, s48
	s_nop 0
	global_load_lds_dwordx4 v132, s[30:31]
	s_waitcnt vmcnt(8)
	s_waitcnt lgkmcnt(0)
	s_barrier
	s_setprio 1
	s_waitcnt lgkmcnt(0)
	v_mfma_f32_16x16x32_bf16 v[62:65], v[136:139], v[184:187], v[62:65]
	v_mfma_f32_16x16x32_bf16 v[58:61], v[144:147], v[184:187], v[58:61]
	v_mfma_f32_16x16x32_bf16 v[46:49], v[136:139], v[192:195], v[46:49]
	v_mfma_f32_16x16x32_bf16 v[42:45], v[144:147], v[192:195], v[42:45]
	v_mfma_f32_16x16x32_bf16 v[30:33], v[136:139], v[212:215], v[30:33]
	v_mfma_f32_16x16x32_bf16 v[26:29], v[144:147], v[212:215], v[26:29]
	v_mfma_f32_16x16x32_bf16 v[14:17], v[136:139], v[220:223], v[14:17]
	v_mfma_f32_16x16x32_bf16 v[10:13], v[144:147], v[220:223], v[10:13]
	v_mfma_f32_16x16x32_bf16 v[62:65], v[140:143], v[188:191], v[62:65]
	v_mfma_f32_16x16x32_bf16 v[58:61], v[148:151], v[188:191], v[58:61]
	v_mfma_f32_16x16x32_bf16 v[46:49], v[140:143], v[196:199], v[46:49]
	v_mfma_f32_16x16x32_bf16 v[42:45], v[148:151], v[196:199], v[42:45]
	v_mfma_f32_16x16x32_bf16 v[30:33], v[140:143], v[216:219], v[30:33]
	v_mfma_f32_16x16x32_bf16 v[26:29], v[148:151], v[216:219], v[26:29]
	v_mfma_f32_16x16x32_bf16 v[14:17], v[140:143], v[224:227], v[14:17]
	v_mfma_f32_16x16x32_bf16 v[10:13], v[148:151], v[224:227], v[10:13]
	s_setprio 0
	s_setprio 1
	v_mfma_f32_16x16x32_bf16 v[54:57], v[158:161], v[184:187], v[54:57]
	v_mfma_f32_16x16x32_bf16 v[50:53], v[176:179], v[184:187], v[50:53]
	v_mfma_f32_16x16x32_bf16 v[38:41], v[158:161], v[192:195], v[38:41]
	v_mfma_f32_16x16x32_bf16 v[34:37], v[176:179], v[192:195], v[34:37]
	v_mfma_f32_16x16x32_bf16 v[22:25], v[158:161], v[212:215], v[22:25]
	v_mfma_f32_16x16x32_bf16 v[18:21], v[176:179], v[212:215], v[18:21]
	v_mfma_f32_16x16x32_bf16 v[6:9], v[158:161], v[220:223], v[6:9]
	v_mfma_f32_16x16x32_bf16 v[2:5], v[176:179], v[220:223], v[2:5]
	v_mfma_f32_16x16x32_bf16 v[54:57], v[172:175], v[188:191], v[54:57]
	v_mfma_f32_16x16x32_bf16 v[50:53], v[180:183], v[188:191], v[50:53]
	v_mfma_f32_16x16x32_bf16 v[38:41], v[172:175], v[196:199], v[38:41]
	v_mfma_f32_16x16x32_bf16 v[34:37], v[180:183], v[196:199], v[34:37]
	v_mfma_f32_16x16x32_bf16 v[22:25], v[172:175], v[216:219], v[22:25]
	v_mfma_f32_16x16x32_bf16 v[18:21], v[180:183], v[216:219], v[18:21]
	v_mfma_f32_16x16x32_bf16 v[6:9], v[172:175], v[224:227], v[6:9]
	s_barrier
	v_mfma_f32_16x16x32_bf16 v[2:5], v[180:183], v[224:227], v[2:5]
	s_setprio 0
	v_add_u32_e32 v148, s55, v155
	v_add_u32_e32 v152, s60, v155
	ds_read_b128 v[136:139], v148
	ds_read_b128 v[140:143], v148 offset:1024
	ds_read_b128 v[144:147], v148 offset:2048
	ds_read_b128 v[148:151], v148 offset:3072
	ds_read_b128 v[158:161], v152
	ds_read_b128 v[172:175], v152 offset:1024
	ds_read_b128 v[176:179], v152 offset:2048
	ds_read_b128 v[180:183], v152 offset:3072
	s_add_u32 s30, s30, s40
	s_addc_u32 s31, s31, 0
	s_mov_b32 m0, s49
	ds_read_b128 v[184:187], v157 offset:32768
	ds_read_b128 v[188:191], v157 offset:33792
	ds_read_b128 v[192:195], v157 offset:34816
	ds_read_b128 v[196:199], v157 offset:35840
	ds_read_b128 v[212:215], v157 offset:36864
	ds_read_b128 v[216:219], v157 offset:37888
	ds_read_b128 v[220:223], v157 offset:38912
	ds_read_b128 v[224:227], v157 offset:39936
	global_load_lds_dwordx4 v130, s[30:31]
	s_mov_b32 m0, s50
	s_nop 0
	global_load_lds_dwordx4 v132, s[30:31]
	s_waitcnt vmcnt(8)
	s_waitcnt lgkmcnt(0)
	s_barrier
	s_setprio 1
	s_waitcnt lgkmcnt(0)
	v_mfma_f32_16x16x32_bf16 v[126:129], v[136:139], v[184:187], v[126:129]
	v_mfma_f32_16x16x32_bf16 v[122:125], v[144:147], v[184:187], v[122:125]
	v_mfma_f32_16x16x32_bf16 v[110:113], v[136:139], v[192:195], v[110:113]
	v_mfma_f32_16x16x32_bf16 v[106:109], v[144:147], v[192:195], v[106:109]
	v_mfma_f32_16x16x32_bf16 v[94:97], v[136:139], v[212:215], v[94:97]
	v_mfma_f32_16x16x32_bf16 v[90:93], v[144:147], v[212:215], v[90:93]
	v_mfma_f32_16x16x32_bf16 v[78:81], v[136:139], v[220:223], v[78:81]
	v_mfma_f32_16x16x32_bf16 v[74:77], v[144:147], v[220:223], v[74:77]
	v_mfma_f32_16x16x32_bf16 v[126:129], v[140:143], v[188:191], v[126:129]
	v_mfma_f32_16x16x32_bf16 v[122:125], v[148:151], v[188:191], v[122:125]
	v_mfma_f32_16x16x32_bf16 v[110:113], v[140:143], v[196:199], v[110:113]
	v_mfma_f32_16x16x32_bf16 v[106:109], v[148:151], v[196:199], v[106:109]
	v_mfma_f32_16x16x32_bf16 v[94:97], v[140:143], v[216:219], v[94:97]
	v_mfma_f32_16x16x32_bf16 v[90:93], v[148:151], v[216:219], v[90:93]
	v_mfma_f32_16x16x32_bf16 v[78:81], v[140:143], v[224:227], v[78:81]
	v_mfma_f32_16x16x32_bf16 v[74:77], v[148:151], v[224:227], v[74:77]
	s_setprio 0
	s_setprio 1
	v_mfma_f32_16x16x32_bf16 v[118:121], v[158:161], v[184:187], v[118:121]
	v_mfma_f32_16x16x32_bf16 v[114:117], v[176:179], v[184:187], v[114:117]
	v_mfma_f32_16x16x32_bf16 v[102:105], v[158:161], v[192:195], v[102:105]
	v_mfma_f32_16x16x32_bf16 v[98:101], v[176:179], v[192:195], v[98:101]
	v_mfma_f32_16x16x32_bf16 v[86:89], v[158:161], v[212:215], v[86:89]
	v_mfma_f32_16x16x32_bf16 v[82:85], v[176:179], v[212:215], v[82:85]
	v_mfma_f32_16x16x32_bf16 v[70:73], v[158:161], v[220:223], v[70:73]
	v_mfma_f32_16x16x32_bf16 v[66:69], v[176:179], v[220:223], v[66:69]
	v_mfma_f32_16x16x32_bf16 v[118:121], v[172:175], v[188:191], v[118:121]
	v_mfma_f32_16x16x32_bf16 v[114:117], v[180:183], v[188:191], v[114:117]
	v_mfma_f32_16x16x32_bf16 v[102:105], v[172:175], v[196:199], v[102:105]
	v_mfma_f32_16x16x32_bf16 v[98:101], v[180:183], v[196:199], v[98:101]
	v_mfma_f32_16x16x32_bf16 v[86:89], v[172:175], v[216:219], v[86:89]
	v_mfma_f32_16x16x32_bf16 v[82:85], v[180:183], v[216:219], v[82:85]
	v_mfma_f32_16x16x32_bf16 v[70:73], v[172:175], v[224:227], v[70:73]
	s_barrier
	v_mfma_f32_16x16x32_bf16 v[66:69], v[180:183], v[224:227], v[66:69]
	s_setprio 0
	s_add_u32 s28, s28, s54
	s_addc_u32 s29, s29, 0
	s_mov_b32 m0, s56
	ds_read_b128 v[184:187], v157 offset:49152
	ds_read_b128 v[188:191], v157 offset:50176
	ds_read_b128 v[192:195], v157 offset:51200
	ds_read_b128 v[196:199], v157 offset:52224
	ds_read_b128 v[212:215], v157 offset:53248
	ds_read_b128 v[216:219], v157 offset:54272
	ds_read_b128 v[220:223], v157 offset:55296
	ds_read_b128 v[224:227], v157 offset:56320
	global_load_lds_dwordx4 v0, s[28:29]
	v_lshl_add_u64 v[152:153], s[28:29], 0, v[134:135]
	s_add_u32 s28, s28, s40
	s_mov_b32 m0, s57
	s_addc_u32 s29, s29, 0
	global_load_lds_dwordx4 v[152:153], off
	s_mov_b32 m0, s62
	s_nop 0
	global_load_lds_dwordx4 v0, s[28:29]
	s_mov_b32 m0, s63
	s_nop 0
	global_load_lds_dwordx4 v134, s[28:29]
	s_mov_b32 m0, s58
	s_nop 0
	global_load_lds_dwordx4 v130, s[26:27]
	s_mov_b32 m0, s59
	s_nop 0
	global_load_lds_dwordx4 v132, s[26:27]
	s_waitcnt vmcnt(8)
	s_waitcnt lgkmcnt(0)
	s_barrier
	s_setprio 1
	s_waitcnt lgkmcnt(0)
	v_mfma_f32_16x16x32_bf16 v[62:65], v[136:139], v[184:187], v[62:65]
	v_mfma_f32_16x16x32_bf16 v[58:61], v[144:147], v[184:187], v[58:61]
	v_mfma_f32_16x16x32_bf16 v[46:49], v[136:139], v[192:195], v[46:49]
	v_mfma_f32_16x16x32_bf16 v[42:45], v[144:147], v[192:195], v[42:45]
	v_mfma_f32_16x16x32_bf16 v[30:33], v[136:139], v[212:215], v[30:33]
	v_mfma_f32_16x16x32_bf16 v[26:29], v[144:147], v[212:215], v[26:29]
	v_mfma_f32_16x16x32_bf16 v[14:17], v[136:139], v[220:223], v[14:17]
	v_mfma_f32_16x16x32_bf16 v[10:13], v[144:147], v[220:223], v[10:13]
	v_mfma_f32_16x16x32_bf16 v[62:65], v[140:143], v[188:191], v[62:65]
	v_mfma_f32_16x16x32_bf16 v[58:61], v[148:151], v[188:191], v[58:61]
	v_mfma_f32_16x16x32_bf16 v[46:49], v[140:143], v[196:199], v[46:49]
	v_mfma_f32_16x16x32_bf16 v[42:45], v[148:151], v[196:199], v[42:45]
	v_mfma_f32_16x16x32_bf16 v[30:33], v[140:143], v[216:219], v[30:33]
	v_mfma_f32_16x16x32_bf16 v[26:29], v[148:151], v[216:219], v[26:29]
	v_mfma_f32_16x16x32_bf16 v[14:17], v[140:143], v[224:227], v[14:17]
	v_mfma_f32_16x16x32_bf16 v[10:13], v[148:151], v[224:227], v[10:13]
	s_setprio 0
	s_setprio 1
	v_mfma_f32_16x16x32_bf16 v[54:57], v[158:161], v[184:187], v[54:57]
	v_mfma_f32_16x16x32_bf16 v[50:53], v[176:179], v[184:187], v[50:53]
	v_mfma_f32_16x16x32_bf16 v[38:41], v[158:161], v[192:195], v[38:41]
	v_mfma_f32_16x16x32_bf16 v[34:37], v[176:179], v[192:195], v[34:37]
	v_mfma_f32_16x16x32_bf16 v[22:25], v[158:161], v[212:215], v[22:25]
	v_mfma_f32_16x16x32_bf16 v[18:21], v[176:179], v[212:215], v[18:21]
	v_mfma_f32_16x16x32_bf16 v[6:9], v[158:161], v[220:223], v[6:9]
	v_mfma_f32_16x16x32_bf16 v[2:5], v[176:179], v[220:223], v[2:5]
	v_mfma_f32_16x16x32_bf16 v[54:57], v[172:175], v[188:191], v[54:57]
	v_mfma_f32_16x16x32_bf16 v[50:53], v[180:183], v[188:191], v[50:53]
	v_mfma_f32_16x16x32_bf16 v[38:41], v[172:175], v[196:199], v[38:41]
	v_mfma_f32_16x16x32_bf16 v[34:37], v[180:183], v[196:199], v[34:37]
	v_mfma_f32_16x16x32_bf16 v[22:25], v[172:175], v[216:219], v[22:25]
	v_mfma_f32_16x16x32_bf16 v[18:21], v[180:183], v[216:219], v[18:21]
	v_mfma_f32_16x16x32_bf16 v[6:9], v[172:175], v[224:227], v[6:9]
	s_barrier
	v_mfma_f32_16x16x32_bf16 v[2:5], v[180:183], v[224:227], v[2:5]
	s_setprio 0
	s_add_i32 s77, s77, 2
	s_cmp_ge_i32 s77, s52
	s_cbranch_scc0 .LBB0_575

.LBB0_852:
	s_add_i32 s26, s0, s79
	s_add_i32 s24, s26, 1
	s_cmp_ge_i32 s24, s53
	s_cselect_b32 s25, s53, 0
	s_sub_i32 s24, s24, s25
	s_ashr_i32 s25, s24, 31
	s_lshl_b64 s[82:83], s[24:25], s39
	s_add_i32 s26, s26, 2
	s_cmp_ge_i32 s26, s53
	s_cselect_b32 s24, s53, 0
	s_sub_i32 s24, s26, s24
	s_ashr_i32 s25, s24, 31
	v_add_u32_e32 v137, s1, v134
	s_lshl_b64 s[24:25], s[24:25], s39
	ds_read_b128 v[138:141], v137
	ds_read_b128 v[142:145], v137 offset:1024
	ds_read_b128 v[146:149], v137 offset:2048
	ds_read_b128 v[150:153], v137 offset:3072
	v_add_u32_e32 v137, s46, v134
	s_add_u32 s26, s20, s24
	ds_read_b128 v[156:159], v137
	ds_read_b128 v[160:163], v137 offset:1024
	ds_read_b128 v[172:175], v137 offset:2048
	ds_read_b128 v[176:179], v137 offset:3072
	s_addc_u32 s27, s21, s25
	s_add_u32 s24, s22, s24
	s_addc_u32 s25, s23, s25
	s_cmp_eq_u32 s55, s79
	s_cselect_b32 s28, s75, s26
	s_cselect_b32 s29, s76, s27
	s_cselect_b32 s27, s78, s25
	s_cselect_b32 s26, s77, s24
	s_add_u32 s24, s28, s56
	s_addc_u32 s25, s29, 0
	s_add_u32 s82, s72, s82
	s_addc_u32 s83, s73, s83
	s_add_i32 m0, s49, 0xc000
	ds_read_b128 v[180:183], v136
	ds_read_b128 v[184:187], v136 offset:1024
	ds_read_b128 v[188:191], v136 offset:2048
	ds_read_b128 v[192:195], v136 offset:3072
	ds_read_b128 v[196:199], v136 offset:4096
	ds_read_b128 v[212:215], v136 offset:5120
	ds_read_b128 v[216:219], v136 offset:6144
	ds_read_b128 v[220:223], v136 offset:7168
	global_load_lds_dwordx4 v0, s[82:83]
	s_add_i32 m0, s49, 0xe000
	s_nop 0
	global_load_lds_dwordx4 v132, s[82:83]
	s_waitcnt vmcnt(8)
	s_waitcnt lgkmcnt(0)
	s_barrier
	s_setprio 1
	s_waitcnt lgkmcnt(0)
	v_mfma_f32_16x16x32_bf16 v[126:129], v[138:141], v[180:183], v[126:129]
	v_mfma_f32_16x16x32_bf16 v[122:125], v[146:149], v[180:183], v[122:125]
	v_mfma_f32_16x16x32_bf16 v[110:113], v[138:141], v[188:191], v[110:113]
	v_mfma_f32_16x16x32_bf16 v[106:109], v[146:149], v[188:191], v[106:109]
	v_mfma_f32_16x16x32_bf16 v[94:97], v[138:141], v[196:199], v[94:97]
	v_mfma_f32_16x16x32_bf16 v[90:93], v[146:149], v[196:199], v[90:93]
	v_mfma_f32_16x16x32_bf16 v[78:81], v[138:141], v[216:219], v[78:81]
	v_mfma_f32_16x16x32_bf16 v[74:77], v[146:149], v[216:219], v[74:77]
	v_mfma_f32_16x16x32_bf16 v[126:129], v[142:145], v[184:187], v[126:129]
	v_mfma_f32_16x16x32_bf16 v[122:125], v[150:153], v[184:187], v[122:125]
	v_mfma_f32_16x16x32_bf16 v[110:113], v[142:145], v[192:195], v[110:113]
	v_mfma_f32_16x16x32_bf16 v[106:109], v[150:153], v[192:195], v[106:109]
	v_mfma_f32_16x16x32_bf16 v[94:97], v[142:145], v[212:215], v[94:97]
	v_mfma_f32_16x16x32_bf16 v[90:93], v[150:153], v[212:215], v[90:93]
	v_mfma_f32_16x16x32_bf16 v[78:81], v[142:145], v[220:223], v[78:81]
	v_mfma_f32_16x16x32_bf16 v[74:77], v[150:153], v[220:223], v[74:77]
	s_setprio 0
	s_setprio 1
	v_mfma_f32_16x16x32_bf16 v[118:121], v[156:159], v[180:183], v[118:121]
	v_mfma_f32_16x16x32_bf16 v[114:117], v[172:175], v[180:183], v[114:117]
	v_mfma_f32_16x16x32_bf16 v[102:105], v[156:159], v[188:191], v[102:105]
	v_mfma_f32_16x16x32_bf16 v[98:101], v[172:175], v[188:191], v[98:101]
	v_mfma_f32_16x16x32_bf16 v[86:89], v[156:159], v[196:199], v[86:89]
	v_mfma_f32_16x16x32_bf16 v[82:85], v[172:175], v[196:199], v[82:85]
	v_mfma_f32_16x16x32_bf16 v[70:73], v[156:159], v[216:219], v[70:73]
	v_mfma_f32_16x16x32_bf16 v[66:69], v[172:175], v[216:219], v[66:69]
	v_mfma_f32_16x16x32_bf16 v[118:121], v[160:163], v[184:187], v[118:121]
	v_mfma_f32_16x16x32_bf16 v[114:117], v[176:179], v[184:187], v[114:117]
	v_mfma_f32_16x16x32_bf16 v[102:105], v[160:163], v[192:195], v[102:105]
	v_mfma_f32_16x16x32_bf16 v[98:101], v[176:179], v[192:195], v[98:101]
	v_mfma_f32_16x16x32_bf16 v[86:89], v[160:163], v[212:215], v[86:89]
	v_mfma_f32_16x16x32_bf16 v[82:85], v[176:179], v[212:215], v[82:85]
	v_mfma_f32_16x16x32_bf16 v[70:73], v[160:163], v[220:223], v[70:73]
	s_barrier
	v_mfma_f32_16x16x32_bf16 v[66:69], v[176:179], v[220:223], v[66:69]
	s_setprio 0
	s_mov_b32 m0, s40
	s_add_u32 s82, s26, s38
	ds_read_b128 v[180:183], v136 offset:16384
	ds_read_b128 v[184:187], v136 offset:17408
	ds_read_b128 v[188:191], v136 offset:18432
	ds_read_b128 v[192:195], v136 offset:19456
	ds_read_b128 v[196:199], v136 offset:20480
	ds_read_b128 v[212:215], v136 offset:21504
	ds_read_b128 v[216:219], v136 offset:22528
	ds_read_b128 v[220:223], v136 offset:23552
	global_load_lds_dwordx4 v0, s[26:27]
	s_mov_b32 m0, s41
	s_addc_u32 s83, s27, 0
	global_load_lds_dwordx4 v132, s[26:27]
	s_mov_b32 m0, s47
	s_nop 0
	global_load_lds_dwordx4 v0, s[82:83]
	s_mov_b32 m0, s48
	s_nop 0
	global_load_lds_dwordx4 v132, s[82:83]
	s_mov_b32 m0, s49
	s_nop 0
	global_load_lds_dwordx4 v0, s[28:29]
	s_mov_b32 m0, s50
	s_nop 0
	global_load_lds_dwordx4 v132, s[28:29]
	s_waitcnt vmcnt(8)
	s_waitcnt lgkmcnt(0)
	s_barrier
	s_setprio 1
	s_waitcnt lgkmcnt(0)
	v_mfma_f32_16x16x32_bf16 v[62:65], v[138:141], v[180:183], v[62:65]
	v_mfma_f32_16x16x32_bf16 v[58:61], v[146:149], v[180:183], v[58:61]
	v_mfma_f32_16x16x32_bf16 v[46:49], v[138:141], v[188:191], v[46:49]
	v_mfma_f32_16x16x32_bf16 v[42:45], v[146:149], v[188:191], v[42:45]
	v_mfma_f32_16x16x32_bf16 v[30:33], v[138:141], v[196:199], v[30:33]
	v_mfma_f32_16x16x32_bf16 v[26:29], v[146:149], v[196:199], v[26:29]
	v_mfma_f32_16x16x32_bf16 v[14:17], v[138:141], v[216:219], v[14:17]
	v_mfma_f32_16x16x32_bf16 v[10:13], v[146:149], v[216:219], v[10:13]
	v_mfma_f32_16x16x32_bf16 v[62:65], v[142:145], v[184:187], v[62:65]
	v_mfma_f32_16x16x32_bf16 v[58:61], v[150:153], v[184:187], v[58:61]
	v_mfma_f32_16x16x32_bf16 v[46:49], v[142:145], v[192:195], v[46:49]
	v_mfma_f32_16x16x32_bf16 v[42:45], v[150:153], v[192:195], v[42:45]
	v_mfma_f32_16x16x32_bf16 v[30:33], v[142:145], v[212:215], v[30:33]
	v_mfma_f32_16x16x32_bf16 v[26:29], v[150:153], v[212:215], v[26:29]
	v_mfma_f32_16x16x32_bf16 v[14:17], v[142:145], v[220:223], v[14:17]
	v_mfma_f32_16x16x32_bf16 v[10:13], v[150:153], v[220:223], v[10:13]
	s_setprio 0
	s_setprio 1
	v_mfma_f32_16x16x32_bf16 v[54:57], v[156:159], v[180:183], v[54:57]
	v_mfma_f32_16x16x32_bf16 v[50:53], v[172:175], v[180:183], v[50:53]
	v_mfma_f32_16x16x32_bf16 v[38:41], v[156:159], v[188:191], v[38:41]
	v_mfma_f32_16x16x32_bf16 v[34:37], v[172:175], v[188:191], v[34:37]
	v_mfma_f32_16x16x32_bf16 v[22:25], v[156:159], v[196:199], v[22:25]
	v_mfma_f32_16x16x32_bf16 v[18:21], v[172:175], v[196:199], v[18:21]
	v_mfma_f32_16x16x32_bf16 v[6:9], v[156:159], v[216:219], v[6:9]
	v_mfma_f32_16x16x32_bf16 v[2:5], v[172:175], v[216:219], v[2:5]
	v_mfma_f32_16x16x32_bf16 v[54:57], v[160:163], v[184:187], v[54:57]
	v_mfma_f32_16x16x32_bf16 v[50:53], v[176:179], v[184:187], v[50:53]
	v_mfma_f32_16x16x32_bf16 v[38:41], v[160:163], v[192:195], v[38:41]
	v_mfma_f32_16x16x32_bf16 v[34:37], v[176:179], v[192:195], v[34:37]
	v_mfma_f32_16x16x32_bf16 v[22:25], v[160:163], v[212:215], v[22:25]
	v_mfma_f32_16x16x32_bf16 v[18:21], v[176:179], v[212:215], v[18:21]
	v_mfma_f32_16x16x32_bf16 v[6:9], v[160:163], v[220:223], v[6:9]
	s_barrier
	v_mfma_f32_16x16x32_bf16 v[2:5], v[176:179], v[220:223], v[2:5]
	s_setprio 0
	v_add_u32_e32 v137, s57, v134
	ds_read_b128 v[138:141], v137
	ds_read_b128 v[142:145], v137 offset:1024
	ds_read_b128 v[146:149], v137 offset:2048
	ds_read_b128 v[150:153], v137 offset:3072
	v_add_u32_e32 v137, s63, v134
	ds_read_b128 v[156:159], v137
	ds_read_b128 v[160:163], v137 offset:1024
	ds_read_b128 v[172:175], v137 offset:2048
	ds_read_b128 v[176:179], v137 offset:3072
	s_add_u32 s28, s28, s38
	s_addc_u32 s29, s29, 0
	s_mov_b32 m0, s51
	ds_read_b128 v[180:183], v136 offset:32768
	ds_read_b128 v[184:187], v136 offset:33792
	ds_read_b128 v[188:191], v136 offset:34816
	ds_read_b128 v[192:195], v136 offset:35840
	ds_read_b128 v[196:199], v136 offset:36864
	ds_read_b128 v[212:215], v136 offset:37888
	ds_read_b128 v[216:219], v136 offset:38912
	ds_read_b128 v[220:223], v136 offset:39936
	global_load_lds_dwordx4 v0, s[28:29]
	s_mov_b32 m0, s52
	s_nop 0
	global_load_lds_dwordx4 v132, s[28:29]
	s_waitcnt vmcnt(8)
	s_waitcnt lgkmcnt(0)
	s_barrier
	s_setprio 1
	s_waitcnt lgkmcnt(0)
	v_mfma_f32_16x16x32_bf16 v[126:129], v[138:141], v[180:183], v[126:129]
	v_mfma_f32_16x16x32_bf16 v[122:125], v[146:149], v[180:183], v[122:125]
	v_mfma_f32_16x16x32_bf16 v[110:113], v[138:141], v[188:191], v[110:113]
	v_mfma_f32_16x16x32_bf16 v[106:109], v[146:149], v[188:191], v[106:109]
	v_mfma_f32_16x16x32_bf16 v[94:97], v[138:141], v[196:199], v[94:97]
	v_mfma_f32_16x16x32_bf16 v[90:93], v[146:149], v[196:199], v[90:93]
	v_mfma_f32_16x16x32_bf16 v[78:81], v[138:141], v[216:219], v[78:81]
	v_mfma_f32_16x16x32_bf16 v[74:77], v[146:149], v[216:219], v[74:77]
	v_mfma_f32_16x16x32_bf16 v[126:129], v[142:145], v[184:187], v[126:129]
	v_mfma_f32_16x16x32_bf16 v[122:125], v[150:153], v[184:187], v[122:125]
	v_mfma_f32_16x16x32_bf16 v[110:113], v[142:145], v[192:195], v[110:113]
	v_mfma_f32_16x16x32_bf16 v[106:109], v[150:153], v[192:195], v[106:109]
	v_mfma_f32_16x16x32_bf16 v[94:97], v[142:145], v[212:215], v[94:97]
	v_mfma_f32_16x16x32_bf16 v[90:93], v[150:153], v[212:215], v[90:93]
	v_mfma_f32_16x16x32_bf16 v[78:81], v[142:145], v[220:223], v[78:81]
	v_mfma_f32_16x16x32_bf16 v[74:77], v[150:153], v[220:223], v[74:77]
	s_setprio 0
	s_setprio 1
	v_mfma_f32_16x16x32_bf16 v[118:121], v[156:159], v[180:183], v[118:121]
	v_mfma_f32_16x16x32_bf16 v[114:117], v[172:175], v[180:183], v[114:117]
	v_mfma_f32_16x16x32_bf16 v[102:105], v[156:159], v[188:191], v[102:105]
	v_mfma_f32_16x16x32_bf16 v[98:101], v[172:175], v[188:191], v[98:101]
	v_mfma_f32_16x16x32_bf16 v[86:89], v[156:159], v[196:199], v[86:89]
	v_mfma_f32_16x16x32_bf16 v[82:85], v[172:175], v[196:199], v[82:85]
	v_mfma_f32_16x16x32_bf16 v[70:73], v[156:159], v[216:219], v[70:73]
	v_mfma_f32_16x16x32_bf16 v[66:69], v[172:175], v[216:219], v[66:69]
	v_mfma_f32_16x16x32_bf16 v[118:121], v[160:163], v[184:187], v[118:121]
	v_mfma_f32_16x16x32_bf16 v[114:117], v[176:179], v[184:187], v[114:117]
	v_mfma_f32_16x16x32_bf16 v[102:105], v[160:163], v[192:195], v[102:105]
	v_mfma_f32_16x16x32_bf16 v[98:101], v[176:179], v[192:195], v[98:101]
	v_mfma_f32_16x16x32_bf16 v[86:89], v[160:163], v[212:215], v[86:89]
	v_mfma_f32_16x16x32_bf16 v[82:85], v[176:179], v[212:215], v[82:85]
	v_mfma_f32_16x16x32_bf16 v[70:73], v[160:163], v[220:223], v[70:73]
	s_barrier
	v_mfma_f32_16x16x32_bf16 v[66:69], v[176:179], v[220:223], v[66:69]
	s_setprio 0
	s_add_u32 s26, s26, s56
	s_addc_u32 s27, s27, 0
	s_mov_b32 m0, s58
	ds_read_b128 v[180:183], v136 offset:49152
	ds_read_b128 v[184:187], v136 offset:50176
	ds_read_b128 v[188:191], v136 offset:51200
	ds_read_b128 v[192:195], v136 offset:52224
	ds_read_b128 v[196:199], v136 offset:53248
	ds_read_b128 v[212:215], v136 offset:54272
	ds_read_b128 v[216:219], v136 offset:55296
	ds_read_b128 v[220:223], v136 offset:56320
	global_load_lds_dwordx4 v0, s[26:27]
	v_lshl_add_u64 v[168:169], s[26:27], 0, v[132:133]
	s_add_u32 s26, s26, s38
	s_mov_b32 m0, s59
	s_addc_u32 s27, s27, 0
	global_load_lds_dwordx4 v[168:169], off
	s_mov_b32 m0, s64
	s_nop 0
	global_load_lds_dwordx4 v0, s[26:27]
	s_mov_b32 m0, s65
	s_nop 0
	global_load_lds_dwordx4 v132, s[26:27]
	s_mov_b32 m0, s60
	s_nop 0
	global_load_lds_dwordx4 v0, s[24:25]
	s_mov_b32 m0, s62
	s_nop 0
	global_load_lds_dwordx4 v132, s[24:25]
	s_waitcnt vmcnt(8)
	s_waitcnt lgkmcnt(0)
	s_barrier
	s_setprio 1
	s_waitcnt lgkmcnt(0)
	v_mfma_f32_16x16x32_bf16 v[62:65], v[138:141], v[180:183], v[62:65]
	v_mfma_f32_16x16x32_bf16 v[58:61], v[146:149], v[180:183], v[58:61]
	v_mfma_f32_16x16x32_bf16 v[46:49], v[138:141], v[188:191], v[46:49]
	v_mfma_f32_16x16x32_bf16 v[42:45], v[146:149], v[188:191], v[42:45]
	v_mfma_f32_16x16x32_bf16 v[30:33], v[138:141], v[196:199], v[30:33]
	v_mfma_f32_16x16x32_bf16 v[26:29], v[146:149], v[196:199], v[26:29]
	v_mfma_f32_16x16x32_bf16 v[14:17], v[138:141], v[216:219], v[14:17]
	v_mfma_f32_16x16x32_bf16 v[10:13], v[146:149], v[216:219], v[10:13]
	v_mfma_f32_16x16x32_bf16 v[62:65], v[142:145], v[184:187], v[62:65]
	v_mfma_f32_16x16x32_bf16 v[58:61], v[150:153], v[184:187], v[58:61]
	v_mfma_f32_16x16x32_bf16 v[46:49], v[142:145], v[192:195], v[46:49]
	v_mfma_f32_16x16x32_bf16 v[42:45], v[150:153], v[192:195], v[42:45]
	v_mfma_f32_16x16x32_bf16 v[30:33], v[142:145], v[212:215], v[30:33]
	v_mfma_f32_16x16x32_bf16 v[26:29], v[150:153], v[212:215], v[26:29]
	v_mfma_f32_16x16x32_bf16 v[14:17], v[142:145], v[220:223], v[14:17]
	v_mfma_f32_16x16x32_bf16 v[10:13], v[150:153], v[220:223], v[10:13]
	s_setprio 0
	s_setprio 1
	v_mfma_f32_16x16x32_bf16 v[54:57], v[156:159], v[180:183], v[54:57]
	v_mfma_f32_16x16x32_bf16 v[50:53], v[172:175], v[180:183], v[50:53]
	v_mfma_f32_16x16x32_bf16 v[38:41], v[156:159], v[188:191], v[38:41]
	v_mfma_f32_16x16x32_bf16 v[34:37], v[172:175], v[188:191], v[34:37]
	v_mfma_f32_16x16x32_bf16 v[22:25], v[156:159], v[196:199], v[22:25]
	v_mfma_f32_16x16x32_bf16 v[18:21], v[172:175], v[196:199], v[18:21]
	v_mfma_f32_16x16x32_bf16 v[6:9], v[156:159], v[216:219], v[6:9]
	v_mfma_f32_16x16x32_bf16 v[2:5], v[172:175], v[216:219], v[2:5]
	v_mfma_f32_16x16x32_bf16 v[54:57], v[160:163], v[184:187], v[54:57]
	v_mfma_f32_16x16x32_bf16 v[50:53], v[176:179], v[184:187], v[50:53]
	v_mfma_f32_16x16x32_bf16 v[38:41], v[160:163], v[192:195], v[38:41]
	v_mfma_f32_16x16x32_bf16 v[34:37], v[176:179], v[192:195], v[34:37]
	v_mfma_f32_16x16x32_bf16 v[22:25], v[160:163], v[212:215], v[22:25]
	v_mfma_f32_16x16x32_bf16 v[18:21], v[176:179], v[212:215], v[18:21]
	v_mfma_f32_16x16x32_bf16 v[6:9], v[160:163], v[220:223], v[6:9]
	s_barrier
	v_mfma_f32_16x16x32_bf16 v[2:5], v[176:179], v[220:223], v[2:5]
	s_setprio 0
	s_add_i32 s79, s79, 2
	s_cmp_ge_i32 s79, s53
	s_cbranch_scc0 .LBB0_852

.LBB0_1216:
	s_add_i32 s28, s0, s74
	s_add_i32 s4, s28, 1
	s_cmp_ge_i32 s4, s50
	s_cselect_b32 s5, s50, 0
	s_sub_i32 s4, s4, s5
	s_ashr_i32 s5, s4, 31
	s_lshl_b64 s[76:77], s[4:5], s39
	s_add_i32 s28, s28, 2
	s_cmp_ge_i32 s28, s50
	s_cselect_b32 s4, s50, 0
	s_sub_i32 s4, s28, s4
	s_ashr_i32 s5, s4, 31
	v_add_u32_e32 v0, s1, v188
	s_lshl_b64 s[4:5], s[4:5], s39
	ds_read_b128 v[132:135], v0
	ds_read_b128 v[136:139], v0 offset:1024
	ds_read_b128 v[140:143], v0 offset:2048
	ds_read_b128 v[144:147], v0 offset:3072
	v_add_u32_e32 v0, s42, v188
	s_add_u32 s28, s6, s4
	ds_read_b128 v[148:151], v0
	ds_read_b128 v[152:155], v0 offset:1024
	ds_read_b128 v[156:159], v0 offset:2048
	ds_read_b128 v[160:163], v0 offset:3072
	s_addc_u32 s29, s7, s5
	s_add_u32 s4, s26, s4
	s_addc_u32 s5, s27, s5
	s_cmp_eq_u32 s51, s74
	s_cselect_b32 s30, s70, s28
	s_cselect_b32 s31, s71, s29
	s_cselect_b32 s29, s73, s5
	s_cselect_b32 s28, s72, s4
	s_add_u32 s4, s30, s52
	s_addc_u32 s5, s31, 0
	s_add_u32 s76, s68, s76
	s_addc_u32 s77, s69, s77
	s_add_i32 m0, s45, 0xc000
	ds_read_b128 v[180:183], v190
	ds_read_b128 v[184:187], v190 offset:1024
	ds_read_b128 v[192:195], v190 offset:2048
	ds_read_b128 v[196:199], v190 offset:3072
	ds_read_b128 v[212:215], v190 offset:4096
	ds_read_b128 v[216:219], v190 offset:5120
	ds_read_b128 v[220:223], v190 offset:6144
	ds_read_b128 v[224:227], v190 offset:7168
	global_load_lds_dwordx4 v172, s[76:77]
	s_add_i32 m0, s45, 0xe000
	s_nop 0
	global_load_lds_dwordx4 v176, s[76:77]
	s_waitcnt vmcnt(8)
	s_waitcnt lgkmcnt(0)
	s_barrier
	s_setprio 1
	s_waitcnt lgkmcnt(0)
	v_mfma_f32_16x16x32_bf16 v[112:115], v[132:135], v[180:183], v[112:115]
	v_mfma_f32_16x16x32_bf16 v[108:111], v[140:143], v[180:183], v[108:111]
	v_mfma_f32_16x16x32_bf16 v[104:107], v[132:135], v[192:195], v[104:107]
	v_mfma_f32_16x16x32_bf16 v[100:103], v[140:143], v[192:195], v[100:103]
	v_mfma_f32_16x16x32_bf16 v[96:99], v[132:135], v[212:215], v[96:99]
	v_mfma_f32_16x16x32_bf16 v[92:95], v[140:143], v[212:215], v[92:95]
	v_mfma_f32_16x16x32_bf16 v[88:91], v[132:135], v[220:223], v[88:91]
	v_mfma_f32_16x16x32_bf16 v[84:87], v[140:143], v[220:223], v[84:87]
	v_mfma_f32_16x16x32_bf16 v[112:115], v[136:139], v[184:187], v[112:115]
	v_mfma_f32_16x16x32_bf16 v[108:111], v[144:147], v[184:187], v[108:111]
	v_mfma_f32_16x16x32_bf16 v[104:107], v[136:139], v[196:199], v[104:107]
	v_mfma_f32_16x16x32_bf16 v[100:103], v[144:147], v[196:199], v[100:103]
	v_mfma_f32_16x16x32_bf16 v[96:99], v[136:139], v[216:219], v[96:99]
	v_mfma_f32_16x16x32_bf16 v[92:95], v[144:147], v[216:219], v[92:95]
	v_mfma_f32_16x16x32_bf16 v[88:91], v[136:139], v[224:227], v[88:91]
	v_mfma_f32_16x16x32_bf16 v[84:87], v[144:147], v[224:227], v[84:87]
	s_setprio 0
	s_setprio 1
	v_mfma_f32_16x16x32_bf16 v[80:83], v[148:151], v[180:183], v[80:83]
	v_mfma_f32_16x16x32_bf16 v[76:79], v[156:159], v[180:183], v[76:79]
	v_mfma_f32_16x16x32_bf16 v[72:75], v[148:151], v[192:195], v[72:75]
	v_mfma_f32_16x16x32_bf16 v[68:71], v[156:159], v[192:195], v[68:71]
	v_mfma_f32_16x16x32_bf16 v[64:67], v[148:151], v[212:215], v[64:67]
	v_mfma_f32_16x16x32_bf16 v[60:63], v[156:159], v[212:215], v[60:63]
	v_mfma_f32_16x16x32_bf16 v[56:59], v[148:151], v[220:223], v[56:59]
	v_mfma_f32_16x16x32_bf16 v[48:51], v[156:159], v[220:223], v[48:51]
	v_mfma_f32_16x16x32_bf16 v[80:83], v[152:155], v[184:187], v[80:83]
	v_mfma_f32_16x16x32_bf16 v[76:79], v[160:163], v[184:187], v[76:79]
	v_mfma_f32_16x16x32_bf16 v[72:75], v[152:155], v[196:199], v[72:75]
	v_mfma_f32_16x16x32_bf16 v[68:71], v[160:163], v[196:199], v[68:71]
	v_mfma_f32_16x16x32_bf16 v[64:67], v[152:155], v[216:219], v[64:67]
	v_mfma_f32_16x16x32_bf16 v[60:63], v[160:163], v[216:219], v[60:63]
	v_mfma_f32_16x16x32_bf16 v[56:59], v[152:155], v[224:227], v[56:59]
	s_barrier
	v_mfma_f32_16x16x32_bf16 v[48:51], v[160:163], v[224:227], v[48:51]
	s_setprio 0
	s_mov_b32 m0, s40
	s_add_u32 s76, s28, s38
	ds_read_b128 v[180:183], v190 offset:16384
	ds_read_b128 v[184:187], v190 offset:17408
	ds_read_b128 v[192:195], v190 offset:18432
	ds_read_b128 v[196:199], v190 offset:19456
	ds_read_b128 v[212:215], v190 offset:20480
	ds_read_b128 v[216:219], v190 offset:21504
	ds_read_b128 v[220:223], v190 offset:22528
	ds_read_b128 v[224:227], v190 offset:23552
	global_load_lds_dwordx4 v174, s[28:29]
	s_mov_b32 m0, s41
	s_addc_u32 s77, s29, 0
	global_load_lds_dwordx4 v178, s[28:29]
	s_mov_b32 m0, s43
	s_nop 0
	global_load_lds_dwordx4 v174, s[76:77]
	s_mov_b32 m0, s44
	s_nop 0
	global_load_lds_dwordx4 v178, s[76:77]
	s_mov_b32 m0, s45
	s_nop 0
	global_load_lds_dwordx4 v172, s[30:31]
	s_mov_b32 m0, s46
	s_nop 0
	global_load_lds_dwordx4 v176, s[30:31]
	s_waitcnt vmcnt(8)
	s_waitcnt lgkmcnt(0)
	s_barrier
	s_setprio 1
	s_waitcnt lgkmcnt(0)
	v_mfma_f32_16x16x32_bf16 v[52:55], v[132:135], v[180:183], v[52:55]
	v_mfma_f32_16x16x32_bf16 v[44:47], v[140:143], v[180:183], v[44:47]
	v_mfma_f32_16x16x32_bf16 v[40:43], v[132:135], v[192:195], v[40:43]
	v_mfma_f32_16x16x32_bf16 v[36:39], v[140:143], v[192:195], v[36:39]
	v_mfma_f32_16x16x32_bf16 v[32:35], v[132:135], v[212:215], v[32:35]
	v_mfma_f32_16x16x32_bf16 v[28:31], v[140:143], v[212:215], v[28:31]
	v_mfma_f32_16x16x32_bf16 v[24:27], v[132:135], v[220:223], v[24:27]
	v_mfma_f32_16x16x32_bf16 v[20:23], v[140:143], v[220:223], v[20:23]
	v_mfma_f32_16x16x32_bf16 v[52:55], v[136:139], v[184:187], v[52:55]
	v_mfma_f32_16x16x32_bf16 v[44:47], v[144:147], v[184:187], v[44:47]
	v_mfma_f32_16x16x32_bf16 v[40:43], v[136:139], v[196:199], v[40:43]
	v_mfma_f32_16x16x32_bf16 v[36:39], v[144:147], v[196:199], v[36:39]
	v_mfma_f32_16x16x32_bf16 v[32:35], v[136:139], v[216:219], v[32:35]
	v_mfma_f32_16x16x32_bf16 v[28:31], v[144:147], v[216:219], v[28:31]
	v_mfma_f32_16x16x32_bf16 v[24:27], v[136:139], v[224:227], v[24:27]
	v_mfma_f32_16x16x32_bf16 v[20:23], v[144:147], v[224:227], v[20:23]
	s_setprio 0
	s_setprio 1
	v_mfma_f32_16x16x32_bf16 v[16:19], v[148:151], v[180:183], v[16:19]
	v_mfma_f32_16x16x32_bf16 v[12:15], v[156:159], v[180:183], v[12:15]
	v_mfma_f32_16x16x32_bf16 v[8:11], v[148:151], v[192:195], v[8:11]
	v_mfma_f32_16x16x32_bf16 v[2:5], v[156:159], v[192:195], v[4:7]
	v_mfma_f32_16x16x32_bf16 v[116:119], v[148:151], v[212:215], v[116:119]
	v_mfma_f32_16x16x32_bf16 v[120:123], v[156:159], v[212:215], v[120:123]
	v_mfma_f32_16x16x32_bf16 v[124:127], v[148:151], v[220:223], v[124:127]
	v_mfma_f32_16x16x32_bf16 v[128:131], v[156:159], v[220:223], v[128:131]
	v_mfma_f32_16x16x32_bf16 v[16:19], v[152:155], v[184:187], v[16:19]
	v_mfma_f32_16x16x32_bf16 v[12:15], v[160:163], v[184:187], v[12:15]
	v_mfma_f32_16x16x32_bf16 v[8:11], v[152:155], v[196:199], v[8:11]
	v_mfma_f32_16x16x32_bf16 v[2:5], v[160:163], v[196:199], v[2:5]
	v_mfma_f32_16x16x32_bf16 v[116:119], v[152:155], v[216:219], v[116:119]
	v_mfma_f32_16x16x32_bf16 v[120:123], v[160:163], v[216:219], v[120:123]
	v_mfma_f32_16x16x32_bf16 v[124:127], v[152:155], v[224:227], v[124:127]
	s_barrier
	v_mfma_f32_16x16x32_bf16 v[128:131], v[160:163], v[224:227], v[128:131]
	s_setprio 0
	v_add_u32_e32 v0, s54, v188
	ds_read_b128 v[132:135], v0
	ds_read_b128 v[136:139], v0 offset:1024
	ds_read_b128 v[140:143], v0 offset:2048
	ds_read_b128 v[144:147], v0 offset:3072
	v_add_u32_e32 v0, s59, v188
	ds_read_b128 v[148:151], v0
	ds_read_b128 v[152:155], v0 offset:1024
	ds_read_b128 v[156:159], v0 offset:2048
	ds_read_b128 v[160:163], v0 offset:3072
	s_add_u32 s30, s30, s38
	s_addc_u32 s31, s31, 0
	s_mov_b32 m0, s47
	ds_read_b128 v[180:183], v190 offset:32768
	ds_read_b128 v[184:187], v190 offset:33792
	ds_read_b128 v[192:195], v190 offset:34816
	ds_read_b128 v[196:199], v190 offset:35840
	ds_read_b128 v[212:215], v190 offset:36864
	ds_read_b128 v[216:219], v190 offset:37888
	ds_read_b128 v[220:223], v190 offset:38912
	ds_read_b128 v[224:227], v190 offset:39936
	global_load_lds_dwordx4 v172, s[30:31]
	s_mov_b32 m0, s48
	s_nop 0
	global_load_lds_dwordx4 v176, s[30:31]
	s_waitcnt vmcnt(8)
	s_waitcnt lgkmcnt(0)
	s_barrier
	s_setprio 1
	s_waitcnt lgkmcnt(0)
	v_mfma_f32_16x16x32_bf16 v[112:115], v[132:135], v[180:183], v[112:115]
	v_mfma_f32_16x16x32_bf16 v[108:111], v[140:143], v[180:183], v[108:111]
	v_mfma_f32_16x16x32_bf16 v[104:107], v[132:135], v[192:195], v[104:107]
	v_mfma_f32_16x16x32_bf16 v[100:103], v[140:143], v[192:195], v[100:103]
	v_mfma_f32_16x16x32_bf16 v[96:99], v[132:135], v[212:215], v[96:99]
	v_mfma_f32_16x16x32_bf16 v[92:95], v[140:143], v[212:215], v[92:95]
	v_mfma_f32_16x16x32_bf16 v[88:91], v[132:135], v[220:223], v[88:91]
	v_mfma_f32_16x16x32_bf16 v[84:87], v[140:143], v[220:223], v[84:87]
	v_mfma_f32_16x16x32_bf16 v[112:115], v[136:139], v[184:187], v[112:115]
	v_mfma_f32_16x16x32_bf16 v[108:111], v[144:147], v[184:187], v[108:111]
	v_mfma_f32_16x16x32_bf16 v[104:107], v[136:139], v[196:199], v[104:107]
	v_mfma_f32_16x16x32_bf16 v[100:103], v[144:147], v[196:199], v[100:103]
	v_mfma_f32_16x16x32_bf16 v[96:99], v[136:139], v[216:219], v[96:99]
	v_mfma_f32_16x16x32_bf16 v[92:95], v[144:147], v[216:219], v[92:95]
	v_mfma_f32_16x16x32_bf16 v[88:91], v[136:139], v[224:227], v[88:91]
	v_mfma_f32_16x16x32_bf16 v[84:87], v[144:147], v[224:227], v[84:87]
	s_setprio 0
	s_setprio 1
	v_mfma_f32_16x16x32_bf16 v[80:83], v[148:151], v[180:183], v[80:83]
	v_mfma_f32_16x16x32_bf16 v[76:79], v[156:159], v[180:183], v[76:79]
	v_mfma_f32_16x16x32_bf16 v[72:75], v[148:151], v[192:195], v[72:75]
	v_mfma_f32_16x16x32_bf16 v[68:71], v[156:159], v[192:195], v[68:71]
	v_mfma_f32_16x16x32_bf16 v[64:67], v[148:151], v[212:215], v[64:67]
	v_mfma_f32_16x16x32_bf16 v[60:63], v[156:159], v[212:215], v[60:63]
	v_mfma_f32_16x16x32_bf16 v[56:59], v[148:151], v[220:223], v[56:59]
	v_mfma_f32_16x16x32_bf16 v[48:51], v[156:159], v[220:223], v[48:51]
	v_mfma_f32_16x16x32_bf16 v[80:83], v[152:155], v[184:187], v[80:83]
	v_mfma_f32_16x16x32_bf16 v[76:79], v[160:163], v[184:187], v[76:79]
	v_mfma_f32_16x16x32_bf16 v[72:75], v[152:155], v[196:199], v[72:75]
	v_mfma_f32_16x16x32_bf16 v[68:71], v[160:163], v[196:199], v[68:71]
	v_mfma_f32_16x16x32_bf16 v[64:67], v[152:155], v[216:219], v[64:67]
	v_mfma_f32_16x16x32_bf16 v[60:63], v[160:163], v[216:219], v[60:63]
	v_mfma_f32_16x16x32_bf16 v[56:59], v[152:155], v[224:227], v[56:59]
	s_barrier
	v_mfma_f32_16x16x32_bf16 v[48:51], v[160:163], v[224:227], v[48:51]
	s_setprio 0
	s_add_u32 s28, s28, s52
	s_addc_u32 s29, s29, 0
	s_mov_b32 m0, s55
	ds_read_b128 v[180:183], v190 offset:49152
	ds_read_b128 v[184:187], v190 offset:50176
	ds_read_b128 v[192:195], v190 offset:51200
	ds_read_b128 v[196:199], v190 offset:52224
	ds_read_b128 v[212:215], v190 offset:53248
	ds_read_b128 v[216:219], v190 offset:54272
	ds_read_b128 v[220:223], v190 offset:55296
	ds_read_b128 v[224:227], v190 offset:56320
	global_load_lds_dwordx4 v174, s[28:29]
	v_lshl_add_u64 v[6:7], s[28:29], 0, v[178:179]
	s_add_u32 s28, s28, s38
	s_mov_b32 m0, s56
	s_addc_u32 s29, s29, 0
	global_load_lds_dwordx4 v[6:7], off
	s_mov_b32 m0, s60
	s_nop 0
	global_load_lds_dwordx4 v174, s[28:29]
	s_mov_b32 m0, s62
	s_nop 0
	global_load_lds_dwordx4 v178, s[28:29]
	s_mov_b32 m0, s57
	s_nop 0
	global_load_lds_dwordx4 v172, s[4:5]
	s_mov_b32 m0, s58
	s_nop 0
	global_load_lds_dwordx4 v176, s[4:5]
	s_waitcnt vmcnt(8)
	s_waitcnt lgkmcnt(0)
	s_barrier
	s_setprio 1
	s_waitcnt lgkmcnt(0)
	v_mfma_f32_16x16x32_bf16 v[52:55], v[132:135], v[180:183], v[52:55]
	v_mfma_f32_16x16x32_bf16 v[44:47], v[140:143], v[180:183], v[44:47]
	v_mfma_f32_16x16x32_bf16 v[40:43], v[132:135], v[192:195], v[40:43]
	v_mfma_f32_16x16x32_bf16 v[36:39], v[140:143], v[192:195], v[36:39]
	v_mfma_f32_16x16x32_bf16 v[32:35], v[132:135], v[212:215], v[32:35]
	v_mfma_f32_16x16x32_bf16 v[28:31], v[140:143], v[212:215], v[28:31]
	v_mfma_f32_16x16x32_bf16 v[24:27], v[132:135], v[220:223], v[24:27]
	v_mfma_f32_16x16x32_bf16 v[20:23], v[140:143], v[220:223], v[20:23]
	v_mfma_f32_16x16x32_bf16 v[52:55], v[136:139], v[184:187], v[52:55]
	v_mfma_f32_16x16x32_bf16 v[44:47], v[144:147], v[184:187], v[44:47]
	v_mfma_f32_16x16x32_bf16 v[40:43], v[136:139], v[196:199], v[40:43]
	v_mfma_f32_16x16x32_bf16 v[36:39], v[144:147], v[196:199], v[36:39]
	v_mfma_f32_16x16x32_bf16 v[32:35], v[136:139], v[216:219], v[32:35]
	v_mfma_f32_16x16x32_bf16 v[28:31], v[144:147], v[216:219], v[28:31]
	v_mfma_f32_16x16x32_bf16 v[24:27], v[136:139], v[224:227], v[24:27]
	v_mfma_f32_16x16x32_bf16 v[20:23], v[144:147], v[224:227], v[20:23]
	s_setprio 0
	s_setprio 1
	v_mfma_f32_16x16x32_bf16 v[16:19], v[148:151], v[180:183], v[16:19]
	v_mfma_f32_16x16x32_bf16 v[12:15], v[156:159], v[180:183], v[12:15]
	v_mfma_f32_16x16x32_bf16 v[6:9], v[148:151], v[192:195], v[8:11]
	v_mfma_f32_16x16x32_bf16 v[2:5], v[156:159], v[192:195], v[2:5]
	v_mfma_f32_16x16x32_bf16 v[116:119], v[148:151], v[212:215], v[116:119]
	v_mfma_f32_16x16x32_bf16 v[120:123], v[156:159], v[212:215], v[120:123]
	v_mfma_f32_16x16x32_bf16 v[124:127], v[148:151], v[220:223], v[124:127]
	v_mfma_f32_16x16x32_bf16 v[128:131], v[156:159], v[220:223], v[128:131]
	v_mfma_f32_16x16x32_bf16 v[16:19], v[152:155], v[184:187], v[16:19]
	v_mfma_f32_16x16x32_bf16 v[12:15], v[160:163], v[184:187], v[12:15]
	v_mfma_f32_16x16x32_bf16 v[8:11], v[152:155], v[196:199], v[6:9]
	v_mfma_f32_16x16x32_bf16 v[4:7], v[160:163], v[196:199], v[2:5]
	v_mfma_f32_16x16x32_bf16 v[116:119], v[152:155], v[216:219], v[116:119]
	v_mfma_f32_16x16x32_bf16 v[120:123], v[160:163], v[216:219], v[120:123]
	v_mfma_f32_16x16x32_bf16 v[124:127], v[152:155], v[224:227], v[124:127]
	s_barrier
	v_mfma_f32_16x16x32_bf16 v[128:131], v[160:163], v[224:227], v[128:131]
	s_setprio 0
	s_add_i32 s74, s74, 2
	s_cmp_ge_i32 s74, s50
	s_cbranch_scc0 .LBB0_1216

.LBB0_1464:
	s_add_i32 s30, s6, s78
	s_add_i32 s28, s30, 1
	s_cmp_ge_i32 s28, s52
	s_cselect_b32 s29, s52, 0
	s_sub_i32 s28, s28, s29
	s_ashr_i32 s29, s28, 31
	s_lshl_b64 s[80:81], s[28:29], s42
	s_add_i32 s30, s30, 2
	s_cmp_ge_i32 s30, s52
	s_cselect_b32 s28, s52, 0
	s_sub_i32 s28, s30, s28
	s_ashr_i32 s29, s28, 31
	s_lshl_b64 s[28:29], s[28:29], s42
	v_add_u32_e32 v142, s7, v187
	v_add_u32_e32 v158, s45, v187
	s_add_u32 s30, s4, s28
	ds_read_b128 v[130:133], v142
	ds_read_b128 v[134:137], v142 offset:1024
	ds_read_b128 v[138:141], v142 offset:2048
	ds_read_b128 v[142:145], v142 offset:3072
	ds_read_b128 v[146:149], v158
	ds_read_b128 v[150:153], v158 offset:1024
	ds_read_b128 v[154:157], v158 offset:2048
	ds_read_b128 v[158:161], v158 offset:3072
	s_addc_u32 s31, s5, s29
	s_add_u32 s28, s26, s28
	s_addc_u32 s29, s27, s29
	s_cmp_eq_u32 s53, s78
	s_cselect_b32 s34, s74, s30
	s_cselect_b32 s35, s75, s31
	s_cselect_b32 s31, s77, s29
	s_cselect_b32 s30, s76, s28
	s_add_u32 s28, s34, s54
	s_addc_u32 s29, s35, 0
	s_add_u32 s80, s72, s80
	s_addc_u32 s81, s73, s81
	s_add_i32 m0, s48, 0xc000
	ds_read_b128 v[172:175], v189
	ds_read_b128 v[176:179], v189 offset:1024
	ds_read_b128 v[180:183], v189 offset:2048
	ds_read_b128 v[190:193], v189 offset:3072
	ds_read_b128 v[194:197], v189 offset:4096
	ds_read_b128 v[212:215], v189 offset:5120
	ds_read_b128 v[216:219], v189 offset:6144
	ds_read_b128 v[220:223], v189 offset:7168
	global_load_lds_dwordx4 v0, s[80:81]
	s_add_i32 m0, s48, 0xe000
	s_nop 0
	global_load_lds_dwordx4 v162, s[80:81]
	s_waitcnt vmcnt(8)
	s_waitcnt lgkmcnt(0)
	s_barrier
	s_setprio 1
	s_waitcnt lgkmcnt(0)
	v_mfma_f32_16x16x32_bf16 v[126:129], v[130:133], v[172:175], v[126:129]
	v_mfma_f32_16x16x32_bf16 v[122:125], v[138:141], v[172:175], v[122:125]
	v_mfma_f32_16x16x32_bf16 v[110:113], v[130:133], v[180:183], v[110:113]
	v_mfma_f32_16x16x32_bf16 v[106:109], v[138:141], v[180:183], v[106:109]
	v_mfma_f32_16x16x32_bf16 v[94:97], v[130:133], v[194:197], v[94:97]
	v_mfma_f32_16x16x32_bf16 v[90:93], v[138:141], v[194:197], v[90:93]
	v_mfma_f32_16x16x32_bf16 v[78:81], v[130:133], v[216:219], v[78:81]
	v_mfma_f32_16x16x32_bf16 v[74:77], v[138:141], v[216:219], v[74:77]
	v_mfma_f32_16x16x32_bf16 v[126:129], v[134:137], v[176:179], v[126:129]
	v_mfma_f32_16x16x32_bf16 v[122:125], v[142:145], v[176:179], v[122:125]
	v_mfma_f32_16x16x32_bf16 v[110:113], v[134:137], v[190:193], v[110:113]
	v_mfma_f32_16x16x32_bf16 v[106:109], v[142:145], v[190:193], v[106:109]
	v_mfma_f32_16x16x32_bf16 v[94:97], v[134:137], v[212:215], v[94:97]
	v_mfma_f32_16x16x32_bf16 v[90:93], v[142:145], v[212:215], v[90:93]
	v_mfma_f32_16x16x32_bf16 v[78:81], v[134:137], v[220:223], v[78:81]
	v_mfma_f32_16x16x32_bf16 v[74:77], v[142:145], v[220:223], v[74:77]
	s_setprio 0
	s_setprio 1
	v_mfma_f32_16x16x32_bf16 v[118:121], v[146:149], v[172:175], v[118:121]
	v_mfma_f32_16x16x32_bf16 v[114:117], v[154:157], v[172:175], v[114:117]
	v_mfma_f32_16x16x32_bf16 v[102:105], v[146:149], v[180:183], v[102:105]
	v_mfma_f32_16x16x32_bf16 v[98:101], v[154:157], v[180:183], v[98:101]
	v_mfma_f32_16x16x32_bf16 v[86:89], v[146:149], v[194:197], v[86:89]
	v_mfma_f32_16x16x32_bf16 v[82:85], v[154:157], v[194:197], v[82:85]
	v_mfma_f32_16x16x32_bf16 v[70:73], v[146:149], v[216:219], v[70:73]
	v_mfma_f32_16x16x32_bf16 v[66:69], v[154:157], v[216:219], v[66:69]
	v_mfma_f32_16x16x32_bf16 v[118:121], v[150:153], v[176:179], v[118:121]
	v_mfma_f32_16x16x32_bf16 v[114:117], v[158:161], v[176:179], v[114:117]
	v_mfma_f32_16x16x32_bf16 v[102:105], v[150:153], v[190:193], v[102:105]
	v_mfma_f32_16x16x32_bf16 v[98:101], v[158:161], v[190:193], v[98:101]
	v_mfma_f32_16x16x32_bf16 v[86:89], v[150:153], v[212:215], v[86:89]
	v_mfma_f32_16x16x32_bf16 v[82:85], v[158:161], v[212:215], v[82:85]
	v_mfma_f32_16x16x32_bf16 v[70:73], v[150:153], v[220:223], v[70:73]
	s_barrier
	v_mfma_f32_16x16x32_bf16 v[66:69], v[158:161], v[220:223], v[66:69]
	s_setprio 0
	s_mov_b32 m0, s43
	s_add_u32 s80, s30, s41
	ds_read_b128 v[172:175], v189 offset:16384
	ds_read_b128 v[176:179], v189 offset:17408
	ds_read_b128 v[180:183], v189 offset:18432
	ds_read_b128 v[190:193], v189 offset:19456
	ds_read_b128 v[194:197], v189 offset:20480
	ds_read_b128 v[212:215], v189 offset:21504
	ds_read_b128 v[216:219], v189 offset:22528
	ds_read_b128 v[220:223], v189 offset:23552
	global_load_lds_dwordx4 v0, s[30:31]
	s_mov_b32 m0, s44
	s_addc_u32 s81, s31, 0
	global_load_lds_dwordx4 v162, s[30:31]
	s_mov_b32 m0, s46
	s_nop 0
	global_load_lds_dwordx4 v0, s[80:81]
	s_mov_b32 m0, s47
	s_nop 0
	global_load_lds_dwordx4 v162, s[80:81]
	s_mov_b32 m0, s48
	s_nop 0
	global_load_lds_dwordx4 v0, s[34:35]
	s_mov_b32 m0, s49
	s_nop 0
	global_load_lds_dwordx4 v162, s[34:35]
	s_waitcnt vmcnt(8)
	s_waitcnt lgkmcnt(0)
	s_barrier
	s_setprio 1
	s_waitcnt lgkmcnt(0)
	v_mfma_f32_16x16x32_bf16 v[62:65], v[130:133], v[172:175], v[62:65]
	v_mfma_f32_16x16x32_bf16 v[58:61], v[138:141], v[172:175], v[58:61]
	v_mfma_f32_16x16x32_bf16 v[46:49], v[130:133], v[180:183], v[46:49]
	v_mfma_f32_16x16x32_bf16 v[42:45], v[138:141], v[180:183], v[42:45]
	v_mfma_f32_16x16x32_bf16 v[30:33], v[130:133], v[194:197], v[30:33]
	v_mfma_f32_16x16x32_bf16 v[26:29], v[138:141], v[194:197], v[26:29]
	v_mfma_f32_16x16x32_bf16 v[14:17], v[130:133], v[216:219], v[14:17]
	v_mfma_f32_16x16x32_bf16 v[10:13], v[138:141], v[216:219], v[10:13]
	v_mfma_f32_16x16x32_bf16 v[62:65], v[134:137], v[176:179], v[62:65]
	v_mfma_f32_16x16x32_bf16 v[58:61], v[142:145], v[176:179], v[58:61]
	v_mfma_f32_16x16x32_bf16 v[46:49], v[134:137], v[190:193], v[46:49]
	v_mfma_f32_16x16x32_bf16 v[42:45], v[142:145], v[190:193], v[42:45]
	v_mfma_f32_16x16x32_bf16 v[30:33], v[134:137], v[212:215], v[30:33]
	v_mfma_f32_16x16x32_bf16 v[26:29], v[142:145], v[212:215], v[26:29]
	v_mfma_f32_16x16x32_bf16 v[14:17], v[134:137], v[220:223], v[14:17]
	v_mfma_f32_16x16x32_bf16 v[10:13], v[142:145], v[220:223], v[10:13]
	s_setprio 0
	s_setprio 1
	v_mfma_f32_16x16x32_bf16 v[54:57], v[146:149], v[172:175], v[54:57]
	v_mfma_f32_16x16x32_bf16 v[50:53], v[154:157], v[172:175], v[50:53]
	v_mfma_f32_16x16x32_bf16 v[38:41], v[146:149], v[180:183], v[38:41]
	v_mfma_f32_16x16x32_bf16 v[34:37], v[154:157], v[180:183], v[34:37]
	v_mfma_f32_16x16x32_bf16 v[22:25], v[146:149], v[194:197], v[22:25]
	v_mfma_f32_16x16x32_bf16 v[18:21], v[154:157], v[194:197], v[18:21]
	v_mfma_f32_16x16x32_bf16 v[6:9], v[146:149], v[216:219], v[6:9]
	v_mfma_f32_16x16x32_bf16 v[2:5], v[154:157], v[216:219], v[2:5]
	v_mfma_f32_16x16x32_bf16 v[54:57], v[150:153], v[176:179], v[54:57]
	v_mfma_f32_16x16x32_bf16 v[50:53], v[158:161], v[176:179], v[50:53]
	v_mfma_f32_16x16x32_bf16 v[38:41], v[150:153], v[190:193], v[38:41]
	v_mfma_f32_16x16x32_bf16 v[34:37], v[158:161], v[190:193], v[34:37]
	v_mfma_f32_16x16x32_bf16 v[22:25], v[150:153], v[212:215], v[22:25]
	v_mfma_f32_16x16x32_bf16 v[18:21], v[158:161], v[212:215], v[18:21]
	v_mfma_f32_16x16x32_bf16 v[6:9], v[150:153], v[220:223], v[6:9]
	s_barrier
	v_mfma_f32_16x16x32_bf16 v[2:5], v[158:161], v[220:223], v[2:5]
	s_setprio 0
	v_add_u32_e32 v142, s56, v187
	v_add_u32_e32 v158, s62, v187
	ds_read_b128 v[130:133], v142
	ds_read_b128 v[134:137], v142 offset:1024
	ds_read_b128 v[138:141], v142 offset:2048
	ds_read_b128 v[142:145], v142 offset:3072
	ds_read_b128 v[146:149], v158
	ds_read_b128 v[150:153], v158 offset:1024
	ds_read_b128 v[154:157], v158 offset:2048
	ds_read_b128 v[158:161], v158 offset:3072
	s_add_u32 s34, s34, s41
	s_addc_u32 s35, s35, 0
	s_mov_b32 m0, s50
	ds_read_b128 v[172:175], v189 offset:32768
	ds_read_b128 v[176:179], v189 offset:33792
	ds_read_b128 v[180:183], v189 offset:34816
	ds_read_b128 v[190:193], v189 offset:35840
	ds_read_b128 v[194:197], v189 offset:36864
	ds_read_b128 v[212:215], v189 offset:37888
	ds_read_b128 v[216:219], v189 offset:38912
	ds_read_b128 v[220:223], v189 offset:39936
	global_load_lds_dwordx4 v0, s[34:35]
	s_mov_b32 m0, s51
	s_nop 0
	global_load_lds_dwordx4 v162, s[34:35]
	s_waitcnt vmcnt(8)
	s_waitcnt lgkmcnt(0)
	s_barrier
	s_setprio 1
	s_waitcnt lgkmcnt(0)
	v_mfma_f32_16x16x32_bf16 v[126:129], v[130:133], v[172:175], v[126:129]
	v_mfma_f32_16x16x32_bf16 v[122:125], v[138:141], v[172:175], v[122:125]
	v_mfma_f32_16x16x32_bf16 v[110:113], v[130:133], v[180:183], v[110:113]
	v_mfma_f32_16x16x32_bf16 v[106:109], v[138:141], v[180:183], v[106:109]
	v_mfma_f32_16x16x32_bf16 v[94:97], v[130:133], v[194:197], v[94:97]
	v_mfma_f32_16x16x32_bf16 v[90:93], v[138:141], v[194:197], v[90:93]
	v_mfma_f32_16x16x32_bf16 v[78:81], v[130:133], v[216:219], v[78:81]
	v_mfma_f32_16x16x32_bf16 v[74:77], v[138:141], v[216:219], v[74:77]
	v_mfma_f32_16x16x32_bf16 v[126:129], v[134:137], v[176:179], v[126:129]
	v_mfma_f32_16x16x32_bf16 v[122:125], v[142:145], v[176:179], v[122:125]
	v_mfma_f32_16x16x32_bf16 v[110:113], v[134:137], v[190:193], v[110:113]
	v_mfma_f32_16x16x32_bf16 v[106:109], v[142:145], v[190:193], v[106:109]
	v_mfma_f32_16x16x32_bf16 v[94:97], v[134:137], v[212:215], v[94:97]
	v_mfma_f32_16x16x32_bf16 v[90:93], v[142:145], v[212:215], v[90:93]
	v_mfma_f32_16x16x32_bf16 v[78:81], v[134:137], v[220:223], v[78:81]
	v_mfma_f32_16x16x32_bf16 v[74:77], v[142:145], v[220:223], v[74:77]
	s_setprio 0
	s_setprio 1
	v_mfma_f32_16x16x32_bf16 v[118:121], v[146:149], v[172:175], v[118:121]
	v_mfma_f32_16x16x32_bf16 v[114:117], v[154:157], v[172:175], v[114:117]
	v_mfma_f32_16x16x32_bf16 v[102:105], v[146:149], v[180:183], v[102:105]
	v_mfma_f32_16x16x32_bf16 v[98:101], v[154:157], v[180:183], v[98:101]
	v_mfma_f32_16x16x32_bf16 v[86:89], v[146:149], v[194:197], v[86:89]
	v_mfma_f32_16x16x32_bf16 v[82:85], v[154:157], v[194:197], v[82:85]
	v_mfma_f32_16x16x32_bf16 v[70:73], v[146:149], v[216:219], v[70:73]
	v_mfma_f32_16x16x32_bf16 v[66:69], v[154:157], v[216:219], v[66:69]
	v_mfma_f32_16x16x32_bf16 v[118:121], v[150:153], v[176:179], v[118:121]
	v_mfma_f32_16x16x32_bf16 v[114:117], v[158:161], v[176:179], v[114:117]
	v_mfma_f32_16x16x32_bf16 v[102:105], v[150:153], v[190:193], v[102:105]
	v_mfma_f32_16x16x32_bf16 v[98:101], v[158:161], v[190:193], v[98:101]
	v_mfma_f32_16x16x32_bf16 v[86:89], v[150:153], v[212:215], v[86:89]
	v_mfma_f32_16x16x32_bf16 v[82:85], v[158:161], v[212:215], v[82:85]
	v_mfma_f32_16x16x32_bf16 v[70:73], v[150:153], v[220:223], v[70:73]
	s_barrier
	v_mfma_f32_16x16x32_bf16 v[66:69], v[158:161], v[220:223], v[66:69]
	s_setprio 0
	s_add_u32 s30, s30, s54
	s_addc_u32 s31, s31, 0
	s_mov_b32 m0, s57
	ds_read_b128 v[172:175], v189 offset:49152
	ds_read_b128 v[176:179], v189 offset:50176
	ds_read_b128 v[180:183], v189 offset:51200
	ds_read_b128 v[190:193], v189 offset:52224
	ds_read_b128 v[194:197], v189 offset:53248
	ds_read_b128 v[212:215], v189 offset:54272
	ds_read_b128 v[216:219], v189 offset:55296
	ds_read_b128 v[220:223], v189 offset:56320
	global_load_lds_dwordx4 v0, s[30:31]
	v_lshl_add_u64 v[168:169], s[30:31], 0, v[162:163]
	s_add_u32 s30, s30, s41
	s_mov_b32 m0, s58
	s_addc_u32 s31, s31, 0
	global_load_lds_dwordx4 v[168:169], off
	s_mov_b32 m0, s63
	s_nop 0
	global_load_lds_dwordx4 v0, s[30:31]
	s_mov_b32 m0, s64
	s_nop 0
	global_load_lds_dwordx4 v162, s[30:31]
	s_mov_b32 m0, s59
	s_nop 0
	global_load_lds_dwordx4 v0, s[28:29]
	s_mov_b32 m0, s60
	s_nop 0
	global_load_lds_dwordx4 v162, s[28:29]
	s_waitcnt vmcnt(8)
	s_waitcnt lgkmcnt(0)
	s_barrier
	s_setprio 1
	s_waitcnt lgkmcnt(0)
	v_mfma_f32_16x16x32_bf16 v[62:65], v[130:133], v[172:175], v[62:65]
	v_mfma_f32_16x16x32_bf16 v[58:61], v[138:141], v[172:175], v[58:61]
	v_mfma_f32_16x16x32_bf16 v[46:49], v[130:133], v[180:183], v[46:49]
	v_mfma_f32_16x16x32_bf16 v[42:45], v[138:141], v[180:183], v[42:45]
	v_mfma_f32_16x16x32_bf16 v[30:33], v[130:133], v[194:197], v[30:33]
	v_mfma_f32_16x16x32_bf16 v[26:29], v[138:141], v[194:197], v[26:29]
	v_mfma_f32_16x16x32_bf16 v[14:17], v[130:133], v[216:219], v[14:17]
	v_mfma_f32_16x16x32_bf16 v[10:13], v[138:141], v[216:219], v[10:13]
	v_mfma_f32_16x16x32_bf16 v[62:65], v[134:137], v[176:179], v[62:65]
	v_mfma_f32_16x16x32_bf16 v[58:61], v[142:145], v[176:179], v[58:61]
	v_mfma_f32_16x16x32_bf16 v[46:49], v[134:137], v[190:193], v[46:49]
	v_mfma_f32_16x16x32_bf16 v[42:45], v[142:145], v[190:193], v[42:45]
	v_mfma_f32_16x16x32_bf16 v[30:33], v[134:137], v[212:215], v[30:33]
	v_mfma_f32_16x16x32_bf16 v[26:29], v[142:145], v[212:215], v[26:29]
	v_mfma_f32_16x16x32_bf16 v[14:17], v[134:137], v[220:223], v[14:17]
	v_mfma_f32_16x16x32_bf16 v[10:13], v[142:145], v[220:223], v[10:13]
	s_setprio 0
	s_setprio 1
	v_mfma_f32_16x16x32_bf16 v[54:57], v[146:149], v[172:175], v[54:57]
	v_mfma_f32_16x16x32_bf16 v[50:53], v[154:157], v[172:175], v[50:53]
	v_mfma_f32_16x16x32_bf16 v[38:41], v[146:149], v[180:183], v[38:41]
	v_mfma_f32_16x16x32_bf16 v[34:37], v[154:157], v[180:183], v[34:37]
	v_mfma_f32_16x16x32_bf16 v[22:25], v[146:149], v[194:197], v[22:25]
	v_mfma_f32_16x16x32_bf16 v[18:21], v[154:157], v[194:197], v[18:21]
	v_mfma_f32_16x16x32_bf16 v[6:9], v[146:149], v[216:219], v[6:9]
	v_mfma_f32_16x16x32_bf16 v[2:5], v[154:157], v[216:219], v[2:5]
	v_mfma_f32_16x16x32_bf16 v[54:57], v[150:153], v[176:179], v[54:57]
	v_mfma_f32_16x16x32_bf16 v[50:53], v[158:161], v[176:179], v[50:53]
	v_mfma_f32_16x16x32_bf16 v[38:41], v[150:153], v[190:193], v[38:41]
	v_mfma_f32_16x16x32_bf16 v[34:37], v[158:161], v[190:193], v[34:37]
	v_mfma_f32_16x16x32_bf16 v[22:25], v[150:153], v[212:215], v[22:25]
	v_mfma_f32_16x16x32_bf16 v[18:21], v[158:161], v[212:215], v[18:21]
	v_mfma_f32_16x16x32_bf16 v[6:9], v[150:153], v[220:223], v[6:9]
	s_barrier
	v_mfma_f32_16x16x32_bf16 v[2:5], v[158:161], v[220:223], v[2:5]
	s_setprio 0
	s_add_i32 s78, s78, 2
	s_cmp_ge_i32 s78, s52
	s_cbranch_scc0 .LBB0_1464

.LBB0_1983:
	s_add_i32 s3, s3, 1
	s_cmp_ge_i32 s3, s71
	s_cselect_b32 vcc_lo, s71, 0
	s_sub_i32 vcc_lo, s3, vcc_lo
	s_ashr_i32 vcc_hi, vcc_lo, 31
	v_add_u32_e32 v154, s1, v190
	s_lshl_b64 vcc, vcc, s75
	ds_read_b128 v[160:163], v154
	ds_read_b128 v[172:175], v154 offset:1024
	ds_read_b128 v[176:179], v154 offset:2048
	ds_read_b128 v[180:183], v154 offset:3072
	v_add_u32_e32 v154, s93, v190
	s_add_u32 vcc_lo, s65, vcc_lo
	ds_read_b128 v[196:199], v154
	ds_read_b128 v[212:215], v154 offset:1024
	ds_read_b128 v[216:219], v154 offset:2048
	ds_read_b128 v[220:223], v154 offset:3072
	s_addc_u32 vcc_hi, s66, vcc_hi
	s_and_b64 s[52:53], exec, s[52:53]
	s_cselect_b32 s52, s16, s54
	s_cselect_b32 s3, s17, s55
	s_add_u32 s54, s65, s52
	s_addc_u32 s55, s66, s3
	s_add_u32 s52, s54, s73
	s_addc_u32 s53, s55, 0
	s_add_i32 m0, s78, 0xc000
	ds_read_b128 v[224:227], v192
	ds_read_b128 v[228:231], v192 offset:1024
	ds_read_b128 v[232:235], v192 offset:2048
	ds_read_b128 v[236:239], v192 offset:3072
	ds_read_b128 v[240:243], v192 offset:4096
	ds_read_b128 v[244:247], v192 offset:5120
	ds_read_b128 v[248:251], v192 offset:6144
	ds_read_b128 v[168:171], v192 offset:7168
	global_load_lds_dwordx4 v0, vcc
	s_add_i32 m0, s78, 0xe000
	s_nop 0
	global_load_lds_dwordx4 v144, vcc
	s_waitcnt vmcnt(8)
	s_waitcnt lgkmcnt(0)
	s_barrier
	s_setprio 1
	s_waitcnt lgkmcnt(0)
	v_mfma_f32_16x16x32_bf16 v[122:125], v[160:163], v[224:227], v[122:125]
	v_mfma_f32_16x16x32_bf16 v[114:117], v[176:179], v[224:227], v[114:117]
	v_mfma_f32_16x16x32_bf16 v[106:109], v[160:163], v[232:235], v[106:109]
	v_mfma_f32_16x16x32_bf16 v[98:101], v[176:179], v[232:235], v[98:101]
	v_mfma_f32_16x16x32_bf16 v[90:93], v[160:163], v[240:243], v[90:93]
	v_mfma_f32_16x16x32_bf16 v[82:85], v[176:179], v[240:243], v[82:85]
	v_mfma_f32_16x16x32_bf16 v[74:77], v[160:163], v[248:251], v[74:77]
	v_mfma_f32_16x16x32_bf16 v[66:69], v[176:179], v[248:251], v[66:69]
	v_mfma_f32_16x16x32_bf16 v[122:125], v[172:175], v[228:231], v[122:125]
	v_mfma_f32_16x16x32_bf16 v[114:117], v[180:183], v[228:231], v[114:117]
	v_mfma_f32_16x16x32_bf16 v[106:109], v[172:175], v[236:239], v[106:109]
	v_mfma_f32_16x16x32_bf16 v[98:101], v[180:183], v[236:239], v[98:101]
	v_mfma_f32_16x16x32_bf16 v[90:93], v[172:175], v[244:247], v[90:93]
	v_mfma_f32_16x16x32_bf16 v[82:85], v[180:183], v[244:247], v[82:85]
	v_mfma_f32_16x16x32_bf16 v[74:77], v[172:175], v[168:171], v[74:77]
	v_mfma_f32_16x16x32_bf16 v[66:69], v[180:183], v[168:171], v[66:69]
	s_setprio 0
	s_setprio 1
	v_mfma_f32_16x16x32_bf16 v[126:129], v[196:199], v[224:227], v[126:129]
	v_mfma_f32_16x16x32_bf16 v[118:121], v[216:219], v[224:227], v[118:121]
	v_mfma_f32_16x16x32_bf16 v[110:113], v[196:199], v[232:235], v[110:113]
	v_mfma_f32_16x16x32_bf16 v[102:105], v[216:219], v[232:235], v[102:105]
	v_mfma_f32_16x16x32_bf16 v[94:97], v[196:199], v[240:243], v[94:97]
	v_mfma_f32_16x16x32_bf16 v[86:89], v[216:219], v[240:243], v[86:89]
	v_mfma_f32_16x16x32_bf16 v[78:81], v[196:199], v[248:251], v[78:81]
	v_mfma_f32_16x16x32_bf16 v[70:73], v[216:219], v[248:251], v[70:73]
	v_mfma_f32_16x16x32_bf16 v[126:129], v[212:215], v[228:231], v[126:129]
	v_mfma_f32_16x16x32_bf16 v[118:121], v[220:223], v[228:231], v[118:121]
	v_mfma_f32_16x16x32_bf16 v[110:113], v[212:215], v[236:239], v[110:113]
	v_mfma_f32_16x16x32_bf16 v[102:105], v[220:223], v[236:239], v[102:105]
	v_mfma_f32_16x16x32_bf16 v[94:97], v[212:215], v[244:247], v[94:97]
	v_mfma_f32_16x16x32_bf16 v[86:89], v[220:223], v[244:247], v[86:89]
	v_mfma_f32_16x16x32_bf16 v[78:81], v[212:215], v[168:171], v[78:81]
	s_barrier
	v_mfma_f32_16x16x32_bf16 v[70:73], v[220:223], v[168:171], v[70:73]
	s_setprio 0
	s_mov_b32 m0, s13
	s_add_u32 vcc_lo, s50, s74
	ds_read_b128 v[168:171], v192 offset:16384
	ds_read_b128 v[224:227], v192 offset:17408
	ds_read_b128 v[228:231], v192 offset:18432
	ds_read_b128 v[232:235], v192 offset:19456
	ds_read_b128 v[236:239], v192 offset:20480
	ds_read_b128 v[240:243], v192 offset:21504
	ds_read_b128 v[244:247], v192 offset:22528
	ds_read_b128 v[248:251], v192 offset:23552
	global_load_lds_dwordx4 v130, s[50:51]
	s_mov_b32 m0, s76
	s_addc_u32 vcc_hi, s51, 0
	global_load_lds_dwordx4 v132, s[50:51]
	s_mov_b32 m0, s79
	s_nop 0
	global_load_lds_dwordx4 v130, vcc
	s_mov_b32 m0, s77
	s_nop 0
	global_load_lds_dwordx4 v132, vcc
	s_mov_b32 m0, s78
	s_nop 0
	global_load_lds_dwordx4 v149, s[54:55]
	s_mov_b32 m0, s80
	s_nop 0
	global_load_lds_dwordx4 v147, s[54:55]
	s_waitcnt vmcnt(8)
	s_waitcnt lgkmcnt(0)
	s_barrier
	s_setprio 1
	s_waitcnt lgkmcnt(0)
	v_mfma_f32_16x16x32_bf16 v[58:61], v[160:163], v[168:171], v[58:61]
	v_mfma_f32_16x16x32_bf16 v[50:53], v[176:179], v[168:171], v[50:53]
	v_mfma_f32_16x16x32_bf16 v[42:45], v[160:163], v[228:231], v[42:45]
	v_mfma_f32_16x16x32_bf16 v[38:41], v[176:179], v[228:231], v[38:41]
	v_mfma_f32_16x16x32_bf16 v[26:29], v[160:163], v[236:239], v[26:29]
	v_mfma_f32_16x16x32_bf16 v[18:21], v[176:179], v[236:239], v[18:21]
	v_mfma_f32_16x16x32_bf16 v[10:13], v[160:163], v[244:247], v[10:13]
	v_mfma_f32_16x16x32_bf16 v[6:9], v[176:179], v[244:247], v[6:9]
	v_mfma_f32_16x16x32_bf16 v[58:61], v[172:175], v[224:227], v[58:61]
	v_mfma_f32_16x16x32_bf16 v[50:53], v[180:183], v[224:227], v[50:53]
	v_mfma_f32_16x16x32_bf16 v[42:45], v[172:175], v[232:235], v[42:45]
	v_mfma_f32_16x16x32_bf16 v[38:41], v[180:183], v[232:235], v[38:41]
	v_mfma_f32_16x16x32_bf16 v[26:29], v[172:175], v[240:243], v[26:29]
	v_mfma_f32_16x16x32_bf16 v[18:21], v[180:183], v[240:243], v[18:21]
	v_mfma_f32_16x16x32_bf16 v[10:13], v[172:175], v[248:251], v[10:13]
	v_mfma_f32_16x16x32_bf16 v[6:9], v[180:183], v[248:251], v[6:9]
	s_setprio 0
	s_setprio 1
	v_mfma_f32_16x16x32_bf16 v[62:65], v[196:199], v[168:171], v[62:65]
	v_mfma_f32_16x16x32_bf16 v[54:57], v[216:219], v[168:171], v[54:57]
	v_mfma_f32_16x16x32_bf16 v[46:49], v[196:199], v[228:231], v[46:49]
	v_mfma_f32_16x16x32_bf16 v[34:37], v[216:219], v[228:231], v[34:37]
	v_mfma_f32_16x16x32_bf16 v[30:33], v[196:199], v[236:239], v[30:33]
	v_mfma_f32_16x16x32_bf16 v[22:25], v[216:219], v[236:239], v[22:25]
	v_mfma_f32_16x16x32_bf16 v[14:17], v[196:199], v[244:247], v[14:17]
	v_mfma_f32_16x16x32_bf16 v[2:5], v[216:219], v[244:247], v[2:5]
	v_mfma_f32_16x16x32_bf16 v[62:65], v[212:215], v[224:227], v[62:65]
	v_mfma_f32_16x16x32_bf16 v[54:57], v[220:223], v[224:227], v[54:57]
	v_mfma_f32_16x16x32_bf16 v[46:49], v[212:215], v[232:235], v[46:49]
	v_mfma_f32_16x16x32_bf16 v[34:37], v[220:223], v[232:235], v[34:37]
	v_mfma_f32_16x16x32_bf16 v[30:33], v[212:215], v[240:243], v[30:33]
	v_mfma_f32_16x16x32_bf16 v[22:25], v[220:223], v[240:243], v[22:25]
	v_mfma_f32_16x16x32_bf16 v[14:17], v[212:215], v[248:251], v[14:17]
	s_barrier
	v_mfma_f32_16x16x32_bf16 v[2:5], v[220:223], v[248:251], v[2:5]
	s_setprio 0
	v_add_u32_e32 v154, s94, v190
	ds_read_b128 v[160:163], v154
	ds_read_b128 v[168:171], v154 offset:1024
	ds_read_b128 v[172:175], v154 offset:2048
	ds_read_b128 v[176:179], v154 offset:3072
	v_add_u32_e32 v154, s95, v190
	ds_read_b128 v[180:183], v154
	ds_read_b128 v[196:199], v154 offset:1024
	ds_read_b128 v[212:215], v154 offset:2048
	ds_read_b128 v[216:219], v154 offset:3072
	s_mov_b32 m0, s81
	ds_read_b128 v[220:223], v192 offset:32768
	ds_read_b128 v[224:227], v192 offset:33792
	ds_read_b128 v[228:231], v192 offset:34816
	ds_read_b128 v[232:235], v192 offset:35840
	ds_read_b128 v[236:239], v192 offset:36864
	ds_read_b128 v[240:243], v192 offset:37888
	ds_read_b128 v[244:247], v192 offset:38912
	ds_read_b128 v[248:251], v192 offset:39936
	global_load_lds_dwordx4 v152, s[54:55]
	s_mov_b32 m0, s82
	s_nop 0
	global_load_lds_dwordx4 v150, s[54:55]
	s_waitcnt vmcnt(8)
	s_waitcnt lgkmcnt(0)
	s_barrier
	s_setprio 1
	s_waitcnt lgkmcnt(0)
	v_mfma_f32_16x16x32_bf16 v[122:125], v[160:163], v[220:223], v[122:125]
	v_mfma_f32_16x16x32_bf16 v[114:117], v[172:175], v[220:223], v[114:117]
	v_mfma_f32_16x16x32_bf16 v[106:109], v[160:163], v[228:231], v[106:109]
	v_mfma_f32_16x16x32_bf16 v[98:101], v[172:175], v[228:231], v[98:101]
	v_mfma_f32_16x16x32_bf16 v[90:93], v[160:163], v[236:239], v[90:93]
	v_mfma_f32_16x16x32_bf16 v[82:85], v[172:175], v[236:239], v[82:85]
	v_mfma_f32_16x16x32_bf16 v[74:77], v[160:163], v[244:247], v[74:77]
	v_mfma_f32_16x16x32_bf16 v[66:69], v[172:175], v[244:247], v[66:69]
	v_mfma_f32_16x16x32_bf16 v[122:125], v[168:171], v[224:227], v[122:125]
	v_mfma_f32_16x16x32_bf16 v[114:117], v[176:179], v[224:227], v[114:117]
	v_mfma_f32_16x16x32_bf16 v[106:109], v[168:171], v[232:235], v[106:109]
	v_mfma_f32_16x16x32_bf16 v[98:101], v[176:179], v[232:235], v[98:101]
	v_mfma_f32_16x16x32_bf16 v[90:93], v[168:171], v[240:243], v[90:93]
	v_mfma_f32_16x16x32_bf16 v[82:85], v[176:179], v[240:243], v[82:85]
	v_mfma_f32_16x16x32_bf16 v[74:77], v[168:171], v[248:251], v[74:77]
	v_mfma_f32_16x16x32_bf16 v[66:69], v[176:179], v[248:251], v[66:69]
	s_setprio 0
	s_setprio 1
	v_mfma_f32_16x16x32_bf16 v[126:129], v[180:183], v[220:223], v[126:129]
	v_mfma_f32_16x16x32_bf16 v[118:121], v[212:215], v[220:223], v[118:121]
	v_mfma_f32_16x16x32_bf16 v[110:113], v[180:183], v[228:231], v[110:113]
	v_mfma_f32_16x16x32_bf16 v[102:105], v[212:215], v[228:231], v[102:105]
	v_mfma_f32_16x16x32_bf16 v[94:97], v[180:183], v[236:239], v[94:97]
	v_mfma_f32_16x16x32_bf16 v[86:89], v[212:215], v[236:239], v[86:89]
	v_mfma_f32_16x16x32_bf16 v[78:81], v[180:183], v[244:247], v[78:81]
	v_mfma_f32_16x16x32_bf16 v[70:73], v[212:215], v[244:247], v[70:73]
	v_mfma_f32_16x16x32_bf16 v[126:129], v[196:199], v[224:227], v[126:129]
	v_mfma_f32_16x16x32_bf16 v[118:121], v[216:219], v[224:227], v[118:121]
	v_mfma_f32_16x16x32_bf16 v[110:113], v[196:199], v[232:235], v[110:113]
	v_mfma_f32_16x16x32_bf16 v[102:105], v[216:219], v[232:235], v[102:105]
	v_mfma_f32_16x16x32_bf16 v[94:97], v[196:199], v[240:243], v[94:97]
	v_mfma_f32_16x16x32_bf16 v[86:89], v[216:219], v[240:243], v[86:89]
	v_mfma_f32_16x16x32_bf16 v[78:81], v[196:199], v[248:251], v[78:81]
	s_barrier
	v_mfma_f32_16x16x32_bf16 v[70:73], v[216:219], v[248:251], v[70:73]
	s_setprio 0
	s_add_u32 s50, s50, s73
	s_addc_u32 s51, s51, 0
	s_mov_b32 m0, s60
	ds_read_b128 v[150:153], v192 offset:49152
	ds_read_b128 v[220:223], v192 offset:50176
	ds_read_b128 v[224:227], v192 offset:51200
	ds_read_b128 v[228:231], v192 offset:52224
	ds_read_b128 v[232:235], v192 offset:53248
	ds_read_b128 v[236:239], v192 offset:54272
	ds_read_b128 v[240:243], v192 offset:55296
	ds_read_b128 v[244:247], v192 offset:56320
	global_load_lds_dwordx4 v130, s[50:51]
	v_lshl_add_u64 v[156:157], s[50:51], 0, v[132:133]
	s_add_u32 s50, s50, s74
	s_mov_b32 m0, s83
	s_addc_u32 s51, s51, 0
	global_load_lds_dwordx4 v[156:157], off
	s_mov_b32 m0, s88
	s_nop 0
	global_load_lds_dwordx4 v130, s[50:51]
	s_mov_b32 m0, s89
	s_nop 0
	global_load_lds_dwordx4 v132, s[50:51]
	s_mov_b32 m0, s84
	s_nop 0
	global_load_lds_dwordx4 v149, s[52:53]
	s_mov_b32 m0, s87
	s_nop 0
	global_load_lds_dwordx4 v147, s[52:53]
	s_waitcnt vmcnt(8)
	s_waitcnt lgkmcnt(0)
	s_barrier
	s_setprio 1
	s_waitcnt lgkmcnt(0)
	v_mfma_f32_16x16x32_bf16 v[58:61], v[160:163], v[150:153], v[58:61]
	v_mfma_f32_16x16x32_bf16 v[50:53], v[172:175], v[150:153], v[50:53]
	v_mfma_f32_16x16x32_bf16 v[42:45], v[160:163], v[224:227], v[42:45]
	v_mfma_f32_16x16x32_bf16 v[38:41], v[172:175], v[224:227], v[38:41]
	v_mfma_f32_16x16x32_bf16 v[26:29], v[160:163], v[232:235], v[26:29]
	v_mfma_f32_16x16x32_bf16 v[18:21], v[172:175], v[232:235], v[18:21]
	v_mfma_f32_16x16x32_bf16 v[10:13], v[160:163], v[240:243], v[10:13]
	v_mfma_f32_16x16x32_bf16 v[6:9], v[172:175], v[240:243], v[6:9]
	v_mfma_f32_16x16x32_bf16 v[58:61], v[168:171], v[220:223], v[58:61]
	v_mfma_f32_16x16x32_bf16 v[50:53], v[176:179], v[220:223], v[50:53]
	v_mfma_f32_16x16x32_bf16 v[42:45], v[168:171], v[228:231], v[42:45]
	v_mfma_f32_16x16x32_bf16 v[38:41], v[176:179], v[228:231], v[38:41]
	v_mfma_f32_16x16x32_bf16 v[26:29], v[168:171], v[236:239], v[26:29]
	v_mfma_f32_16x16x32_bf16 v[18:21], v[176:179], v[236:239], v[18:21]
	v_mfma_f32_16x16x32_bf16 v[10:13], v[168:171], v[244:247], v[10:13]
	v_mfma_f32_16x16x32_bf16 v[6:9], v[176:179], v[244:247], v[6:9]
	s_setprio 0
	s_setprio 1
	v_mfma_f32_16x16x32_bf16 v[62:65], v[180:183], v[150:153], v[62:65]
	v_mfma_f32_16x16x32_bf16 v[54:57], v[212:215], v[150:153], v[54:57]
	v_mfma_f32_16x16x32_bf16 v[46:49], v[180:183], v[224:227], v[46:49]
	v_mfma_f32_16x16x32_bf16 v[34:37], v[212:215], v[224:227], v[34:37]
	v_mfma_f32_16x16x32_bf16 v[30:33], v[180:183], v[232:235], v[30:33]
	v_mfma_f32_16x16x32_bf16 v[22:25], v[212:215], v[232:235], v[22:25]
	v_mfma_f32_16x16x32_bf16 v[14:17], v[180:183], v[240:243], v[14:17]
	v_mfma_f32_16x16x32_bf16 v[2:5], v[212:215], v[240:243], v[2:5]
	v_mfma_f32_16x16x32_bf16 v[62:65], v[196:199], v[220:223], v[62:65]
	v_mfma_f32_16x16x32_bf16 v[54:57], v[216:219], v[220:223], v[54:57]
	v_mfma_f32_16x16x32_bf16 v[46:49], v[196:199], v[228:231], v[46:49]
	v_mfma_f32_16x16x32_bf16 v[34:37], v[216:219], v[228:231], v[34:37]
	v_mfma_f32_16x16x32_bf16 v[30:33], v[196:199], v[236:239], v[30:33]
	v_mfma_f32_16x16x32_bf16 v[22:25], v[216:219], v[236:239], v[22:25]
	v_mfma_f32_16x16x32_bf16 v[14:17], v[196:199], v[244:247], v[14:17]
	s_barrier
	v_mfma_f32_16x16x32_bf16 v[2:5], v[216:219], v[244:247], v[2:5]
	s_setprio 0
	s_add_i32 s2, s2, 2
	s_cmp_ge_i32 s2, s71
	s_cbranch_scc1 .LBB0_1986

.LBB0_2148:
	s_add_i32 s9, s10, s8
	s_add_i32 s28, s9, 1
	s_cmp_ge_i32 s28, s75
	s_cselect_b32 s29, s75, 0
	s_sub_i32 s28, s28, s29
	s_ashr_i32 s29, s28, 31
	s_lshl_b64 s[40:41], s[28:29], s36
	s_add_i32 s9, s9, 2
	s_cmp_ge_i32 s9, s75
	s_cselect_b32 s28, s75, 0
	s_sub_i32 s28, s9, s28
	s_ashr_i32 s29, s28, 31
	v_add_u32_e32 v0, s11, v180
	s_lshl_b64 s[28:29], s[28:29], s36
	ds_read_b128 v[140:143], v0
	ds_read_b128 v[144:147], v0 offset:1024
	ds_read_b128 v[148:151], v0 offset:2048
	ds_read_b128 v[152:155], v0 offset:3072
	v_add_u32_e32 v0, s66, v180
	s_add_u32 s9, s24, s28
	ds_read_b128 v[156:159], v0
	ds_read_b128 v[160:163], v0 offset:1024
	ds_read_b128 v[168:171], v0 offset:2048
	ds_read_b128 v[172:175], v0 offset:3072
	s_addc_u32 s30, s25, s29
	s_add_u32 s28, s26, s28
	s_addc_u32 s29, s27, s29
	s_cmp_eq_u32 s76, s8
	s_cselect_b32 s34, s91, s9
	s_cselect_b32 s35, s97, s30
	s_cselect_b32 s31, vcc_hi, s29
	s_cselect_b32 s30, vcc_lo, s28
	s_add_u32 s28, s34, s47
	s_addc_u32 s29, s35, 0
	s_add_u32 s40, s85, s40
	s_addc_u32 s41, s86, s41
	s_add_i32 m0, s71, 0xc000
	ds_read_b128 v[184:187], v182
	ds_read_b128 v[188:191], v182 offset:1024
	ds_read_b128 v[192:195], v182 offset:2048
	ds_read_b128 v[196:199], v182 offset:3072
	ds_read_b128 v[212:215], v182 offset:4096
	ds_read_b128 v[216:219], v182 offset:5120
	ds_read_b128 v[220:223], v182 offset:6144
	ds_read_b128 v[224:227], v182 offset:7168
	global_load_lds_dwordx4 v134, s[40:41]
	s_add_i32 m0, s71, 0xe000
	s_nop 0
	global_load_lds_dwordx4 v136, s[40:41]
	s_waitcnt vmcnt(8)
	s_waitcnt lgkmcnt(0)
	s_barrier
	s_setprio 1
	s_waitcnt lgkmcnt(0)
	v_mfma_f32_16x16x32_bf16 v[126:129], v[140:143], v[184:187], v[126:129]
	v_mfma_f32_16x16x32_bf16 v[122:125], v[148:151], v[184:187], v[122:125]
	v_mfma_f32_16x16x32_bf16 v[110:113], v[140:143], v[192:195], v[110:113]
	v_mfma_f32_16x16x32_bf16 v[106:109], v[148:151], v[192:195], v[106:109]
	v_mfma_f32_16x16x32_bf16 v[94:97], v[140:143], v[212:215], v[94:97]
	v_mfma_f32_16x16x32_bf16 v[90:93], v[148:151], v[212:215], v[90:93]
	v_mfma_f32_16x16x32_bf16 v[78:81], v[140:143], v[220:223], v[78:81]
	v_mfma_f32_16x16x32_bf16 v[74:77], v[148:151], v[220:223], v[74:77]
	v_mfma_f32_16x16x32_bf16 v[126:129], v[144:147], v[188:191], v[126:129]
	v_mfma_f32_16x16x32_bf16 v[122:125], v[152:155], v[188:191], v[122:125]
	v_mfma_f32_16x16x32_bf16 v[110:113], v[144:147], v[196:199], v[110:113]
	v_mfma_f32_16x16x32_bf16 v[106:109], v[152:155], v[196:199], v[106:109]
	v_mfma_f32_16x16x32_bf16 v[94:97], v[144:147], v[216:219], v[94:97]
	v_mfma_f32_16x16x32_bf16 v[90:93], v[152:155], v[216:219], v[90:93]
	v_mfma_f32_16x16x32_bf16 v[78:81], v[144:147], v[224:227], v[78:81]
	v_mfma_f32_16x16x32_bf16 v[74:77], v[152:155], v[224:227], v[74:77]
	s_setprio 0
	s_setprio 1
	v_mfma_f32_16x16x32_bf16 v[118:121], v[156:159], v[184:187], v[118:121]
	v_mfma_f32_16x16x32_bf16 v[114:117], v[168:171], v[184:187], v[114:117]
	v_mfma_f32_16x16x32_bf16 v[102:105], v[156:159], v[192:195], v[102:105]
	v_mfma_f32_16x16x32_bf16 v[98:101], v[168:171], v[192:195], v[98:101]
	v_mfma_f32_16x16x32_bf16 v[86:89], v[156:159], v[212:215], v[86:89]
	v_mfma_f32_16x16x32_bf16 v[82:85], v[168:171], v[212:215], v[82:85]
	v_mfma_f32_16x16x32_bf16 v[70:73], v[156:159], v[220:223], v[70:73]
	v_mfma_f32_16x16x32_bf16 v[66:69], v[168:171], v[220:223], v[66:69]
	v_mfma_f32_16x16x32_bf16 v[118:121], v[160:163], v[188:191], v[118:121]
	v_mfma_f32_16x16x32_bf16 v[114:117], v[172:175], v[188:191], v[114:117]
	v_mfma_f32_16x16x32_bf16 v[102:105], v[160:163], v[196:199], v[102:105]
	v_mfma_f32_16x16x32_bf16 v[98:101], v[172:175], v[196:199], v[98:101]
	v_mfma_f32_16x16x32_bf16 v[86:89], v[160:163], v[216:219], v[86:89]
	v_mfma_f32_16x16x32_bf16 v[82:85], v[172:175], v[216:219], v[82:85]
	v_mfma_f32_16x16x32_bf16 v[70:73], v[160:163], v[224:227], v[70:73]
	s_barrier
	v_mfma_f32_16x16x32_bf16 v[66:69], v[172:175], v[224:227], v[66:69]
	s_setprio 0
	s_mov_b32 m0, s37
	s_add_u32 s40, s30, s33
	ds_read_b128 v[184:187], v182 offset:16384
	ds_read_b128 v[188:191], v182 offset:17408
	ds_read_b128 v[192:195], v182 offset:18432
	ds_read_b128 v[196:199], v182 offset:19456
	ds_read_b128 v[212:215], v182 offset:20480
	ds_read_b128 v[216:219], v182 offset:21504
	ds_read_b128 v[220:223], v182 offset:22528
	ds_read_b128 v[224:227], v182 offset:23552
	global_load_lds_dwordx4 v134, s[30:31]
	s_mov_b32 m0, s60
	s_addc_u32 s41, s31, 0
	global_load_lds_dwordx4 v136, s[30:31]
	s_mov_b32 m0, s67
	s_nop 0
	global_load_lds_dwordx4 v134, s[40:41]
	s_mov_b32 m0, s70
	s_nop 0
	global_load_lds_dwordx4 v136, s[40:41]
	s_mov_b32 m0, s71
	s_nop 0
	global_load_lds_dwordx4 v134, s[34:35]
	s_mov_b32 m0, s72
	s_nop 0
	global_load_lds_dwordx4 v136, s[34:35]
	s_waitcnt vmcnt(8)
	s_waitcnt lgkmcnt(0)
	s_barrier
	s_setprio 1
	s_waitcnt lgkmcnt(0)
	v_mfma_f32_16x16x32_bf16 v[62:65], v[140:143], v[184:187], v[62:65]
	v_mfma_f32_16x16x32_bf16 v[58:61], v[148:151], v[184:187], v[58:61]
	v_mfma_f32_16x16x32_bf16 v[46:49], v[140:143], v[192:195], v[46:49]
	v_mfma_f32_16x16x32_bf16 v[42:45], v[148:151], v[192:195], v[42:45]
	v_mfma_f32_16x16x32_bf16 v[30:33], v[140:143], v[212:215], v[30:33]
	v_mfma_f32_16x16x32_bf16 v[26:29], v[148:151], v[212:215], v[26:29]
	v_mfma_f32_16x16x32_bf16 v[14:17], v[140:143], v[220:223], v[14:17]
	v_mfma_f32_16x16x32_bf16 v[10:13], v[148:151], v[220:223], v[10:13]
	v_mfma_f32_16x16x32_bf16 v[62:65], v[144:147], v[188:191], v[62:65]
	v_mfma_f32_16x16x32_bf16 v[58:61], v[152:155], v[188:191], v[58:61]
	v_mfma_f32_16x16x32_bf16 v[46:49], v[144:147], v[196:199], v[46:49]
	v_mfma_f32_16x16x32_bf16 v[42:45], v[152:155], v[196:199], v[42:45]
	v_mfma_f32_16x16x32_bf16 v[30:33], v[144:147], v[216:219], v[30:33]
	v_mfma_f32_16x16x32_bf16 v[26:29], v[152:155], v[216:219], v[26:29]
	v_mfma_f32_16x16x32_bf16 v[14:17], v[144:147], v[224:227], v[14:17]
	v_mfma_f32_16x16x32_bf16 v[10:13], v[152:155], v[224:227], v[10:13]
	s_setprio 0
	s_setprio 1
	v_mfma_f32_16x16x32_bf16 v[54:57], v[156:159], v[184:187], v[54:57]
	v_mfma_f32_16x16x32_bf16 v[50:53], v[168:171], v[184:187], v[50:53]
	v_mfma_f32_16x16x32_bf16 v[38:41], v[156:159], v[192:195], v[38:41]
	v_mfma_f32_16x16x32_bf16 v[34:37], v[168:171], v[192:195], v[34:37]
	v_mfma_f32_16x16x32_bf16 v[22:25], v[156:159], v[212:215], v[22:25]
	v_mfma_f32_16x16x32_bf16 v[18:21], v[168:171], v[212:215], v[18:21]
	v_mfma_f32_16x16x32_bf16 v[6:9], v[156:159], v[220:223], v[6:9]
	v_mfma_f32_16x16x32_bf16 v[2:5], v[168:171], v[220:223], v[2:5]
	v_mfma_f32_16x16x32_bf16 v[54:57], v[160:163], v[188:191], v[54:57]
	v_mfma_f32_16x16x32_bf16 v[50:53], v[172:175], v[188:191], v[50:53]
	v_mfma_f32_16x16x32_bf16 v[38:41], v[160:163], v[196:199], v[38:41]
	v_mfma_f32_16x16x32_bf16 v[34:37], v[172:175], v[196:199], v[34:37]
	v_mfma_f32_16x16x32_bf16 v[22:25], v[160:163], v[216:219], v[22:25]
	v_mfma_f32_16x16x32_bf16 v[18:21], v[172:175], v[216:219], v[18:21]
	v_mfma_f32_16x16x32_bf16 v[6:9], v[160:163], v[224:227], v[6:9]
	s_barrier
	v_mfma_f32_16x16x32_bf16 v[2:5], v[172:175], v[224:227], v[2:5]
	s_setprio 0
	v_add_u32_e32 v0, s77, v180
	ds_read_b128 v[140:143], v0
	ds_read_b128 v[144:147], v0 offset:1024
	ds_read_b128 v[148:151], v0 offset:2048
	ds_read_b128 v[152:155], v0 offset:3072
	v_add_u32_e32 v0, s82, v180
	ds_read_b128 v[156:159], v0
	ds_read_b128 v[160:163], v0 offset:1024
	ds_read_b128 v[168:171], v0 offset:2048
	ds_read_b128 v[172:175], v0 offset:3072
	s_add_u32 s34, s34, s33
	s_addc_u32 s35, s35, 0
	s_mov_b32 m0, s73
	ds_read_b128 v[184:187], v182 offset:32768
	ds_read_b128 v[188:191], v182 offset:33792
	ds_read_b128 v[192:195], v182 offset:34816
	ds_read_b128 v[196:199], v182 offset:35840
	ds_read_b128 v[212:215], v182 offset:36864
	ds_read_b128 v[216:219], v182 offset:37888
	ds_read_b128 v[220:223], v182 offset:38912
	ds_read_b128 v[224:227], v182 offset:39936
	global_load_lds_dwordx4 v134, s[34:35]
	s_mov_b32 m0, s74
	s_nop 0
	global_load_lds_dwordx4 v136, s[34:35]
	s_waitcnt vmcnt(8)
	s_waitcnt lgkmcnt(0)
	s_barrier
	s_setprio 1
	s_waitcnt lgkmcnt(0)
	v_mfma_f32_16x16x32_bf16 v[126:129], v[140:143], v[184:187], v[126:129]
	v_mfma_f32_16x16x32_bf16 v[122:125], v[148:151], v[184:187], v[122:125]
	v_mfma_f32_16x16x32_bf16 v[110:113], v[140:143], v[192:195], v[110:113]
	v_mfma_f32_16x16x32_bf16 v[106:109], v[148:151], v[192:195], v[106:109]
	v_mfma_f32_16x16x32_bf16 v[94:97], v[140:143], v[212:215], v[94:97]
	v_mfma_f32_16x16x32_bf16 v[90:93], v[148:151], v[212:215], v[90:93]
	v_mfma_f32_16x16x32_bf16 v[78:81], v[140:143], v[220:223], v[78:81]
	v_mfma_f32_16x16x32_bf16 v[74:77], v[148:151], v[220:223], v[74:77]
	v_mfma_f32_16x16x32_bf16 v[126:129], v[144:147], v[188:191], v[126:129]
	v_mfma_f32_16x16x32_bf16 v[122:125], v[152:155], v[188:191], v[122:125]
	v_mfma_f32_16x16x32_bf16 v[110:113], v[144:147], v[196:199], v[110:113]
	v_mfma_f32_16x16x32_bf16 v[106:109], v[152:155], v[196:199], v[106:109]
	v_mfma_f32_16x16x32_bf16 v[94:97], v[144:147], v[216:219], v[94:97]
	v_mfma_f32_16x16x32_bf16 v[90:93], v[152:155], v[216:219], v[90:93]
	v_mfma_f32_16x16x32_bf16 v[78:81], v[144:147], v[224:227], v[78:81]
	v_mfma_f32_16x16x32_bf16 v[74:77], v[152:155], v[224:227], v[74:77]
	s_setprio 0
	s_setprio 1
	v_mfma_f32_16x16x32_bf16 v[118:121], v[156:159], v[184:187], v[118:121]
	v_mfma_f32_16x16x32_bf16 v[114:117], v[168:171], v[184:187], v[114:117]
	v_mfma_f32_16x16x32_bf16 v[102:105], v[156:159], v[192:195], v[102:105]
	v_mfma_f32_16x16x32_bf16 v[98:101], v[168:171], v[192:195], v[98:101]
	v_mfma_f32_16x16x32_bf16 v[86:89], v[156:159], v[212:215], v[86:89]
	v_mfma_f32_16x16x32_bf16 v[82:85], v[168:171], v[212:215], v[82:85]
	v_mfma_f32_16x16x32_bf16 v[70:73], v[156:159], v[220:223], v[70:73]
	v_mfma_f32_16x16x32_bf16 v[66:69], v[168:171], v[220:223], v[66:69]
	v_mfma_f32_16x16x32_bf16 v[118:121], v[160:163], v[188:191], v[118:121]
	v_mfma_f32_16x16x32_bf16 v[114:117], v[172:175], v[188:191], v[114:117]
	v_mfma_f32_16x16x32_bf16 v[102:105], v[160:163], v[196:199], v[102:105]
	v_mfma_f32_16x16x32_bf16 v[98:101], v[172:175], v[196:199], v[98:101]
	v_mfma_f32_16x16x32_bf16 v[86:89], v[160:163], v[216:219], v[86:89]
	v_mfma_f32_16x16x32_bf16 v[82:85], v[172:175], v[216:219], v[82:85]
	v_mfma_f32_16x16x32_bf16 v[70:73], v[160:163], v[224:227], v[70:73]
	s_barrier
	v_mfma_f32_16x16x32_bf16 v[66:69], v[172:175], v[224:227], v[66:69]
	s_setprio 0
	s_add_u32 s30, s30, s47
	s_addc_u32 s31, s31, 0
	s_mov_b32 m0, s78
	ds_read_b128 v[184:187], v182 offset:49152
	ds_read_b128 v[188:191], v182 offset:50176
	ds_read_b128 v[192:195], v182 offset:51200
	ds_read_b128 v[196:199], v182 offset:52224
	ds_read_b128 v[212:215], v182 offset:53248
	ds_read_b128 v[216:219], v182 offset:54272
	ds_read_b128 v[220:223], v182 offset:55296
	ds_read_b128 v[224:227], v182 offset:56320
	global_load_lds_dwordx4 v134, s[30:31]
	v_lshl_add_u64 v[228:229], s[30:31], 0, v[136:137]
	s_add_u32 s30, s30, s33
	s_mov_b32 m0, s79
	s_addc_u32 s31, s31, 0
	global_load_lds_dwordx4 v[228:229], off
	s_mov_b32 m0, s83
	s_nop 0
	global_load_lds_dwordx4 v134, s[30:31]
	s_mov_b32 m0, s92
	s_nop 0
	global_load_lds_dwordx4 v136, s[30:31]
	s_mov_b32 m0, s80
	s_nop 0
	global_load_lds_dwordx4 v134, s[28:29]
	s_mov_b32 m0, s81
	s_nop 0
	global_load_lds_dwordx4 v136, s[28:29]
	s_waitcnt vmcnt(8)
	s_waitcnt lgkmcnt(0)
	s_barrier
	s_setprio 1
	s_waitcnt lgkmcnt(0)
	v_mfma_f32_16x16x32_bf16 v[62:65], v[140:143], v[184:187], v[62:65]
	v_mfma_f32_16x16x32_bf16 v[58:61], v[148:151], v[184:187], v[58:61]
	v_mfma_f32_16x16x32_bf16 v[46:49], v[140:143], v[192:195], v[46:49]
	v_mfma_f32_16x16x32_bf16 v[42:45], v[148:151], v[192:195], v[42:45]
	v_mfma_f32_16x16x32_bf16 v[30:33], v[140:143], v[212:215], v[30:33]
	v_mfma_f32_16x16x32_bf16 v[26:29], v[148:151], v[212:215], v[26:29]
	v_mfma_f32_16x16x32_bf16 v[14:17], v[140:143], v[220:223], v[14:17]
	v_mfma_f32_16x16x32_bf16 v[10:13], v[148:151], v[220:223], v[10:13]
	v_mfma_f32_16x16x32_bf16 v[62:65], v[144:147], v[188:191], v[62:65]
	v_mfma_f32_16x16x32_bf16 v[58:61], v[152:155], v[188:191], v[58:61]
	v_mfma_f32_16x16x32_bf16 v[46:49], v[144:147], v[196:199], v[46:49]
	v_mfma_f32_16x16x32_bf16 v[42:45], v[152:155], v[196:199], v[42:45]
	v_mfma_f32_16x16x32_bf16 v[30:33], v[144:147], v[216:219], v[30:33]
	v_mfma_f32_16x16x32_bf16 v[26:29], v[152:155], v[216:219], v[26:29]
	v_mfma_f32_16x16x32_bf16 v[14:17], v[144:147], v[224:227], v[14:17]
	v_mfma_f32_16x16x32_bf16 v[10:13], v[152:155], v[224:227], v[10:13]
	s_setprio 0
	s_setprio 1
	v_mfma_f32_16x16x32_bf16 v[54:57], v[156:159], v[184:187], v[54:57]
	v_mfma_f32_16x16x32_bf16 v[50:53], v[168:171], v[184:187], v[50:53]
	v_mfma_f32_16x16x32_bf16 v[38:41], v[156:159], v[192:195], v[38:41]
	v_mfma_f32_16x16x32_bf16 v[34:37], v[168:171], v[192:195], v[34:37]
	v_mfma_f32_16x16x32_bf16 v[22:25], v[156:159], v[212:215], v[22:25]
	v_mfma_f32_16x16x32_bf16 v[18:21], v[168:171], v[212:215], v[18:21]
	v_mfma_f32_16x16x32_bf16 v[6:9], v[156:159], v[220:223], v[6:9]
	v_mfma_f32_16x16x32_bf16 v[2:5], v[168:171], v[220:223], v[2:5]
	v_mfma_f32_16x16x32_bf16 v[54:57], v[160:163], v[188:191], v[54:57]
	v_mfma_f32_16x16x32_bf16 v[50:53], v[172:175], v[188:191], v[50:53]
	v_mfma_f32_16x16x32_bf16 v[38:41], v[160:163], v[196:199], v[38:41]
	v_mfma_f32_16x16x32_bf16 v[34:37], v[172:175], v[196:199], v[34:37]
	v_mfma_f32_16x16x32_bf16 v[22:25], v[160:163], v[216:219], v[22:25]
	v_mfma_f32_16x16x32_bf16 v[18:21], v[172:175], v[216:219], v[18:21]
	v_mfma_f32_16x16x32_bf16 v[6:9], v[160:163], v[224:227], v[6:9]
	s_barrier
	v_mfma_f32_16x16x32_bf16 v[2:5], v[172:175], v[224:227], v[2:5]
	s_setprio 0
	s_add_i32 s8, s8, 2
	s_cmp_ge_i32 s8, s75
	s_cbranch_scc0 .LBB0_2148

.LBB0_2381:
	s_add_i32 s8, s52, s66
	s_add_i32 s6, s8, -1
	s_cmp_ge_i32 s6, s67
	s_cselect_b32 s7, s67, 0
	s_sub_i32 s6, s6, s7
	s_ashr_i32 s7, s6, 31
	s_lshl_b64 s[40:41], s[6:7], s21
	s_cmp_ge_i32 s8, s67
	s_cselect_b32 s6, s67, 0
	s_sub_i32 s6, s8, s6
	s_ashr_i32 s7, s6, 31
	v_add_u32_e32 v141, s24, v0
	s_lshl_b64 s[6:7], s[6:7], s21
	ds_read_b128 v[142:145], v141
	ds_read_b128 v[146:149], v141 offset:1024
	ds_read_b128 v[150:153], v141 offset:2048
	ds_read_b128 v[154:157], v141 offset:3072
	v_add_u32_e32 v141, s27, v0
	s_add_u32 s8, s19, s6
	ds_read_b128 v[158:161], v141
	ds_read_b128 v[168:171], v141 offset:1024
	ds_read_b128 v[172:175], v141 offset:2048
	ds_read_b128 v[180:183], v141 offset:3072
	s_addc_u32 s9, s20, s7
	s_add_u32 s6, s22, s6
	s_addc_u32 s7, s23, s7
	s_cmp_eq_u32 s67, s66
	s_cselect_b32 s10, s2, s8
	s_cselect_b32 s11, s3, s9
	s_cselect_b32 s9, s5, s7
	s_cselect_b32 s8, s4, s6
	s_add_u32 s6, s10, s47
	s_addc_u32 s7, s11, 0
	s_add_u32 s40, s64, s40
	s_addc_u32 s41, s65, s41
	s_add_i32 m0, s30, 0xc000
	ds_read_b128 v[184:187], v139
	ds_read_b128 v[188:191], v139 offset:1024
	ds_read_b128 v[192:195], v139 offset:2048
	ds_read_b128 v[196:199], v139 offset:3072
	ds_read_b128 v[212:215], v139 offset:4096
	ds_read_b128 v[216:219], v139 offset:5120
	ds_read_b128 v[220:223], v139 offset:6144
	ds_read_b128 v[224:227], v139 offset:7168
	global_load_lds_dwordx4 v134, s[40:41]
	s_add_i32 m0, s30, 0xe000
	s_nop 0
	global_load_lds_dwordx4 v136, s[40:41]
	s_waitcnt vmcnt(8)
	s_waitcnt lgkmcnt(0)
	s_barrier
	s_setprio 1
	s_waitcnt lgkmcnt(0)
	v_mfma_f32_16x16x32_bf16 v[126:129], v[142:145], v[184:187], v[126:129]
	v_mfma_f32_16x16x32_bf16 v[122:125], v[150:153], v[184:187], v[122:125]
	v_mfma_f32_16x16x32_bf16 v[110:113], v[142:145], v[192:195], v[110:113]
	v_mfma_f32_16x16x32_bf16 v[106:109], v[150:153], v[192:195], v[106:109]
	v_mfma_f32_16x16x32_bf16 v[94:97], v[142:145], v[212:215], v[94:97]
	v_mfma_f32_16x16x32_bf16 v[90:93], v[150:153], v[212:215], v[90:93]
	v_mfma_f32_16x16x32_bf16 v[78:81], v[142:145], v[220:223], v[78:81]
	v_mfma_f32_16x16x32_bf16 v[74:77], v[150:153], v[220:223], v[74:77]
	v_mfma_f32_16x16x32_bf16 v[126:129], v[146:149], v[188:191], v[126:129]
	v_mfma_f32_16x16x32_bf16 v[122:125], v[154:157], v[188:191], v[122:125]
	v_mfma_f32_16x16x32_bf16 v[110:113], v[146:149], v[196:199], v[110:113]
	v_mfma_f32_16x16x32_bf16 v[106:109], v[154:157], v[196:199], v[106:109]
	v_mfma_f32_16x16x32_bf16 v[94:97], v[146:149], v[216:219], v[94:97]
	v_mfma_f32_16x16x32_bf16 v[90:93], v[154:157], v[216:219], v[90:93]
	v_mfma_f32_16x16x32_bf16 v[78:81], v[146:149], v[224:227], v[78:81]
	v_mfma_f32_16x16x32_bf16 v[74:77], v[154:157], v[224:227], v[74:77]
	s_setprio 0
	s_setprio 1
	v_mfma_f32_16x16x32_bf16 v[118:121], v[158:161], v[184:187], v[118:121]
	v_mfma_f32_16x16x32_bf16 v[114:117], v[172:175], v[184:187], v[114:117]
	v_mfma_f32_16x16x32_bf16 v[102:105], v[158:161], v[192:195], v[102:105]
	v_mfma_f32_16x16x32_bf16 v[98:101], v[172:175], v[192:195], v[98:101]
	v_mfma_f32_16x16x32_bf16 v[86:89], v[158:161], v[212:215], v[86:89]
	v_mfma_f32_16x16x32_bf16 v[82:85], v[172:175], v[212:215], v[82:85]
	v_mfma_f32_16x16x32_bf16 v[70:73], v[158:161], v[220:223], v[70:73]
	v_mfma_f32_16x16x32_bf16 v[66:69], v[172:175], v[220:223], v[66:69]
	v_mfma_f32_16x16x32_bf16 v[118:121], v[168:171], v[188:191], v[118:121]
	v_mfma_f32_16x16x32_bf16 v[114:117], v[180:183], v[188:191], v[114:117]
	v_mfma_f32_16x16x32_bf16 v[102:105], v[168:171], v[196:199], v[102:105]
	v_mfma_f32_16x16x32_bf16 v[98:101], v[180:183], v[196:199], v[98:101]
	v_mfma_f32_16x16x32_bf16 v[86:89], v[168:171], v[216:219], v[86:89]
	v_mfma_f32_16x16x32_bf16 v[82:85], v[180:183], v[216:219], v[82:85]
	v_mfma_f32_16x16x32_bf16 v[70:73], v[168:171], v[224:227], v[70:73]
	s_barrier
	v_mfma_f32_16x16x32_bf16 v[66:69], v[180:183], v[224:227], v[66:69]
	s_setprio 0
	s_mov_b32 m0, s25
	s_add_u32 s40, s8, s18
	ds_read_b128 v[184:187], v139 offset:16384
	ds_read_b128 v[188:191], v139 offset:17408
	ds_read_b128 v[192:195], v139 offset:18432
	ds_read_b128 v[196:199], v139 offset:19456
	ds_read_b128 v[212:215], v139 offset:20480
	ds_read_b128 v[216:219], v139 offset:21504
	ds_read_b128 v[220:223], v139 offset:22528
	ds_read_b128 v[224:227], v139 offset:23552
	global_load_lds_dwordx4 v134, s[8:9]
	s_mov_b32 m0, s26
	s_addc_u32 s41, s9, s17
	global_load_lds_dwordx4 v136, s[8:9]
	s_mov_b32 m0, s28
	s_nop 0
	global_load_lds_dwordx4 v134, s[40:41]
	s_mov_b32 m0, s29
	s_nop 0
	global_load_lds_dwordx4 v136, s[40:41]
	s_mov_b32 m0, s30
	s_nop 0
	global_load_lds_dwordx4 v134, s[10:11]
	s_mov_b32 m0, s31
	s_nop 0
	global_load_lds_dwordx4 v136, s[10:11]
	s_waitcnt vmcnt(8)
	s_waitcnt lgkmcnt(0)
	s_barrier
	s_setprio 1
	s_waitcnt lgkmcnt(0)
	v_mfma_f32_16x16x32_bf16 v[62:65], v[142:145], v[184:187], v[62:65]
	v_mfma_f32_16x16x32_bf16 v[58:61], v[150:153], v[184:187], v[58:61]
	v_mfma_f32_16x16x32_bf16 v[46:49], v[142:145], v[192:195], v[46:49]
	v_mfma_f32_16x16x32_bf16 v[42:45], v[150:153], v[192:195], v[42:45]
	v_mfma_f32_16x16x32_bf16 v[30:33], v[142:145], v[212:215], v[30:33]
	v_mfma_f32_16x16x32_bf16 v[26:29], v[150:153], v[212:215], v[26:29]
	v_mfma_f32_16x16x32_bf16 v[14:17], v[142:145], v[220:223], v[14:17]
	v_mfma_f32_16x16x32_bf16 v[10:13], v[150:153], v[220:223], v[10:13]
	v_mfma_f32_16x16x32_bf16 v[62:65], v[146:149], v[188:191], v[62:65]
	v_mfma_f32_16x16x32_bf16 v[58:61], v[154:157], v[188:191], v[58:61]
	v_mfma_f32_16x16x32_bf16 v[46:49], v[146:149], v[196:199], v[46:49]
	v_mfma_f32_16x16x32_bf16 v[42:45], v[154:157], v[196:199], v[42:45]
	v_mfma_f32_16x16x32_bf16 v[30:33], v[146:149], v[216:219], v[30:33]
	v_mfma_f32_16x16x32_bf16 v[26:29], v[154:157], v[216:219], v[26:29]
	v_mfma_f32_16x16x32_bf16 v[14:17], v[146:149], v[224:227], v[14:17]
	v_mfma_f32_16x16x32_bf16 v[10:13], v[154:157], v[224:227], v[10:13]
	s_setprio 0
	s_setprio 1
	v_mfma_f32_16x16x32_bf16 v[54:57], v[158:161], v[184:187], v[54:57]
	v_mfma_f32_16x16x32_bf16 v[50:53], v[172:175], v[184:187], v[50:53]
	v_mfma_f32_16x16x32_bf16 v[38:41], v[158:161], v[192:195], v[38:41]
	v_mfma_f32_16x16x32_bf16 v[34:37], v[172:175], v[192:195], v[34:37]
	v_mfma_f32_16x16x32_bf16 v[22:25], v[158:161], v[212:215], v[22:25]
	v_mfma_f32_16x16x32_bf16 v[18:21], v[172:175], v[212:215], v[18:21]
	v_mfma_f32_16x16x32_bf16 v[6:9], v[158:161], v[220:223], v[6:9]
	v_mfma_f32_16x16x32_bf16 v[2:5], v[172:175], v[220:223], v[2:5]
	v_mfma_f32_16x16x32_bf16 v[54:57], v[168:171], v[188:191], v[54:57]
	v_mfma_f32_16x16x32_bf16 v[50:53], v[180:183], v[188:191], v[50:53]
	v_mfma_f32_16x16x32_bf16 v[38:41], v[168:171], v[196:199], v[38:41]
	v_mfma_f32_16x16x32_bf16 v[34:37], v[180:183], v[196:199], v[34:37]
	v_mfma_f32_16x16x32_bf16 v[22:25], v[168:171], v[216:219], v[22:25]
	v_mfma_f32_16x16x32_bf16 v[18:21], v[180:183], v[216:219], v[18:21]
	v_mfma_f32_16x16x32_bf16 v[6:9], v[168:171], v[224:227], v[6:9]
	s_barrier
	v_mfma_f32_16x16x32_bf16 v[2:5], v[180:183], v[224:227], v[2:5]
	s_setprio 0
	v_add_u32_e32 v141, s35, v0
	ds_read_b128 v[142:145], v141
	ds_read_b128 v[146:149], v141 offset:1024
	ds_read_b128 v[150:153], v141 offset:2048
	ds_read_b128 v[154:157], v141 offset:3072
	v_add_u32_e32 v141, s51, v0
	ds_read_b128 v[158:161], v141
	ds_read_b128 v[168:171], v141 offset:1024
	ds_read_b128 v[172:175], v141 offset:2048
	ds_read_b128 v[180:183], v141 offset:3072
	s_add_u32 s10, s10, s18
	s_addc_u32 s11, s11, s17
	s_mov_b32 m0, s33
	ds_read_b128 v[184:187], v139 offset:32768
	ds_read_b128 v[188:191], v139 offset:33792
	ds_read_b128 v[192:195], v139 offset:34816
	ds_read_b128 v[196:199], v139 offset:35840
	ds_read_b128 v[212:215], v139 offset:36864
	ds_read_b128 v[216:219], v139 offset:37888
	ds_read_b128 v[220:223], v139 offset:38912
	ds_read_b128 v[224:227], v139 offset:39936
	global_load_lds_dwordx4 v134, s[10:11]
	s_mov_b32 m0, s34
	s_nop 0
	global_load_lds_dwordx4 v136, s[10:11]
	s_waitcnt vmcnt(8)
	s_waitcnt lgkmcnt(0)
	s_barrier
	s_setprio 1
	s_waitcnt lgkmcnt(0)
	v_mfma_f32_16x16x32_bf16 v[126:129], v[142:145], v[184:187], v[126:129]
	v_mfma_f32_16x16x32_bf16 v[122:125], v[150:153], v[184:187], v[122:125]
	v_mfma_f32_16x16x32_bf16 v[110:113], v[142:145], v[192:195], v[110:113]
	v_mfma_f32_16x16x32_bf16 v[106:109], v[150:153], v[192:195], v[106:109]
	v_mfma_f32_16x16x32_bf16 v[94:97], v[142:145], v[212:215], v[94:97]
	v_mfma_f32_16x16x32_bf16 v[90:93], v[150:153], v[212:215], v[90:93]
	v_mfma_f32_16x16x32_bf16 v[78:81], v[142:145], v[220:223], v[78:81]
	v_mfma_f32_16x16x32_bf16 v[74:77], v[150:153], v[220:223], v[74:77]
	v_mfma_f32_16x16x32_bf16 v[126:129], v[146:149], v[188:191], v[126:129]
	v_mfma_f32_16x16x32_bf16 v[122:125], v[154:157], v[188:191], v[122:125]
	v_mfma_f32_16x16x32_bf16 v[110:113], v[146:149], v[196:199], v[110:113]
	v_mfma_f32_16x16x32_bf16 v[106:109], v[154:157], v[196:199], v[106:109]
	v_mfma_f32_16x16x32_bf16 v[94:97], v[146:149], v[216:219], v[94:97]
	v_mfma_f32_16x16x32_bf16 v[90:93], v[154:157], v[216:219], v[90:93]
	v_mfma_f32_16x16x32_bf16 v[78:81], v[146:149], v[224:227], v[78:81]
	v_mfma_f32_16x16x32_bf16 v[74:77], v[154:157], v[224:227], v[74:77]
	s_setprio 0
	s_setprio 1
	v_mfma_f32_16x16x32_bf16 v[118:121], v[158:161], v[184:187], v[118:121]
	v_mfma_f32_16x16x32_bf16 v[114:117], v[172:175], v[184:187], v[114:117]
	v_mfma_f32_16x16x32_bf16 v[102:105], v[158:161], v[192:195], v[102:105]
	v_mfma_f32_16x16x32_bf16 v[98:101], v[172:175], v[192:195], v[98:101]
	v_mfma_f32_16x16x32_bf16 v[86:89], v[158:161], v[212:215], v[86:89]
	v_mfma_f32_16x16x32_bf16 v[82:85], v[172:175], v[212:215], v[82:85]
	v_mfma_f32_16x16x32_bf16 v[70:73], v[158:161], v[220:223], v[70:73]
	v_mfma_f32_16x16x32_bf16 v[66:69], v[172:175], v[220:223], v[66:69]
	v_mfma_f32_16x16x32_bf16 v[118:121], v[168:171], v[188:191], v[118:121]
	v_mfma_f32_16x16x32_bf16 v[114:117], v[180:183], v[188:191], v[114:117]
	v_mfma_f32_16x16x32_bf16 v[102:105], v[168:171], v[196:199], v[102:105]
	v_mfma_f32_16x16x32_bf16 v[98:101], v[180:183], v[196:199], v[98:101]
	v_mfma_f32_16x16x32_bf16 v[86:89], v[168:171], v[216:219], v[86:89]
	v_mfma_f32_16x16x32_bf16 v[82:85], v[180:183], v[216:219], v[82:85]
	v_mfma_f32_16x16x32_bf16 v[70:73], v[168:171], v[224:227], v[70:73]
	s_barrier
	v_mfma_f32_16x16x32_bf16 v[66:69], v[180:183], v[224:227], v[66:69]
	s_setprio 0
	s_add_u32 s8, s8, s47
	s_addc_u32 s9, s9, 0
	s_mov_b32 m0, s36
	ds_read_b128 v[184:187], v139 offset:49152
	ds_read_b128 v[188:191], v139 offset:50176
	ds_read_b128 v[192:195], v139 offset:51200
	ds_read_b128 v[196:199], v139 offset:52224
	ds_read_b128 v[212:215], v139 offset:53248
	ds_read_b128 v[216:219], v139 offset:54272
	ds_read_b128 v[220:223], v139 offset:55296
	ds_read_b128 v[224:227], v139 offset:56320
	global_load_lds_dwordx4 v134, s[8:9]
	v_lshl_add_u64 v[162:163], s[8:9], 0, v[136:137]
	s_add_u32 s8, s8, s18
	s_mov_b32 m0, s37
	s_addc_u32 s9, s9, s17
	global_load_lds_dwordx4 v[162:163], off
	s_mov_b32 m0, s55
	s_nop 0
	global_load_lds_dwordx4 v134, s[8:9]
	s_mov_b32 m0, s60
	s_nop 0
	global_load_lds_dwordx4 v136, s[8:9]
	s_mov_b32 m0, s48
	s_nop 0
	global_load_lds_dwordx4 v134, s[6:7]
	s_mov_b32 m0, s50
	s_nop 0
	global_load_lds_dwordx4 v136, s[6:7]
	s_waitcnt vmcnt(8)
	s_waitcnt lgkmcnt(0)
	s_barrier
	s_setprio 1
	s_waitcnt lgkmcnt(0)
	v_mfma_f32_16x16x32_bf16 v[62:65], v[142:145], v[184:187], v[62:65]
	v_mfma_f32_16x16x32_bf16 v[58:61], v[150:153], v[184:187], v[58:61]
	v_mfma_f32_16x16x32_bf16 v[46:49], v[142:145], v[192:195], v[46:49]
	v_mfma_f32_16x16x32_bf16 v[42:45], v[150:153], v[192:195], v[42:45]
	v_mfma_f32_16x16x32_bf16 v[30:33], v[142:145], v[212:215], v[30:33]
	v_mfma_f32_16x16x32_bf16 v[26:29], v[150:153], v[212:215], v[26:29]
	v_mfma_f32_16x16x32_bf16 v[14:17], v[142:145], v[220:223], v[14:17]
	v_mfma_f32_16x16x32_bf16 v[10:13], v[150:153], v[220:223], v[10:13]
	v_mfma_f32_16x16x32_bf16 v[62:65], v[146:149], v[188:191], v[62:65]
	v_mfma_f32_16x16x32_bf16 v[58:61], v[154:157], v[188:191], v[58:61]
	v_mfma_f32_16x16x32_bf16 v[46:49], v[146:149], v[196:199], v[46:49]
	v_mfma_f32_16x16x32_bf16 v[42:45], v[154:157], v[196:199], v[42:45]
	v_mfma_f32_16x16x32_bf16 v[30:33], v[146:149], v[216:219], v[30:33]
	v_mfma_f32_16x16x32_bf16 v[26:29], v[154:157], v[216:219], v[26:29]
	v_mfma_f32_16x16x32_bf16 v[14:17], v[146:149], v[224:227], v[14:17]
	v_mfma_f32_16x16x32_bf16 v[10:13], v[154:157], v[224:227], v[10:13]
	s_setprio 0
	s_setprio 1
	v_mfma_f32_16x16x32_bf16 v[54:57], v[158:161], v[184:187], v[54:57]
	v_mfma_f32_16x16x32_bf16 v[50:53], v[172:175], v[184:187], v[50:53]
	v_mfma_f32_16x16x32_bf16 v[38:41], v[158:161], v[192:195], v[38:41]
	v_mfma_f32_16x16x32_bf16 v[34:37], v[172:175], v[192:195], v[34:37]
	v_mfma_f32_16x16x32_bf16 v[22:25], v[158:161], v[212:215], v[22:25]
	v_mfma_f32_16x16x32_bf16 v[18:21], v[172:175], v[212:215], v[18:21]
	v_mfma_f32_16x16x32_bf16 v[6:9], v[158:161], v[220:223], v[6:9]
	v_mfma_f32_16x16x32_bf16 v[2:5], v[172:175], v[220:223], v[2:5]
	v_mfma_f32_16x16x32_bf16 v[54:57], v[168:171], v[188:191], v[54:57]
	v_mfma_f32_16x16x32_bf16 v[50:53], v[180:183], v[188:191], v[50:53]
	v_mfma_f32_16x16x32_bf16 v[38:41], v[168:171], v[196:199], v[38:41]
	v_mfma_f32_16x16x32_bf16 v[34:37], v[180:183], v[196:199], v[34:37]
	v_mfma_f32_16x16x32_bf16 v[22:25], v[168:171], v[216:219], v[22:25]
	v_mfma_f32_16x16x32_bf16 v[18:21], v[180:183], v[216:219], v[18:21]
	v_mfma_f32_16x16x32_bf16 v[6:9], v[168:171], v[224:227], v[6:9]
	s_barrier
	v_mfma_f32_16x16x32_bf16 v[2:5], v[180:183], v[224:227], v[2:5]
	s_setprio 0
	s_add_i32 s6, s66, 2
	s_cmp_ge_i32 s66, s67
	s_mov_b32 s66, s6
	s_cbranch_scc0 .LBB0_2381

.LBB0_2391:
	s_add_i32 s8, s52, s60
	s_add_i32 s6, s8, -1
	s_cmp_ge_i32 s6, s64
	s_cselect_b32 s7, s64, 0
	s_sub_i32 s6, s6, s7
	s_ashr_i32 s7, s6, 31
	s_lshl_b64 s[40:41], s[6:7], s19
	s_cmp_ge_i32 s8, s64
	s_cselect_b32 s6, s64, 0
	s_sub_i32 s6, s8, s6
	s_ashr_i32 s7, s6, 31
	s_lshl_b64 s[6:7], s[6:7], s19
	v_add_u32_e32 v152, s22, v138
	v_add_u32_e32 v165, s25, v138
	s_add_u32 s8, s17, s6
	ds_read_b128 v[140:143], v152
	ds_read_b128 v[144:147], v152 offset:1024
	ds_read_b128 v[148:151], v152 offset:2048
	ds_read_b128 v[152:155], v152 offset:3072
	ds_read_b128 v[156:159], v165
	ds_read_b128 v[160:163], v165 offset:1024
	ds_read_b128 v[168:171], v165 offset:2048
	ds_read_b128 v[172:175], v165 offset:3072
	s_addc_u32 s9, s18, s7
	s_add_u32 s6, s20, s6
	s_addc_u32 s7, s21, s7
	s_cmp_eq_u32 s64, s60
	s_cselect_b32 s10, s2, s8
	s_cselect_b32 s11, s3, s9
	s_cselect_b32 s9, s5, s7
	s_cselect_b32 s8, s4, s6
	s_add_u32 s6, s10, s47
	s_addc_u32 s7, s11, 0
	s_add_u32 s40, s51, s40
	s_addc_u32 s41, s55, s41
	s_add_i32 m0, s28, 0xc000
	ds_read_b128 v[180:183], v139
	ds_read_b128 v[184:187], v139 offset:1024
	ds_read_b128 v[188:191], v139 offset:2048
	ds_read_b128 v[192:195], v139 offset:3072
	ds_read_b128 v[196:199], v139 offset:4096
	ds_read_b128 v[212:215], v139 offset:5120
	ds_read_b128 v[216:219], v139 offset:6144
	ds_read_b128 v[220:223], v139 offset:7168
	global_load_lds_dwordx4 v134, s[40:41]
	s_add_i32 m0, s28, 0xe000
	s_nop 0
	global_load_lds_dwordx4 v136, s[40:41]
	s_waitcnt vmcnt(8)
	s_waitcnt lgkmcnt(0)
	s_barrier
	s_setprio 1
	s_waitcnt lgkmcnt(0)
	v_mfma_f32_16x16x32_bf16 v[126:129], v[140:143], v[180:183], v[126:129]
	v_mfma_f32_16x16x32_bf16 v[122:125], v[148:151], v[180:183], v[122:125]
	v_mfma_f32_16x16x32_bf16 v[110:113], v[140:143], v[188:191], v[110:113]
	v_mfma_f32_16x16x32_bf16 v[106:109], v[148:151], v[188:191], v[106:109]
	v_mfma_f32_16x16x32_bf16 v[94:97], v[140:143], v[196:199], v[94:97]
	v_mfma_f32_16x16x32_bf16 v[90:93], v[148:151], v[196:199], v[90:93]
	v_mfma_f32_16x16x32_bf16 v[78:81], v[140:143], v[216:219], v[78:81]
	v_mfma_f32_16x16x32_bf16 v[74:77], v[148:151], v[216:219], v[74:77]
	v_mfma_f32_16x16x32_bf16 v[126:129], v[144:147], v[184:187], v[126:129]
	v_mfma_f32_16x16x32_bf16 v[122:125], v[152:155], v[184:187], v[122:125]
	v_mfma_f32_16x16x32_bf16 v[110:113], v[144:147], v[192:195], v[110:113]
	v_mfma_f32_16x16x32_bf16 v[106:109], v[152:155], v[192:195], v[106:109]
	v_mfma_f32_16x16x32_bf16 v[94:97], v[144:147], v[212:215], v[94:97]
	v_mfma_f32_16x16x32_bf16 v[90:93], v[152:155], v[212:215], v[90:93]
	v_mfma_f32_16x16x32_bf16 v[78:81], v[144:147], v[220:223], v[78:81]
	v_mfma_f32_16x16x32_bf16 v[74:77], v[152:155], v[220:223], v[74:77]
	s_setprio 0
	s_setprio 1
	v_mfma_f32_16x16x32_bf16 v[118:121], v[156:159], v[180:183], v[118:121]
	v_mfma_f32_16x16x32_bf16 v[114:117], v[168:171], v[180:183], v[114:117]
	v_mfma_f32_16x16x32_bf16 v[102:105], v[156:159], v[188:191], v[102:105]
	v_mfma_f32_16x16x32_bf16 v[98:101], v[168:171], v[188:191], v[98:101]
	v_mfma_f32_16x16x32_bf16 v[86:89], v[156:159], v[196:199], v[86:89]
	v_mfma_f32_16x16x32_bf16 v[82:85], v[168:171], v[196:199], v[82:85]
	v_mfma_f32_16x16x32_bf16 v[70:73], v[156:159], v[216:219], v[70:73]
	v_mfma_f32_16x16x32_bf16 v[66:69], v[168:171], v[216:219], v[66:69]
	v_mfma_f32_16x16x32_bf16 v[118:121], v[160:163], v[184:187], v[118:121]
	v_mfma_f32_16x16x32_bf16 v[114:117], v[172:175], v[184:187], v[114:117]
	v_mfma_f32_16x16x32_bf16 v[102:105], v[160:163], v[192:195], v[102:105]
	v_mfma_f32_16x16x32_bf16 v[98:101], v[172:175], v[192:195], v[98:101]
	v_mfma_f32_16x16x32_bf16 v[86:89], v[160:163], v[212:215], v[86:89]
	v_mfma_f32_16x16x32_bf16 v[82:85], v[172:175], v[212:215], v[82:85]
	v_mfma_f32_16x16x32_bf16 v[70:73], v[160:163], v[220:223], v[70:73]
	s_barrier
	v_mfma_f32_16x16x32_bf16 v[66:69], v[172:175], v[220:223], v[66:69]
	s_setprio 0
	s_mov_b32 m0, s23
	s_add_u32 s40, s8, s16
	ds_read_b128 v[180:183], v139 offset:16384
	ds_read_b128 v[184:187], v139 offset:17408
	ds_read_b128 v[188:191], v139 offset:18432
	ds_read_b128 v[192:195], v139 offset:19456
	ds_read_b128 v[196:199], v139 offset:20480
	ds_read_b128 v[212:215], v139 offset:21504
	ds_read_b128 v[216:219], v139 offset:22528
	ds_read_b128 v[220:223], v139 offset:23552
	global_load_lds_dwordx4 v134, s[8:9]
	s_mov_b32 m0, s24
	s_addc_u32 s41, s9, s15
	global_load_lds_dwordx4 v136, s[8:9]
	s_mov_b32 m0, s26
	s_nop 0
	global_load_lds_dwordx4 v134, s[40:41]
	s_mov_b32 m0, s27
	s_nop 0
	global_load_lds_dwordx4 v136, s[40:41]
	s_mov_b32 m0, s28
	s_nop 0
	global_load_lds_dwordx4 v134, s[10:11]
	s_mov_b32 m0, s29
	s_nop 0
	global_load_lds_dwordx4 v136, s[10:11]
	s_waitcnt vmcnt(8)
	s_waitcnt lgkmcnt(0)
	s_barrier
	s_setprio 1
	s_waitcnt lgkmcnt(0)
	v_mfma_f32_16x16x32_bf16 v[62:65], v[140:143], v[180:183], v[62:65]
	v_mfma_f32_16x16x32_bf16 v[58:61], v[148:151], v[180:183], v[58:61]
	v_mfma_f32_16x16x32_bf16 v[46:49], v[140:143], v[188:191], v[46:49]
	v_mfma_f32_16x16x32_bf16 v[42:45], v[148:151], v[188:191], v[42:45]
	v_mfma_f32_16x16x32_bf16 v[30:33], v[140:143], v[196:199], v[30:33]
	v_mfma_f32_16x16x32_bf16 v[26:29], v[148:151], v[196:199], v[26:29]
	v_mfma_f32_16x16x32_bf16 v[14:17], v[140:143], v[216:219], v[14:17]
	v_mfma_f32_16x16x32_bf16 v[10:13], v[148:151], v[216:219], v[10:13]
	v_mfma_f32_16x16x32_bf16 v[62:65], v[144:147], v[184:187], v[62:65]
	v_mfma_f32_16x16x32_bf16 v[58:61], v[152:155], v[184:187], v[58:61]
	v_mfma_f32_16x16x32_bf16 v[46:49], v[144:147], v[192:195], v[46:49]
	v_mfma_f32_16x16x32_bf16 v[42:45], v[152:155], v[192:195], v[42:45]
	v_mfma_f32_16x16x32_bf16 v[30:33], v[144:147], v[212:215], v[30:33]
	v_mfma_f32_16x16x32_bf16 v[26:29], v[152:155], v[212:215], v[26:29]
	v_mfma_f32_16x16x32_bf16 v[14:17], v[144:147], v[220:223], v[14:17]
	v_mfma_f32_16x16x32_bf16 v[10:13], v[152:155], v[220:223], v[10:13]
	s_setprio 0
	s_setprio 1
	v_mfma_f32_16x16x32_bf16 v[54:57], v[156:159], v[180:183], v[54:57]
	v_mfma_f32_16x16x32_bf16 v[50:53], v[168:171], v[180:183], v[50:53]
	v_mfma_f32_16x16x32_bf16 v[38:41], v[156:159], v[188:191], v[38:41]
	v_mfma_f32_16x16x32_bf16 v[34:37], v[168:171], v[188:191], v[34:37]
	v_mfma_f32_16x16x32_bf16 v[22:25], v[156:159], v[196:199], v[22:25]
	v_mfma_f32_16x16x32_bf16 v[18:21], v[168:171], v[196:199], v[18:21]
	v_mfma_f32_16x16x32_bf16 v[6:9], v[156:159], v[216:219], v[6:9]
	v_mfma_f32_16x16x32_bf16 v[2:5], v[168:171], v[216:219], v[2:5]
	v_mfma_f32_16x16x32_bf16 v[54:57], v[160:163], v[184:187], v[54:57]
	v_mfma_f32_16x16x32_bf16 v[50:53], v[172:175], v[184:187], v[50:53]
	v_mfma_f32_16x16x32_bf16 v[38:41], v[160:163], v[192:195], v[38:41]
	v_mfma_f32_16x16x32_bf16 v[34:37], v[172:175], v[192:195], v[34:37]
	v_mfma_f32_16x16x32_bf16 v[22:25], v[160:163], v[212:215], v[22:25]
	v_mfma_f32_16x16x32_bf16 v[18:21], v[172:175], v[212:215], v[18:21]
	v_mfma_f32_16x16x32_bf16 v[6:9], v[160:163], v[220:223], v[6:9]
	s_barrier
	v_mfma_f32_16x16x32_bf16 v[2:5], v[172:175], v[220:223], v[2:5]
	s_setprio 0
	v_add_u32_e32 v152, s33, v138
	v_add_u32_e32 v165, s38, v138
	ds_read_b128 v[140:143], v152
	ds_read_b128 v[144:147], v152 offset:1024
	ds_read_b128 v[148:151], v152 offset:2048
	ds_read_b128 v[152:155], v152 offset:3072
	ds_read_b128 v[156:159], v165
	ds_read_b128 v[160:163], v165 offset:1024
	ds_read_b128 v[168:171], v165 offset:2048
	ds_read_b128 v[172:175], v165 offset:3072
	s_add_u32 s10, s10, s16
	s_addc_u32 s11, s11, s15
	s_mov_b32 m0, s30
	ds_read_b128 v[180:183], v139 offset:32768
	ds_read_b128 v[184:187], v139 offset:33792
	ds_read_b128 v[188:191], v139 offset:34816
	ds_read_b128 v[192:195], v139 offset:35840
	ds_read_b128 v[196:199], v139 offset:36864
	ds_read_b128 v[212:215], v139 offset:37888
	ds_read_b128 v[216:219], v139 offset:38912
	ds_read_b128 v[220:223], v139 offset:39936
	global_load_lds_dwordx4 v134, s[10:11]
	s_mov_b32 m0, s31
	s_nop 0
	global_load_lds_dwordx4 v136, s[10:11]
	s_waitcnt vmcnt(8)
	s_waitcnt lgkmcnt(0)
	s_barrier
	s_setprio 1
	s_waitcnt lgkmcnt(0)
	v_mfma_f32_16x16x32_bf16 v[126:129], v[140:143], v[180:183], v[126:129]
	v_mfma_f32_16x16x32_bf16 v[122:125], v[148:151], v[180:183], v[122:125]
	v_mfma_f32_16x16x32_bf16 v[110:113], v[140:143], v[188:191], v[110:113]
	v_mfma_f32_16x16x32_bf16 v[106:109], v[148:151], v[188:191], v[106:109]
	v_mfma_f32_16x16x32_bf16 v[94:97], v[140:143], v[196:199], v[94:97]
	v_mfma_f32_16x16x32_bf16 v[90:93], v[148:151], v[196:199], v[90:93]
	v_mfma_f32_16x16x32_bf16 v[78:81], v[140:143], v[216:219], v[78:81]
	v_mfma_f32_16x16x32_bf16 v[74:77], v[148:151], v[216:219], v[74:77]
	v_mfma_f32_16x16x32_bf16 v[126:129], v[144:147], v[184:187], v[126:129]
	v_mfma_f32_16x16x32_bf16 v[122:125], v[152:155], v[184:187], v[122:125]
	v_mfma_f32_16x16x32_bf16 v[110:113], v[144:147], v[192:195], v[110:113]
	v_mfma_f32_16x16x32_bf16 v[106:109], v[152:155], v[192:195], v[106:109]
	v_mfma_f32_16x16x32_bf16 v[94:97], v[144:147], v[212:215], v[94:97]
	v_mfma_f32_16x16x32_bf16 v[90:93], v[152:155], v[212:215], v[90:93]
	v_mfma_f32_16x16x32_bf16 v[78:81], v[144:147], v[220:223], v[78:81]
	v_mfma_f32_16x16x32_bf16 v[74:77], v[152:155], v[220:223], v[74:77]
	s_setprio 0
	s_setprio 1
	v_mfma_f32_16x16x32_bf16 v[118:121], v[156:159], v[180:183], v[118:121]
	v_mfma_f32_16x16x32_bf16 v[114:117], v[168:171], v[180:183], v[114:117]
	v_mfma_f32_16x16x32_bf16 v[102:105], v[156:159], v[188:191], v[102:105]
	v_mfma_f32_16x16x32_bf16 v[98:101], v[168:171], v[188:191], v[98:101]
	v_mfma_f32_16x16x32_bf16 v[86:89], v[156:159], v[196:199], v[86:89]
	v_mfma_f32_16x16x32_bf16 v[82:85], v[168:171], v[196:199], v[82:85]
	v_mfma_f32_16x16x32_bf16 v[70:73], v[156:159], v[216:219], v[70:73]
	v_mfma_f32_16x16x32_bf16 v[66:69], v[168:171], v[216:219], v[66:69]
	v_mfma_f32_16x16x32_bf16 v[118:121], v[160:163], v[184:187], v[118:121]
	v_mfma_f32_16x16x32_bf16 v[114:117], v[172:175], v[184:187], v[114:117]
	v_mfma_f32_16x16x32_bf16 v[102:105], v[160:163], v[192:195], v[102:105]
	v_mfma_f32_16x16x32_bf16 v[98:101], v[172:175], v[192:195], v[98:101]
	v_mfma_f32_16x16x32_bf16 v[86:89], v[160:163], v[212:215], v[86:89]
	v_mfma_f32_16x16x32_bf16 v[82:85], v[172:175], v[212:215], v[82:85]
	v_mfma_f32_16x16x32_bf16 v[70:73], v[160:163], v[220:223], v[70:73]
	s_barrier
	v_mfma_f32_16x16x32_bf16 v[66:69], v[172:175], v[220:223], v[66:69]
	s_setprio 0
	s_add_u32 s8, s8, s47
	s_addc_u32 s9, s9, 0
	s_mov_b32 m0, s34
	ds_read_b128 v[180:183], v139 offset:49152
	ds_read_b128 v[184:187], v139 offset:50176
	ds_read_b128 v[188:191], v139 offset:51200
	ds_read_b128 v[192:195], v139 offset:52224
	ds_read_b128 v[196:199], v139 offset:53248
	ds_read_b128 v[212:215], v139 offset:54272
	ds_read_b128 v[216:219], v139 offset:55296
	ds_read_b128 v[220:223], v139 offset:56320
	global_load_lds_dwordx4 v134, s[8:9]
	v_lshl_add_u64 v[224:225], s[8:9], 0, v[136:137]
	s_add_u32 s8, s8, s16
	s_mov_b32 m0, s35
	s_addc_u32 s9, s9, s15
	global_load_lds_dwordx4 v[224:225], off
	s_mov_b32 m0, s48
	s_nop 0
	global_load_lds_dwordx4 v134, s[8:9]
	s_mov_b32 m0, s50
	s_nop 0
	global_load_lds_dwordx4 v136, s[8:9]
	s_mov_b32 m0, s36
	s_nop 0
	global_load_lds_dwordx4 v134, s[6:7]
	s_mov_b32 m0, s37
	s_nop 0
	global_load_lds_dwordx4 v136, s[6:7]
	s_waitcnt vmcnt(8)
	s_waitcnt lgkmcnt(0)
	s_barrier
	s_setprio 1
	s_waitcnt lgkmcnt(0)
	v_mfma_f32_16x16x32_bf16 v[62:65], v[140:143], v[180:183], v[62:65]
	v_mfma_f32_16x16x32_bf16 v[58:61], v[148:151], v[180:183], v[58:61]
	v_mfma_f32_16x16x32_bf16 v[46:49], v[140:143], v[188:191], v[46:49]
	v_mfma_f32_16x16x32_bf16 v[42:45], v[148:151], v[188:191], v[42:45]
	v_mfma_f32_16x16x32_bf16 v[30:33], v[140:143], v[196:199], v[30:33]
	v_mfma_f32_16x16x32_bf16 v[26:29], v[148:151], v[196:199], v[26:29]
	v_mfma_f32_16x16x32_bf16 v[14:17], v[140:143], v[216:219], v[14:17]
	v_mfma_f32_16x16x32_bf16 v[10:13], v[148:151], v[216:219], v[10:13]
	v_mfma_f32_16x16x32_bf16 v[62:65], v[144:147], v[184:187], v[62:65]
	v_mfma_f32_16x16x32_bf16 v[58:61], v[152:155], v[184:187], v[58:61]
	v_mfma_f32_16x16x32_bf16 v[46:49], v[144:147], v[192:195], v[46:49]
	v_mfma_f32_16x16x32_bf16 v[42:45], v[152:155], v[192:195], v[42:45]
	v_mfma_f32_16x16x32_bf16 v[30:33], v[144:147], v[212:215], v[30:33]
	v_mfma_f32_16x16x32_bf16 v[26:29], v[152:155], v[212:215], v[26:29]
	v_mfma_f32_16x16x32_bf16 v[14:17], v[144:147], v[220:223], v[14:17]
	v_mfma_f32_16x16x32_bf16 v[10:13], v[152:155], v[220:223], v[10:13]
	s_setprio 0
	s_setprio 1
	v_mfma_f32_16x16x32_bf16 v[54:57], v[156:159], v[180:183], v[54:57]
	v_mfma_f32_16x16x32_bf16 v[50:53], v[168:171], v[180:183], v[50:53]
	v_mfma_f32_16x16x32_bf16 v[38:41], v[156:159], v[188:191], v[38:41]
	v_mfma_f32_16x16x32_bf16 v[34:37], v[168:171], v[188:191], v[34:37]
	v_mfma_f32_16x16x32_bf16 v[22:25], v[156:159], v[196:199], v[22:25]
	v_mfma_f32_16x16x32_bf16 v[18:21], v[168:171], v[196:199], v[18:21]
	v_mfma_f32_16x16x32_bf16 v[6:9], v[156:159], v[216:219], v[6:9]
	v_mfma_f32_16x16x32_bf16 v[2:5], v[168:171], v[216:219], v[2:5]
	v_mfma_f32_16x16x32_bf16 v[54:57], v[160:163], v[184:187], v[54:57]
	v_mfma_f32_16x16x32_bf16 v[50:53], v[172:175], v[184:187], v[50:53]
	v_mfma_f32_16x16x32_bf16 v[38:41], v[160:163], v[192:195], v[38:41]
	v_mfma_f32_16x16x32_bf16 v[34:37], v[172:175], v[192:195], v[34:37]
	v_mfma_f32_16x16x32_bf16 v[22:25], v[160:163], v[212:215], v[22:25]
	v_mfma_f32_16x16x32_bf16 v[18:21], v[172:175], v[212:215], v[18:21]
	v_mfma_f32_16x16x32_bf16 v[6:9], v[160:163], v[220:223], v[6:9]
	s_barrier
	v_mfma_f32_16x16x32_bf16 v[2:5], v[172:175], v[220:223], v[2:5]
	s_setprio 0
	s_add_i32 s6, s60, 2
	s_cmp_ge_i32 s60, s64
	s_mov_b32 s60, s6
	s_cbranch_scc0 .LBB0_2391

.LBB0_2802:
	s_add_i32 s28, s4, s75
	s_add_i32 s26, s28, 1
	s_cmp_ge_i32 s26, s51
	s_cselect_b32 s27, s51, 0
	s_sub_i32 s26, s26, s27
	s_ashr_i32 s27, s26, 31
	s_lshl_b64 s[76:77], s[26:27], s39
	s_add_i32 s28, s28, 2
	s_cmp_ge_i32 s28, s51
	s_cselect_b32 s26, s51, 0
	s_sub_i32 s26, s28, s26
	s_ashr_i32 s27, s26, 31
	v_add_u32_e32 v136, s5, v141
	s_lshl_b64 s[26:27], s[26:27], s39
	ds_read_b128 v[146:149], v136
	ds_read_b128 v[150:153], v136 offset:1024
	ds_read_b128 v[154:157], v136 offset:2048
	ds_read_b128 v[158:161], v136 offset:3072
	v_add_u32_e32 v136, s43, v141
	s_add_u32 s28, s22, s26
	ds_read_b128 v[172:175], v136
	ds_read_b128 v[176:179], v136 offset:1024
	ds_read_b128 v[180:183], v136 offset:2048
	ds_read_b128 v[184:187], v136 offset:3072
	s_addc_u32 s29, s23, s27
	s_add_u32 s26, s24, s26
	s_addc_u32 s27, s25, s27
	s_cmp_eq_u32 s52, s75
	s_cselect_b32 s30, s71, s28
	s_cselect_b32 s31, s72, s29
	s_cselect_b32 s29, s74, s27
	s_cselect_b32 s28, s73, s26
	s_add_u32 s26, s30, s53
	s_addc_u32 s27, s31, 0
	s_add_u32 s76, s69, s76
	s_addc_u32 s77, s70, s77
	s_add_i32 m0, s46, 0xc000
	ds_read_b128 v[188:191], v145
	ds_read_b128 v[192:195], v145 offset:1024
	ds_read_b128 v[196:199], v145 offset:2048
	ds_read_b128 v[212:215], v145 offset:3072
	ds_read_b128 v[216:219], v145 offset:4096
	ds_read_b128 v[220:223], v145 offset:5120
	ds_read_b128 v[224:227], v145 offset:6144
	ds_read_b128 v[228:231], v145 offset:7168
	global_load_lds_dwordx4 v134, s[76:77]
	s_add_i32 m0, s46, 0xe000
	s_nop 0
	global_load_lds_dwordx4 v132, s[76:77]
	s_waitcnt vmcnt(8)
	s_waitcnt lgkmcnt(0)
	s_barrier
	s_setprio 1
	s_waitcnt lgkmcnt(0)
	v_mfma_f32_16x16x32_bf16 v[122:125], v[146:149], v[188:191], v[122:125]
	v_mfma_f32_16x16x32_bf16 v[114:117], v[154:157], v[188:191], v[114:117]
	v_mfma_f32_16x16x32_bf16 v[106:109], v[146:149], v[196:199], v[106:109]
	v_mfma_f32_16x16x32_bf16 v[98:101], v[154:157], v[196:199], v[98:101]
	v_mfma_f32_16x16x32_bf16 v[90:93], v[146:149], v[216:219], v[90:93]
	v_mfma_f32_16x16x32_bf16 v[82:85], v[154:157], v[216:219], v[82:85]
	v_mfma_f32_16x16x32_bf16 v[74:77], v[146:149], v[224:227], v[74:77]
	v_mfma_f32_16x16x32_bf16 v[66:69], v[154:157], v[224:227], v[66:69]
	v_mfma_f32_16x16x32_bf16 v[122:125], v[150:153], v[192:195], v[122:125]
	v_mfma_f32_16x16x32_bf16 v[114:117], v[158:161], v[192:195], v[114:117]
	v_mfma_f32_16x16x32_bf16 v[106:109], v[150:153], v[212:215], v[106:109]
	v_mfma_f32_16x16x32_bf16 v[98:101], v[158:161], v[212:215], v[98:101]
	v_mfma_f32_16x16x32_bf16 v[90:93], v[150:153], v[220:223], v[90:93]
	v_mfma_f32_16x16x32_bf16 v[82:85], v[158:161], v[220:223], v[82:85]
	v_mfma_f32_16x16x32_bf16 v[74:77], v[150:153], v[228:231], v[74:77]
	v_mfma_f32_16x16x32_bf16 v[66:69], v[158:161], v[228:231], v[66:69]
	s_setprio 0
	s_setprio 1
	v_mfma_f32_16x16x32_bf16 v[126:129], v[172:175], v[188:191], v[126:129]
	v_mfma_f32_16x16x32_bf16 v[118:121], v[180:183], v[188:191], v[118:121]
	v_mfma_f32_16x16x32_bf16 v[110:113], v[172:175], v[196:199], v[110:113]
	v_mfma_f32_16x16x32_bf16 v[102:105], v[180:183], v[196:199], v[102:105]
	v_mfma_f32_16x16x32_bf16 v[94:97], v[172:175], v[216:219], v[94:97]
	v_mfma_f32_16x16x32_bf16 v[86:89], v[180:183], v[216:219], v[86:89]
	v_mfma_f32_16x16x32_bf16 v[78:81], v[172:175], v[224:227], v[78:81]
	v_mfma_f32_16x16x32_bf16 v[70:73], v[180:183], v[224:227], v[70:73]
	v_mfma_f32_16x16x32_bf16 v[126:129], v[176:179], v[192:195], v[126:129]
	v_mfma_f32_16x16x32_bf16 v[118:121], v[184:187], v[192:195], v[118:121]
	v_mfma_f32_16x16x32_bf16 v[110:113], v[176:179], v[212:215], v[110:113]
	v_mfma_f32_16x16x32_bf16 v[102:105], v[184:187], v[212:215], v[102:105]
	v_mfma_f32_16x16x32_bf16 v[94:97], v[176:179], v[220:223], v[94:97]
	v_mfma_f32_16x16x32_bf16 v[86:89], v[184:187], v[220:223], v[86:89]
	v_mfma_f32_16x16x32_bf16 v[78:81], v[176:179], v[228:231], v[78:81]
	s_barrier
	v_mfma_f32_16x16x32_bf16 v[70:73], v[184:187], v[228:231], v[70:73]
	s_setprio 0
	s_mov_b32 m0, s41
	s_add_u32 s76, s28, s38
	ds_read_b128 v[188:191], v145 offset:16384
	ds_read_b128 v[192:195], v145 offset:17408
	ds_read_b128 v[196:199], v145 offset:18432
	ds_read_b128 v[212:215], v145 offset:19456
	ds_read_b128 v[216:219], v145 offset:20480
	ds_read_b128 v[220:223], v145 offset:21504
	ds_read_b128 v[224:227], v145 offset:22528
	ds_read_b128 v[228:231], v145 offset:23552
	global_load_lds_dwordx4 v0, s[28:29]
	s_mov_b32 m0, s42
	s_addc_u32 s77, s29, 0
	global_load_lds_dwordx4 v130, s[28:29]
	s_mov_b32 m0, s44
	s_nop 0
	global_load_lds_dwordx4 v0, s[76:77]
	s_mov_b32 m0, s45
	s_nop 0
	global_load_lds_dwordx4 v130, s[76:77]
	s_mov_b32 m0, s46
	s_nop 0
	global_load_lds_dwordx4 v134, s[30:31]
	s_mov_b32 m0, s47
	s_nop 0
	global_load_lds_dwordx4 v132, s[30:31]
	s_waitcnt vmcnt(8)
	s_waitcnt lgkmcnt(0)
	s_barrier
	s_setprio 1
	s_waitcnt lgkmcnt(0)
	v_mfma_f32_16x16x32_bf16 v[58:61], v[146:149], v[188:191], v[58:61]
	v_mfma_f32_16x16x32_bf16 v[50:53], v[154:157], v[188:191], v[50:53]
	v_mfma_f32_16x16x32_bf16 v[42:45], v[146:149], v[196:199], v[42:45]
	v_mfma_f32_16x16x32_bf16 v[38:41], v[154:157], v[196:199], v[38:41]
	v_mfma_f32_16x16x32_bf16 v[26:29], v[146:149], v[216:219], v[26:29]
	v_mfma_f32_16x16x32_bf16 v[18:21], v[154:157], v[216:219], v[18:21]
	v_mfma_f32_16x16x32_bf16 v[10:13], v[146:149], v[224:227], v[10:13]
	v_mfma_f32_16x16x32_bf16 v[6:9], v[154:157], v[224:227], v[6:9]
	v_mfma_f32_16x16x32_bf16 v[58:61], v[150:153], v[192:195], v[58:61]
	v_mfma_f32_16x16x32_bf16 v[50:53], v[158:161], v[192:195], v[50:53]
	v_mfma_f32_16x16x32_bf16 v[42:45], v[150:153], v[212:215], v[42:45]
	v_mfma_f32_16x16x32_bf16 v[38:41], v[158:161], v[212:215], v[38:41]
	v_mfma_f32_16x16x32_bf16 v[26:29], v[150:153], v[220:223], v[26:29]
	v_mfma_f32_16x16x32_bf16 v[18:21], v[158:161], v[220:223], v[18:21]
	v_mfma_f32_16x16x32_bf16 v[10:13], v[150:153], v[228:231], v[10:13]
	v_mfma_f32_16x16x32_bf16 v[6:9], v[158:161], v[228:231], v[6:9]
	s_setprio 0
	s_setprio 1
	v_mfma_f32_16x16x32_bf16 v[62:65], v[172:175], v[188:191], v[62:65]
	v_mfma_f32_16x16x32_bf16 v[54:57], v[180:183], v[188:191], v[54:57]
	v_mfma_f32_16x16x32_bf16 v[46:49], v[172:175], v[196:199], v[46:49]
	v_mfma_f32_16x16x32_bf16 v[34:37], v[180:183], v[196:199], v[34:37]
	v_mfma_f32_16x16x32_bf16 v[30:33], v[172:175], v[216:219], v[30:33]
	v_mfma_f32_16x16x32_bf16 v[22:25], v[180:183], v[216:219], v[22:25]
	v_mfma_f32_16x16x32_bf16 v[14:17], v[172:175], v[224:227], v[14:17]
	v_mfma_f32_16x16x32_bf16 v[2:5], v[180:183], v[224:227], v[2:5]
	v_mfma_f32_16x16x32_bf16 v[62:65], v[176:179], v[192:195], v[62:65]
	v_mfma_f32_16x16x32_bf16 v[54:57], v[184:187], v[192:195], v[54:57]
	v_mfma_f32_16x16x32_bf16 v[46:49], v[176:179], v[212:215], v[46:49]
	v_mfma_f32_16x16x32_bf16 v[34:37], v[184:187], v[212:215], v[34:37]
	v_mfma_f32_16x16x32_bf16 v[30:33], v[176:179], v[220:223], v[30:33]
	v_mfma_f32_16x16x32_bf16 v[22:25], v[184:187], v[220:223], v[22:25]
	v_mfma_f32_16x16x32_bf16 v[14:17], v[176:179], v[228:231], v[14:17]
	s_barrier
	v_mfma_f32_16x16x32_bf16 v[2:5], v[184:187], v[228:231], v[2:5]
	s_setprio 0
	v_add_u32_e32 v136, s55, v141
	ds_read_b128 v[146:149], v136
	ds_read_b128 v[150:153], v136 offset:1024
	ds_read_b128 v[154:157], v136 offset:2048
	ds_read_b128 v[158:161], v136 offset:3072
	v_add_u32_e32 v136, s60, v141
	ds_read_b128 v[172:175], v136
	ds_read_b128 v[176:179], v136 offset:1024
	ds_read_b128 v[180:183], v136 offset:2048
	ds_read_b128 v[184:187], v136 offset:3072
	s_add_u32 s30, s30, s38
	s_addc_u32 s31, s31, 0
	s_mov_b32 m0, s48
	ds_read_b128 v[188:191], v145 offset:32768
	ds_read_b128 v[192:195], v145 offset:33792
	ds_read_b128 v[196:199], v145 offset:34816
	ds_read_b128 v[212:215], v145 offset:35840
	ds_read_b128 v[216:219], v145 offset:36864
	ds_read_b128 v[220:223], v145 offset:37888
	ds_read_b128 v[224:227], v145 offset:38912
	ds_read_b128 v[228:231], v145 offset:39936
	global_load_lds_dwordx4 v134, s[30:31]
	s_mov_b32 m0, s49
	s_nop 0
	global_load_lds_dwordx4 v132, s[30:31]
	s_waitcnt vmcnt(8)
	s_waitcnt lgkmcnt(0)
	s_barrier
	s_setprio 1
	s_waitcnt lgkmcnt(0)
	v_mfma_f32_16x16x32_bf16 v[122:125], v[146:149], v[188:191], v[122:125]
	v_mfma_f32_16x16x32_bf16 v[114:117], v[154:157], v[188:191], v[114:117]
	v_mfma_f32_16x16x32_bf16 v[106:109], v[146:149], v[196:199], v[106:109]
	v_mfma_f32_16x16x32_bf16 v[98:101], v[154:157], v[196:199], v[98:101]
	v_mfma_f32_16x16x32_bf16 v[90:93], v[146:149], v[216:219], v[90:93]
	v_mfma_f32_16x16x32_bf16 v[82:85], v[154:157], v[216:219], v[82:85]
	v_mfma_f32_16x16x32_bf16 v[74:77], v[146:149], v[224:227], v[74:77]
	v_mfma_f32_16x16x32_bf16 v[66:69], v[154:157], v[224:227], v[66:69]
	v_mfma_f32_16x16x32_bf16 v[122:125], v[150:153], v[192:195], v[122:125]
	v_mfma_f32_16x16x32_bf16 v[114:117], v[158:161], v[192:195], v[114:117]
	v_mfma_f32_16x16x32_bf16 v[106:109], v[150:153], v[212:215], v[106:109]
	v_mfma_f32_16x16x32_bf16 v[98:101], v[158:161], v[212:215], v[98:101]
	v_mfma_f32_16x16x32_bf16 v[90:93], v[150:153], v[220:223], v[90:93]
	v_mfma_f32_16x16x32_bf16 v[82:85], v[158:161], v[220:223], v[82:85]
	v_mfma_f32_16x16x32_bf16 v[74:77], v[150:153], v[228:231], v[74:77]
	v_mfma_f32_16x16x32_bf16 v[66:69], v[158:161], v[228:231], v[66:69]
	s_setprio 0
	s_setprio 1
	v_mfma_f32_16x16x32_bf16 v[126:129], v[172:175], v[188:191], v[126:129]
	v_mfma_f32_16x16x32_bf16 v[118:121], v[180:183], v[188:191], v[118:121]
	v_mfma_f32_16x16x32_bf16 v[110:113], v[172:175], v[196:199], v[110:113]
	v_mfma_f32_16x16x32_bf16 v[102:105], v[180:183], v[196:199], v[102:105]
	v_mfma_f32_16x16x32_bf16 v[94:97], v[172:175], v[216:219], v[94:97]
	v_mfma_f32_16x16x32_bf16 v[86:89], v[180:183], v[216:219], v[86:89]
	v_mfma_f32_16x16x32_bf16 v[78:81], v[172:175], v[224:227], v[78:81]
	v_mfma_f32_16x16x32_bf16 v[70:73], v[180:183], v[224:227], v[70:73]
	v_mfma_f32_16x16x32_bf16 v[126:129], v[176:179], v[192:195], v[126:129]
	v_mfma_f32_16x16x32_bf16 v[118:121], v[184:187], v[192:195], v[118:121]
	v_mfma_f32_16x16x32_bf16 v[110:113], v[176:179], v[212:215], v[110:113]
	v_mfma_f32_16x16x32_bf16 v[102:105], v[184:187], v[212:215], v[102:105]
	v_mfma_f32_16x16x32_bf16 v[94:97], v[176:179], v[220:223], v[94:97]
	v_mfma_f32_16x16x32_bf16 v[86:89], v[184:187], v[220:223], v[86:89]
	v_mfma_f32_16x16x32_bf16 v[78:81], v[176:179], v[228:231], v[78:81]
	s_barrier
	v_mfma_f32_16x16x32_bf16 v[70:73], v[184:187], v[228:231], v[70:73]
	s_setprio 0
	s_add_u32 s28, s28, s53
	s_addc_u32 s29, s29, 0
	s_mov_b32 m0, s56
	ds_read_b128 v[188:191], v145 offset:49152
	ds_read_b128 v[192:195], v145 offset:50176
	ds_read_b128 v[196:199], v145 offset:51200
	ds_read_b128 v[212:215], v145 offset:52224
	ds_read_b128 v[216:219], v145 offset:53248
	ds_read_b128 v[220:223], v145 offset:54272
	ds_read_b128 v[224:227], v145 offset:55296
	ds_read_b128 v[228:231], v145 offset:56320
	global_load_lds_dwordx4 v0, s[28:29]
	v_lshl_add_u64 v[136:137], s[28:29], 0, v[130:131]
	s_add_u32 s28, s28, s38
	s_mov_b32 m0, s57
	s_addc_u32 s29, s29, 0
	global_load_lds_dwordx4 v[136:137], off
	s_mov_b32 m0, s62
	s_nop 0
	global_load_lds_dwordx4 v0, s[28:29]
	s_mov_b32 m0, s63
	s_nop 0
	global_load_lds_dwordx4 v130, s[28:29]
	s_mov_b32 m0, s58
	s_nop 0
	global_load_lds_dwordx4 v134, s[26:27]
	s_mov_b32 m0, s59
	s_nop 0
	global_load_lds_dwordx4 v132, s[26:27]
	s_waitcnt vmcnt(8)
	s_waitcnt lgkmcnt(0)
	s_barrier
	s_setprio 1
	s_waitcnt lgkmcnt(0)
	v_mfma_f32_16x16x32_bf16 v[58:61], v[146:149], v[188:191], v[58:61]
	v_mfma_f32_16x16x32_bf16 v[50:53], v[154:157], v[188:191], v[50:53]
	v_mfma_f32_16x16x32_bf16 v[42:45], v[146:149], v[196:199], v[42:45]
	v_mfma_f32_16x16x32_bf16 v[38:41], v[154:157], v[196:199], v[38:41]
	v_mfma_f32_16x16x32_bf16 v[26:29], v[146:149], v[216:219], v[26:29]
	v_mfma_f32_16x16x32_bf16 v[18:21], v[154:157], v[216:219], v[18:21]
	v_mfma_f32_16x16x32_bf16 v[10:13], v[146:149], v[224:227], v[10:13]
	v_mfma_f32_16x16x32_bf16 v[6:9], v[154:157], v[224:227], v[6:9]
	v_mfma_f32_16x16x32_bf16 v[58:61], v[150:153], v[192:195], v[58:61]
	v_mfma_f32_16x16x32_bf16 v[50:53], v[158:161], v[192:195], v[50:53]
	v_mfma_f32_16x16x32_bf16 v[42:45], v[150:153], v[212:215], v[42:45]
	v_mfma_f32_16x16x32_bf16 v[38:41], v[158:161], v[212:215], v[38:41]
	v_mfma_f32_16x16x32_bf16 v[26:29], v[150:153], v[220:223], v[26:29]
	v_mfma_f32_16x16x32_bf16 v[18:21], v[158:161], v[220:223], v[18:21]
	v_mfma_f32_16x16x32_bf16 v[10:13], v[150:153], v[228:231], v[10:13]
	v_mfma_f32_16x16x32_bf16 v[6:9], v[158:161], v[228:231], v[6:9]
	s_setprio 0
	s_setprio 1
	v_mfma_f32_16x16x32_bf16 v[62:65], v[172:175], v[188:191], v[62:65]
	v_mfma_f32_16x16x32_bf16 v[54:57], v[180:183], v[188:191], v[54:57]
	v_mfma_f32_16x16x32_bf16 v[46:49], v[172:175], v[196:199], v[46:49]
	v_mfma_f32_16x16x32_bf16 v[34:37], v[180:183], v[196:199], v[34:37]
	v_mfma_f32_16x16x32_bf16 v[30:33], v[172:175], v[216:219], v[30:33]
	v_mfma_f32_16x16x32_bf16 v[22:25], v[180:183], v[216:219], v[22:25]
	v_mfma_f32_16x16x32_bf16 v[14:17], v[172:175], v[224:227], v[14:17]
	v_mfma_f32_16x16x32_bf16 v[2:5], v[180:183], v[224:227], v[2:5]
	v_mfma_f32_16x16x32_bf16 v[62:65], v[176:179], v[192:195], v[62:65]
	v_mfma_f32_16x16x32_bf16 v[54:57], v[184:187], v[192:195], v[54:57]
	v_mfma_f32_16x16x32_bf16 v[46:49], v[176:179], v[212:215], v[46:49]
	v_mfma_f32_16x16x32_bf16 v[34:37], v[184:187], v[212:215], v[34:37]
	v_mfma_f32_16x16x32_bf16 v[30:33], v[176:179], v[220:223], v[30:33]
	v_mfma_f32_16x16x32_bf16 v[22:25], v[184:187], v[220:223], v[22:25]
	v_mfma_f32_16x16x32_bf16 v[14:17], v[176:179], v[228:231], v[14:17]
	s_barrier
	v_mfma_f32_16x16x32_bf16 v[2:5], v[184:187], v[228:231], v[2:5]
	s_setprio 0
	s_add_i32 s75, s75, 2
	s_cmp_ge_i32 s75, s51
	s_cbranch_scc0 .LBB0_2802

.LBB0_2886:
	s_add_i32 s26, s4, s73
	s_add_i32 s24, s26, 1
	s_cmp_ge_i32 s24, s49
	s_cselect_b32 s25, s49, 0
	s_sub_i32 s24, s24, s25
	s_ashr_i32 s25, s24, 31
	s_lshl_b64 s[74:75], s[24:25], s38
	s_add_i32 s26, s26, 2
	s_cmp_ge_i32 s26, s49
	s_cselect_b32 s24, s49, 0
	s_sub_i32 s24, s26, s24
	s_ashr_i32 s25, s24, 31
	s_lshl_b64 s[24:25], s[24:25], s38
	v_add_u32_e32 v144, s5, v155
	v_add_u32_e32 v152, s41, v155
	s_add_u32 s26, s20, s24
	ds_read_b128 v[132:135], v144
	ds_read_b128 v[136:139], v144 offset:1024
	ds_read_b128 v[140:143], v144 offset:2048
	ds_read_b128 v[144:147], v144 offset:3072
	ds_read_b128 v[148:151], v152
	ds_read_b128 v[158:161], v152 offset:1024
	ds_read_b128 v[172:175], v152 offset:2048
	ds_read_b128 v[176:179], v152 offset:3072
	s_addc_u32 s27, s21, s25
	s_add_u32 s24, s22, s24
	s_addc_u32 s25, s23, s25
	s_cmp_eq_u32 s50, s73
	s_cselect_b32 s28, s69, s26
	s_cselect_b32 s29, s70, s27
	s_cselect_b32 s27, s72, s25
	s_cselect_b32 s26, s71, s24
	s_add_u32 s24, s28, s51
	s_addc_u32 s25, s29, 0
	s_add_u32 s74, s67, s74
	s_addc_u32 s75, s68, s75
	s_add_i32 m0, s44, 0xc000
	ds_read_b128 v[180:183], v157
	ds_read_b128 v[184:187], v157 offset:1024
	ds_read_b128 v[188:191], v157 offset:2048
	ds_read_b128 v[192:195], v157 offset:3072
	ds_read_b128 v[196:199], v157 offset:4096
	ds_read_b128 v[212:215], v157 offset:5120
	ds_read_b128 v[216:219], v157 offset:6144
	ds_read_b128 v[220:223], v157 offset:7168
	global_load_lds_dwordx4 v0, s[74:75]
	s_add_i32 m0, s44, 0xe000
	s_nop 0
	global_load_lds_dwordx4 v130, s[74:75]
	s_waitcnt vmcnt(8)
	s_waitcnt lgkmcnt(0)
	s_barrier
	s_setprio 1
	s_waitcnt lgkmcnt(0)
	v_mfma_f32_16x16x32_bf16 v[126:129], v[132:135], v[180:183], v[126:129]
	v_mfma_f32_16x16x32_bf16 v[122:125], v[140:143], v[180:183], v[122:125]
	v_mfma_f32_16x16x32_bf16 v[110:113], v[132:135], v[188:191], v[110:113]
	v_mfma_f32_16x16x32_bf16 v[106:109], v[140:143], v[188:191], v[106:109]
	v_mfma_f32_16x16x32_bf16 v[94:97], v[132:135], v[196:199], v[94:97]
	v_mfma_f32_16x16x32_bf16 v[90:93], v[140:143], v[196:199], v[90:93]
	v_mfma_f32_16x16x32_bf16 v[78:81], v[132:135], v[216:219], v[78:81]
	v_mfma_f32_16x16x32_bf16 v[74:77], v[140:143], v[216:219], v[74:77]
	v_mfma_f32_16x16x32_bf16 v[126:129], v[136:139], v[184:187], v[126:129]
	v_mfma_f32_16x16x32_bf16 v[122:125], v[144:147], v[184:187], v[122:125]
	v_mfma_f32_16x16x32_bf16 v[110:113], v[136:139], v[192:195], v[110:113]
	v_mfma_f32_16x16x32_bf16 v[106:109], v[144:147], v[192:195], v[106:109]
	v_mfma_f32_16x16x32_bf16 v[94:97], v[136:139], v[212:215], v[94:97]
	v_mfma_f32_16x16x32_bf16 v[90:93], v[144:147], v[212:215], v[90:93]
	v_mfma_f32_16x16x32_bf16 v[78:81], v[136:139], v[220:223], v[78:81]
	v_mfma_f32_16x16x32_bf16 v[74:77], v[144:147], v[220:223], v[74:77]
	s_setprio 0
	s_setprio 1
	v_mfma_f32_16x16x32_bf16 v[118:121], v[148:151], v[180:183], v[118:121]
	v_mfma_f32_16x16x32_bf16 v[114:117], v[172:175], v[180:183], v[114:117]
	v_mfma_f32_16x16x32_bf16 v[102:105], v[148:151], v[188:191], v[102:105]
	v_mfma_f32_16x16x32_bf16 v[98:101], v[172:175], v[188:191], v[98:101]
	v_mfma_f32_16x16x32_bf16 v[86:89], v[148:151], v[196:199], v[86:89]
	v_mfma_f32_16x16x32_bf16 v[82:85], v[172:175], v[196:199], v[82:85]
	v_mfma_f32_16x16x32_bf16 v[70:73], v[148:151], v[216:219], v[70:73]
	v_mfma_f32_16x16x32_bf16 v[66:69], v[172:175], v[216:219], v[66:69]
	v_mfma_f32_16x16x32_bf16 v[118:121], v[158:161], v[184:187], v[118:121]
	v_mfma_f32_16x16x32_bf16 v[114:117], v[176:179], v[184:187], v[114:117]
	v_mfma_f32_16x16x32_bf16 v[102:105], v[158:161], v[192:195], v[102:105]
	v_mfma_f32_16x16x32_bf16 v[98:101], v[176:179], v[192:195], v[98:101]
	v_mfma_f32_16x16x32_bf16 v[86:89], v[158:161], v[212:215], v[86:89]
	v_mfma_f32_16x16x32_bf16 v[82:85], v[176:179], v[212:215], v[82:85]
	v_mfma_f32_16x16x32_bf16 v[70:73], v[158:161], v[220:223], v[70:73]
	s_barrier
	v_mfma_f32_16x16x32_bf16 v[66:69], v[176:179], v[220:223], v[66:69]
	s_setprio 0
	s_mov_b32 m0, s39
	s_add_u32 s74, s26, s37
	ds_read_b128 v[180:183], v157 offset:16384
	ds_read_b128 v[184:187], v157 offset:17408
	ds_read_b128 v[188:191], v157 offset:18432
	ds_read_b128 v[192:195], v157 offset:19456
	ds_read_b128 v[196:199], v157 offset:20480
	ds_read_b128 v[212:215], v157 offset:21504
	ds_read_b128 v[216:219], v157 offset:22528
	ds_read_b128 v[220:223], v157 offset:23552
	global_load_lds_dwordx4 v0, s[26:27]
	s_mov_b32 m0, s40
	s_addc_u32 s75, s27, 0
	global_load_lds_dwordx4 v130, s[26:27]
	s_mov_b32 m0, s42
	s_nop 0
	global_load_lds_dwordx4 v0, s[74:75]
	s_mov_b32 m0, s43
	s_nop 0
	global_load_lds_dwordx4 v130, s[74:75]
	s_mov_b32 m0, s44
	s_nop 0
	global_load_lds_dwordx4 v0, s[28:29]
	s_mov_b32 m0, s45
	s_nop 0
	global_load_lds_dwordx4 v130, s[28:29]
	s_waitcnt vmcnt(8)
	s_waitcnt lgkmcnt(0)
	s_barrier
	s_setprio 1
	s_waitcnt lgkmcnt(0)
	v_mfma_f32_16x16x32_bf16 v[62:65], v[132:135], v[180:183], v[62:65]
	v_mfma_f32_16x16x32_bf16 v[58:61], v[140:143], v[180:183], v[58:61]
	v_mfma_f32_16x16x32_bf16 v[46:49], v[132:135], v[188:191], v[46:49]
	v_mfma_f32_16x16x32_bf16 v[42:45], v[140:143], v[188:191], v[42:45]
	v_mfma_f32_16x16x32_bf16 v[30:33], v[132:135], v[196:199], v[30:33]
	v_mfma_f32_16x16x32_bf16 v[26:29], v[140:143], v[196:199], v[26:29]
	v_mfma_f32_16x16x32_bf16 v[14:17], v[132:135], v[216:219], v[14:17]
	v_mfma_f32_16x16x32_bf16 v[10:13], v[140:143], v[216:219], v[10:13]
	v_mfma_f32_16x16x32_bf16 v[62:65], v[136:139], v[184:187], v[62:65]
	v_mfma_f32_16x16x32_bf16 v[58:61], v[144:147], v[184:187], v[58:61]
	v_mfma_f32_16x16x32_bf16 v[46:49], v[136:139], v[192:195], v[46:49]
	v_mfma_f32_16x16x32_bf16 v[42:45], v[144:147], v[192:195], v[42:45]
	v_mfma_f32_16x16x32_bf16 v[30:33], v[136:139], v[212:215], v[30:33]
	v_mfma_f32_16x16x32_bf16 v[26:29], v[144:147], v[212:215], v[26:29]
	v_mfma_f32_16x16x32_bf16 v[14:17], v[136:139], v[220:223], v[14:17]
	v_mfma_f32_16x16x32_bf16 v[10:13], v[144:147], v[220:223], v[10:13]
	s_setprio 0
	s_setprio 1
	v_mfma_f32_16x16x32_bf16 v[54:57], v[148:151], v[180:183], v[54:57]
	v_mfma_f32_16x16x32_bf16 v[50:53], v[172:175], v[180:183], v[50:53]
	v_mfma_f32_16x16x32_bf16 v[38:41], v[148:151], v[188:191], v[38:41]
	v_mfma_f32_16x16x32_bf16 v[34:37], v[172:175], v[188:191], v[34:37]
	v_mfma_f32_16x16x32_bf16 v[22:25], v[148:151], v[196:199], v[22:25]
	v_mfma_f32_16x16x32_bf16 v[18:21], v[172:175], v[196:199], v[18:21]
	v_mfma_f32_16x16x32_bf16 v[6:9], v[148:151], v[216:219], v[6:9]
	v_mfma_f32_16x16x32_bf16 v[2:5], v[172:175], v[216:219], v[2:5]
	v_mfma_f32_16x16x32_bf16 v[54:57], v[158:161], v[184:187], v[54:57]
	v_mfma_f32_16x16x32_bf16 v[50:53], v[176:179], v[184:187], v[50:53]
	v_mfma_f32_16x16x32_bf16 v[38:41], v[158:161], v[192:195], v[38:41]
	v_mfma_f32_16x16x32_bf16 v[34:37], v[176:179], v[192:195], v[34:37]
	v_mfma_f32_16x16x32_bf16 v[22:25], v[158:161], v[212:215], v[22:25]
	v_mfma_f32_16x16x32_bf16 v[18:21], v[176:179], v[212:215], v[18:21]
	v_mfma_f32_16x16x32_bf16 v[6:9], v[158:161], v[220:223], v[6:9]
	s_barrier
	v_mfma_f32_16x16x32_bf16 v[2:5], v[176:179], v[220:223], v[2:5]
	s_setprio 0
	v_add_u32_e32 v144, s53, v155
	v_add_u32_e32 v152, s58, v155
	ds_read_b128 v[132:135], v144
	ds_read_b128 v[136:139], v144 offset:1024
	ds_read_b128 v[140:143], v144 offset:2048
	ds_read_b128 v[144:147], v144 offset:3072
	ds_read_b128 v[148:151], v152
	ds_read_b128 v[158:161], v152 offset:1024
	ds_read_b128 v[172:175], v152 offset:2048
	ds_read_b128 v[176:179], v152 offset:3072
	s_add_u32 s28, s28, s37
	s_addc_u32 s29, s29, 0
	s_mov_b32 m0, s46
	ds_read_b128 v[180:183], v157 offset:32768
	ds_read_b128 v[184:187], v157 offset:33792
	ds_read_b128 v[188:191], v157 offset:34816
	ds_read_b128 v[192:195], v157 offset:35840
	ds_read_b128 v[196:199], v157 offset:36864
	ds_read_b128 v[212:215], v157 offset:37888
	ds_read_b128 v[216:219], v157 offset:38912
	ds_read_b128 v[220:223], v157 offset:39936
	global_load_lds_dwordx4 v0, s[28:29]
	s_mov_b32 m0, s47
	s_nop 0
	global_load_lds_dwordx4 v130, s[28:29]
	s_waitcnt vmcnt(8)
	s_waitcnt lgkmcnt(0)
	s_barrier
	s_setprio 1
	s_waitcnt lgkmcnt(0)
	v_mfma_f32_16x16x32_bf16 v[126:129], v[132:135], v[180:183], v[126:129]
	v_mfma_f32_16x16x32_bf16 v[122:125], v[140:143], v[180:183], v[122:125]
	v_mfma_f32_16x16x32_bf16 v[110:113], v[132:135], v[188:191], v[110:113]
	v_mfma_f32_16x16x32_bf16 v[106:109], v[140:143], v[188:191], v[106:109]
	v_mfma_f32_16x16x32_bf16 v[94:97], v[132:135], v[196:199], v[94:97]
	v_mfma_f32_16x16x32_bf16 v[90:93], v[140:143], v[196:199], v[90:93]
	v_mfma_f32_16x16x32_bf16 v[78:81], v[132:135], v[216:219], v[78:81]
	v_mfma_f32_16x16x32_bf16 v[74:77], v[140:143], v[216:219], v[74:77]
	v_mfma_f32_16x16x32_bf16 v[126:129], v[136:139], v[184:187], v[126:129]
	v_mfma_f32_16x16x32_bf16 v[122:125], v[144:147], v[184:187], v[122:125]
	v_mfma_f32_16x16x32_bf16 v[110:113], v[136:139], v[192:195], v[110:113]
	v_mfma_f32_16x16x32_bf16 v[106:109], v[144:147], v[192:195], v[106:109]
	v_mfma_f32_16x16x32_bf16 v[94:97], v[136:139], v[212:215], v[94:97]
	v_mfma_f32_16x16x32_bf16 v[90:93], v[144:147], v[212:215], v[90:93]
	v_mfma_f32_16x16x32_bf16 v[78:81], v[136:139], v[220:223], v[78:81]
	v_mfma_f32_16x16x32_bf16 v[74:77], v[144:147], v[220:223], v[74:77]
	s_setprio 0
	s_setprio 1
	v_mfma_f32_16x16x32_bf16 v[118:121], v[148:151], v[180:183], v[118:121]
	v_mfma_f32_16x16x32_bf16 v[114:117], v[172:175], v[180:183], v[114:117]
	v_mfma_f32_16x16x32_bf16 v[102:105], v[148:151], v[188:191], v[102:105]
	v_mfma_f32_16x16x32_bf16 v[98:101], v[172:175], v[188:191], v[98:101]
	v_mfma_f32_16x16x32_bf16 v[86:89], v[148:151], v[196:199], v[86:89]
	v_mfma_f32_16x16x32_bf16 v[82:85], v[172:175], v[196:199], v[82:85]
	v_mfma_f32_16x16x32_bf16 v[70:73], v[148:151], v[216:219], v[70:73]
	v_mfma_f32_16x16x32_bf16 v[66:69], v[172:175], v[216:219], v[66:69]
	v_mfma_f32_16x16x32_bf16 v[118:121], v[158:161], v[184:187], v[118:121]
	v_mfma_f32_16x16x32_bf16 v[114:117], v[176:179], v[184:187], v[114:117]
	v_mfma_f32_16x16x32_bf16 v[102:105], v[158:161], v[192:195], v[102:105]
	v_mfma_f32_16x16x32_bf16 v[98:101], v[176:179], v[192:195], v[98:101]
	v_mfma_f32_16x16x32_bf16 v[86:89], v[158:161], v[212:215], v[86:89]
	v_mfma_f32_16x16x32_bf16 v[82:85], v[176:179], v[212:215], v[82:85]
	v_mfma_f32_16x16x32_bf16 v[70:73], v[158:161], v[220:223], v[70:73]
	s_barrier
	v_mfma_f32_16x16x32_bf16 v[66:69], v[176:179], v[220:223], v[66:69]
	s_setprio 0
	s_add_u32 s26, s26, s51
	s_addc_u32 s27, s27, 0
	s_mov_b32 m0, s54
	ds_read_b128 v[180:183], v157 offset:49152
	ds_read_b128 v[184:187], v157 offset:50176
	ds_read_b128 v[188:191], v157 offset:51200
	ds_read_b128 v[192:195], v157 offset:52224
	ds_read_b128 v[196:199], v157 offset:53248
	ds_read_b128 v[212:215], v157 offset:54272
	ds_read_b128 v[216:219], v157 offset:55296
	ds_read_b128 v[220:223], v157 offset:56320
	global_load_lds_dwordx4 v0, s[26:27]
	v_lshl_add_u64 v[152:153], s[26:27], 0, v[130:131]
	s_add_u32 s26, s26, s37
	s_mov_b32 m0, s55
	s_addc_u32 s27, s27, 0
	global_load_lds_dwordx4 v[152:153], off
	s_mov_b32 m0, s59
	s_nop 0
	global_load_lds_dwordx4 v0, s[26:27]
	s_mov_b32 m0, s60
	s_nop 0
	global_load_lds_dwordx4 v130, s[26:27]
	s_mov_b32 m0, s56
	s_nop 0
	global_load_lds_dwordx4 v0, s[24:25]
	s_mov_b32 m0, s57
	s_nop 0
	global_load_lds_dwordx4 v130, s[24:25]
	s_waitcnt vmcnt(8)
	s_waitcnt lgkmcnt(0)
	s_barrier
	s_setprio 1
	s_waitcnt lgkmcnt(0)
	v_mfma_f32_16x16x32_bf16 v[62:65], v[132:135], v[180:183], v[62:65]
	v_mfma_f32_16x16x32_bf16 v[58:61], v[140:143], v[180:183], v[58:61]
	v_mfma_f32_16x16x32_bf16 v[46:49], v[132:135], v[188:191], v[46:49]
	v_mfma_f32_16x16x32_bf16 v[42:45], v[140:143], v[188:191], v[42:45]
	v_mfma_f32_16x16x32_bf16 v[30:33], v[132:135], v[196:199], v[30:33]
	v_mfma_f32_16x16x32_bf16 v[26:29], v[140:143], v[196:199], v[26:29]
	v_mfma_f32_16x16x32_bf16 v[14:17], v[132:135], v[216:219], v[14:17]
	v_mfma_f32_16x16x32_bf16 v[10:13], v[140:143], v[216:219], v[10:13]
	v_mfma_f32_16x16x32_bf16 v[62:65], v[136:139], v[184:187], v[62:65]
	v_mfma_f32_16x16x32_bf16 v[58:61], v[144:147], v[184:187], v[58:61]
	v_mfma_f32_16x16x32_bf16 v[46:49], v[136:139], v[192:195], v[46:49]
	v_mfma_f32_16x16x32_bf16 v[42:45], v[144:147], v[192:195], v[42:45]
	v_mfma_f32_16x16x32_bf16 v[30:33], v[136:139], v[212:215], v[30:33]
	v_mfma_f32_16x16x32_bf16 v[26:29], v[144:147], v[212:215], v[26:29]
	v_mfma_f32_16x16x32_bf16 v[14:17], v[136:139], v[220:223], v[14:17]
	v_mfma_f32_16x16x32_bf16 v[10:13], v[144:147], v[220:223], v[10:13]
	s_setprio 0
	s_setprio 1
	v_mfma_f32_16x16x32_bf16 v[54:57], v[148:151], v[180:183], v[54:57]
	v_mfma_f32_16x16x32_bf16 v[50:53], v[172:175], v[180:183], v[50:53]
	v_mfma_f32_16x16x32_bf16 v[38:41], v[148:151], v[188:191], v[38:41]
	v_mfma_f32_16x16x32_bf16 v[34:37], v[172:175], v[188:191], v[34:37]
	v_mfma_f32_16x16x32_bf16 v[22:25], v[148:151], v[196:199], v[22:25]
	v_mfma_f32_16x16x32_bf16 v[18:21], v[172:175], v[196:199], v[18:21]
	v_mfma_f32_16x16x32_bf16 v[6:9], v[148:151], v[216:219], v[6:9]
	v_mfma_f32_16x16x32_bf16 v[2:5], v[172:175], v[216:219], v[2:5]
	v_mfma_f32_16x16x32_bf16 v[54:57], v[158:161], v[184:187], v[54:57]
	v_mfma_f32_16x16x32_bf16 v[50:53], v[176:179], v[184:187], v[50:53]
	v_mfma_f32_16x16x32_bf16 v[38:41], v[158:161], v[192:195], v[38:41]
	v_mfma_f32_16x16x32_bf16 v[34:37], v[176:179], v[192:195], v[34:37]
	v_mfma_f32_16x16x32_bf16 v[22:25], v[158:161], v[212:215], v[22:25]
	v_mfma_f32_16x16x32_bf16 v[18:21], v[176:179], v[212:215], v[18:21]
	v_mfma_f32_16x16x32_bf16 v[6:9], v[158:161], v[220:223], v[6:9]
	s_barrier
	v_mfma_f32_16x16x32_bf16 v[2:5], v[176:179], v[220:223], v[2:5]
	s_setprio 0
	s_add_i32 s73, s73, 2
	s_cmp_ge_i32 s73, s49
	s_cbranch_scc0 .LBB0_2886
